# v26 + nt on P1's u stores and P6's x1/u2 stores (row-contiguous dword/dwordx2)
# speedup vs baseline: 1.0003x; 1.0003x over previous
; __device__ __forceinline__ void p1_ln_mod(Frame& F) {
;     ...
;     for (int m = gw; m < MTOT; m += NGW) {
;         const int b = m / RPB, idx = m % RPB; const float* src; const float* md;
;         if (idx < SEQ) { src = F.in[I_X] + (size_t)(b * SEQ + idx) * DM; md = mod + (size_t)b * 12288; } else { src = F.in[I_CTX] + (size_t)(b * CTXL + idx - SEQ) * DM; md = mod + 2 * 12288; }
;         const f32x4* xr = (const f32x4*)src + F.lane; f32x4 v[8]; float s = 0.f;
; #pragma unroll
;         for (int j = 0; j < 8; ++j) { v[j] = xr[64 * j]; s += (v[j][0] + v[j][1]) + (v[j][2] + v[j][3]); }
;         const float mean = wave_sum(s) * (1.f / DM); float s2 = 0.f;
; #pragma unroll
;         for (int j = 0; j < 8; ++j) { v[j] = v[j] - mean; s2 += (v[j][0] * v[j][0] + v[j][1] * v[j][1]) + (v[j][2] * v[j][2] + v[j][3] * v[j][3]); }
;         const float rstd = 1.f / sqrtf(wave_sum(s2) * (1.f / DM) + LN_EPS);
.LBB0_189:
	global_load_dwordx4 v[30:33], v34, s[0:1] nt
	global_load_dwordx4 v[26:29], v34, s[0:1] offset:1024 nt
	global_load_dwordx4 v[22:25], v34, s[0:1] offset:2048 nt
	global_load_dwordx4 v[18:21], v34, s[0:1] offset:3072 nt
	v_lshl_add_u64 v[2:3], s[0:1], 0, v[34:35]
	v_add_co_u32_e32 v2, vcc, s42, v2
	s_ashr_i32 s13, s12, 31
	s_nop 0
	v_addc_co_u32_e32 v3, vcc, 0, v3, vcc
	global_load_dwordx4 v[14:17], v[2:3], off nt
	global_load_dwordx4 v[10:13], v[2:3], off offset:1024 nt
	global_load_dwordx4 v[6:9], v[2:3], off offset:2048 nt
	s_nop 0
	global_load_dwordx4 v[2:5], v[2:3], off offset:3072 nt
	s_lshl_b64 s[38:39], s[12:13], 11
	s_lshl_b64 s[0:1], s[12:13], 12
	s_add_u32 s24, s20, 0x2000
	s_addc_u32 s25, s21, 0
	s_add_i32 s12, s12, s3
	s_cmpk_lt_i32 s12, 0x2200
	s_waitcnt vmcnt(7)
	v_mov_b32_e32 v56, v30
	s_waitcnt vmcnt(6)
	v_mov_b32_e32 v57, v26
	v_mov_b32_e32 v58, v31
	v_mov_b32_e32 v59, v27
	v_mov_b32_e32 v60, v32
	v_mov_b32_e32 v61, v28
	v_mov_b32_e32 v62, v33
	v_mov_b32_e32 v63, v29
	s_waitcnt vmcnt(5)
	v_mov_b32_e32 v64, v23
	v_mov_b32_e32 v65, v24
	v_mov_b32_e32 v66, v22
	v_mov_b32_e32 v67, v25
	v_pk_add_f32 v[56:57], v[56:57], v[58:59]
	v_pk_add_f32 v[58:59], v[60:61], v[62:63]
	v_pk_add_f32 v[60:61], v[64:65], v[66:67]
	v_pk_add_f32 v[56:57], v[56:57], v[58:59]
	v_pk_add_f32 v[58:59], v[60:61], v[60:61] op_sel:[0,1] op_sel_hi:[1,0]
	v_add_f32_e32 v56, 0, v56
	s_waitcnt vmcnt(4)
	v_add_f32_e32 v68, v18, v19
	v_add_f32_e32 v70, v20, v21
	s_waitcnt vmcnt(3)
	v_mov_b32_e32 v61, v14
	v_mov_b32_e32 v69, v16
	v_mov_b32_e32 v71, v17
	v_mov_b32_e32 v59, v15
	v_add_f32_e32 v60, v56, v57
	s_waitcnt vmcnt(2)
	v_mov_b32_e32 v62, v11
	v_mov_b32_e32 v63, v12
	v_mov_b32_e32 v64, v10
	v_mov_b32_e32 v65, v13
	v_pk_add_f32 v[68:69], v[68:69], v[70:71]
	v_pk_add_f32 v[58:59], v[60:61], v[58:59]
	v_pk_add_f32 v[62:63], v[62:63], v[64:65]
	v_pk_add_f32 v[58:59], v[58:59], v[68:69]
	v_pk_add_f32 v[56:57], v[62:63], v[62:63] op_sel:[0,1] op_sel_hi:[1,0]
	v_pk_add_f32 v[58:59], v[58:59], v[58:59] op_sel:[0,1] op_sel_hi:[1,0]
	s_waitcnt vmcnt(1)
	v_add_f32_e32 v66, v6, v7
	v_add_f32_e32 v72, v8, v9
	s_waitcnt vmcnt(0)
	v_mov_b32_e32 v67, v4
	v_mov_b32_e32 v73, v5
	v_mov_b32_e32 v57, v3
	v_mov_b32_e32 v59, v2
	v_pk_add_f32 v[64:65], v[66:67], v[72:73]
	v_pk_add_f32 v[56:57], v[58:59], v[56:57]
	s_nop 0
	v_pk_add_f32 v[56:57], v[56:57], v[64:65]
	s_nop 0
	v_add_f32_e32 v56, v56, v57
	ds_bpermute_b32 v57, v1, v56
	s_waitcnt lgkmcnt(0)
	v_add_f32_e32 v56, v56, v57
	ds_bpermute_b32 v57, v42, v56
	s_waitcnt lgkmcnt(0)
	v_add_f32_e32 v56, v56, v57
	ds_bpermute_b32 v57, v43, v56
	s_waitcnt lgkmcnt(0)
	v_add_f32_e32 v56, v56, v57
	ds_bpermute_b32 v57, v44, v56
	s_waitcnt lgkmcnt(0)
	v_add_f32_e32 v56, v56, v57
	ds_bpermute_b32 v57, v45, v56
	s_waitcnt lgkmcnt(0)
	v_add_f32_e32 v56, v56, v57
	ds_bpermute_b32 v57, v46, v56
	s_waitcnt lgkmcnt(0)
	v_add_f32_e32 v78, v56, v57
	v_fmamk_f32 v33, v78, 0xba000000, v33
	v_fmamk_f32 v31, v78, 0xba000000, v31
	v_fmamk_f32 v65, v78, 0xba000000, v29
	v_fmamk_f32 v27, v78, 0xba000000, v27
	v_fmamk_f32 v67, v78, 0xba000000, v23
	v_fmamk_f32 v66, v78, 0xba000000, v22
	v_fmamk_f32 v25, v78, 0xba000000, v25
	v_fmac_f32_e32 v24, 0xba000000, v78
	v_fmamk_f32 v68, v78, 0xba000000, v18
	v_fmac_f32_e32 v20, 0xba000000, v78
	v_fmamk_f32 v11, v78, 0xba000000, v11
	v_fmamk_f32 v10, v78, 0xba000000, v10
	v_fmamk_f32 v13, v78, 0xba000000, v13
	v_fmac_f32_e32 v12, 0xba000000, v78
	v_fmamk_f32 v32, v78, 0xba000000, v32
	v_fmac_f32_e32 v30, 0xba000000, v78
	v_fmamk_f32 v64, v78, 0xba000000, v28
	v_fmac_f32_e32 v26, 0xba000000, v78
	v_fmamk_f32 v69, v78, 0xba000000, v19
	v_fmamk_f32 v21, v78, 0xba000000, v21
	v_mov_b32_e32 v22, v31
	v_mov_b32_e32 v23, v27
	v_mov_b32_e32 v56, v33
	v_mov_b32_e32 v57, v65
	v_pk_mul_f32 v[58:59], v[24:25], v[24:25]
	v_pk_mul_f32 v[60:61], v[66:67], v[66:67]
	v_mul_f32_e32 v62, v68, v68
	v_mul_f32_e32 v70, v20, v20
	v_pk_mul_f32 v[72:73], v[12:13], v[12:13]
	v_pk_mul_f32 v[74:75], v[10:11], v[10:11]
	v_fmamk_f32 v19, v78, 0xba000000, v17
	v_fmamk_f32 v18, v78, 0xba000000, v16
	v_fmamk_f32 v15, v78, 0xba000000, v15
	v_fmac_f32_e32 v14, 0xba000000, v78
	v_mov_b32_e32 v16, v30
	v_mov_b32_e32 v17, v26
	v_mov_b32_e32 v28, v32
	v_mov_b32_e32 v29, v64
	v_pk_mul_f32 v[22:23], v[22:23], v[22:23]
	v_pk_mul_f32 v[56:57], v[56:57], v[56:57]
	v_pk_mov_b32 v[76:77], v[60:61], v[58:59] op_sel:[1,0]
	v_mov_b32_e32 v61, v59
	v_pk_fma_f32 v[58:59], v[68:69], v[68:69], v[62:63] op_sel_hi:[1,1,0]
	v_pk_fma_f32 v[62:63], v[20:21], v[20:21], v[70:71] op_sel_hi:[1,1,0]
	v_pk_mov_b32 v[70:71], v[74:75], v[72:73] op_sel:[1,0]
	v_mov_b32_e32 v75, v73
	v_pk_fma_f32 v[16:17], v[16:17], v[16:17], v[22:23]
	v_pk_fma_f32 v[22:23], v[28:29], v[28:29], v[56:57]
	v_pk_add_f32 v[28:29], v[76:77], v[60:61]
	v_mul_f32_e32 v58, v14, v14
	v_mul_f32_e32 v62, v15, v15
	v_pk_add_f32 v[56:57], v[70:71], v[74:75]
	v_pk_add_f32 v[16:17], v[16:17], v[22:23]
	v_pk_add_f32 v[22:23], v[28:29], v[28:29] op_sel_hi:[0,1]
	v_pk_add_f32 v[28:29], v[58:59], v[62:63]
	v_pk_add_f32 v[70:71], v[56:57], v[56:57] op_sel_hi:[0,1]
	global_load_dwordx4 v[56:59], v34, s[20:21]
	global_load_dwordx4 v[60:63], v34, s[24:25]
	v_pk_add_f32 v[16:17], v[16:17], v[16:17] op_sel_hi:[0,1]
	v_mul_f32_e32 v22, v18, v18
	v_mul_f32_e32 v16, v19, v19
	v_pk_add_f32 v[16:17], v[22:23], v[16:17]
	v_fmac_f32_e32 v8, 0xba000000, v78
	v_pk_add_f32 v[16:17], v[28:29], v[16:17]
	v_fmamk_f32 v9, v78, 0xba000000, v9
	v_pk_add_f32 v[22:23], v[16:17], v[16:17] op_sel_hi:[0,1]
	v_fmamk_f32 v16, v78, 0xba000000, v6
	v_fmamk_f32 v17, v78, 0xba000000, v7
	v_mul_f32_e32 v6, v16, v16
	v_pk_fma_f32 v[6:7], v[16:17], v[16:17], v[6:7] op_sel_hi:[1,1,0]
	v_fmamk_f32 v5, v78, 0xba000000, v5
	v_mul_f32_e32 v6, v8, v8
	v_pk_fma_f32 v[28:29], v[8:9], v[8:9], v[6:7] op_sel_hi:[1,1,0]
	v_fmamk_f32 v4, v78, 0xba000000, v4
	v_fmamk_f32 v3, v78, 0xba000000, v3
	v_fmac_f32_e32 v2, 0xba000000, v78
	v_mul_f32_e32 v6, v2, v2
	v_mul_f32_e32 v28, v3, v3
	v_mul_f32_e32 v70, v4, v4
	v_mul_f32_e32 v22, v5, v5
	v_pk_add_f32 v[6:7], v[6:7], v[28:29]
	v_pk_add_f32 v[22:23], v[70:71], v[22:23]
	s_nop 0
	v_pk_add_f32 v[6:7], v[6:7], v[22:23]
	s_nop 0
	v_add_f32_e32 v6, v6, v7
	ds_bpermute_b32 v7, v1, v6
	s_waitcnt lgkmcnt(0)
; __device__ __forceinline__ unsigned cvt_pk_bf16(float lo, float hi) { unsigned r; asm volatile("v_cvt_pk_bf16_f32 %0, %1, %2" : "=v"(r) : "v"(lo), "v"(hi)); return r; }
; __device__ __forceinline__ unsigned pk4_fp8(float a, float b, float c, float d) { int w = 0; w = __builtin_amdgcn_cvt_pk_fp8_f32(a, b, w, false); w = __builtin_amdgcn_cvt_pk_fp8_f32(c, d, w, true); return (unsigned)w; }
; __device__ __forceinline__ void p1_ln_mod(Frame& F) {
;     ...
;         const float rstd = 1.f / sqrtf(wave_sum(s2) * (1.f / DM) + LN_EPS);
;         u32x2* o8 = (u32x2*)((bf16_t*)(F.ws + WS_U) + (size_t)m * DM) + F.lane;
; #pragma unroll
;         for (int j = 0; j < 8; ++j) { const f32x4 sh = ((const f32x4*)md)[F.lane + 64 * j], sc = ((const f32x4*)(md + 2048))[F.lane + 64 * j];
;             const f32x4 y = v[j] * rstd * (sc + 1.0f) + sh; u32x2 w; w.x = cvt_pk_bf16(y[0], y[1]); w.y = cvt_pk_bf16(y[2], y[3]); o8[64 * j] = w;
;             ((unsigned*)(F.ws + WS_UF8 + (size_t)m * DM))[F.lane + 64 * j] = pk4_fp8(y[0], y[1], y[2], y[3]); }
	v_add_f32_e32 v6, v6, v7
	ds_bpermute_b32 v7, v42, v6
	s_waitcnt lgkmcnt(0)
	v_add_f32_e32 v6, v6, v7
	ds_bpermute_b32 v7, v43, v6
	s_waitcnt lgkmcnt(0)
	v_add_f32_e32 v6, v6, v7
	ds_bpermute_b32 v7, v44, v6
	s_waitcnt lgkmcnt(0)
	v_add_f32_e32 v6, v6, v7
	ds_bpermute_b32 v7, v45, v6
	s_waitcnt lgkmcnt(0)
	v_add_f32_e32 v6, v6, v7
	ds_bpermute_b32 v7, v46, v6
	s_waitcnt lgkmcnt(0)
	v_add_f32_e32 v6, v6, v7
	v_fmamk_f32 v6, v6, 0x3a000000, v47
	v_mul_f32_e32 v7, 0x4f800000, v6
	v_cmp_gt_f32_e32 vcc, s43, v6
	s_nop 1
	v_cndmask_b32_e32 v22, v6, v7, vcc
	v_sqrt_f32_e32 v23, v22
	v_lshl_add_u64 v[6:7], v[36:37], 0, s[0:1]
	v_add_u32_e32 v28, -1, v23
	v_add_u32_e32 v29, 1, v23
	v_fma_f32 v70, -v28, v23, v22
	v_fma_f32 v71, -v29, v23, v22
	v_cmp_ge_f32_e64 s[0:1], 0, v70
	s_nop 1
	v_cndmask_b32_e64 v23, v23, v28, s[0:1]
	v_cmp_lt_f32_e64 s[0:1], 0, v71
	s_nop 1
	v_cndmask_b32_e64 v23, v23, v29, s[0:1]
	v_mul_f32_e32 v28, 0x37800000, v23
	v_cndmask_b32_e32 v23, v23, v28, vcc
	v_cmp_class_f32_e32 vcc, v22, v48
	s_waitcnt vmcnt(0)
	v_pk_add_f32 v[28:29], v[60:61], 1.0 op_sel_hi:[1,0]
	v_cndmask_b32_e32 v22, v23, v22, vcc
	v_div_scale_f32 v23, s[0:1], v22, v22, 1.0
	v_rcp_f32_e32 v70, v23
	v_div_scale_f32 v60, vcc, 1.0, v22, 1.0
	v_fma_f32 v61, -v23, v70, 1.0
	v_fmac_f32_e32 v70, v61, v70
	v_mul_f32_e32 v61, v60, v70
	v_fma_f32 v71, -v23, v61, v60
	v_fmac_f32_e32 v61, v71, v70
	v_fma_f32 v23, -v23, v61, v60
	v_div_fmas_f32 v23, v23, v70, v61
	v_div_fixup_f32 v22, v23, v22, 1.0
	v_pk_mul_f32 v[30:31], v[30:31], v[22:23] op_sel_hi:[1,0]
	v_pk_mul_f32 v[32:33], v[32:33], v[22:23] op_sel_hi:[1,0]
	v_pk_fma_f32 v[28:29], v[28:29], v[30:31], v[56:57]
	v_mov_b32_e32 v23, 0
	v_cvt_pk_fp8_f32 v23, v28, v29
	v_pk_add_f32 v[30:31], v[62:63], 1.0 op_sel_hi:[1,0]
	v_cvt_pk_bf16_f32 v28, v28, v29
	s_nop 0
	v_pk_fma_f32 v[30:31], v[30:31], v[32:33], v[58:59]
	v_lshl_add_u64 v[32:33], v[38:39], 0, s[38:39]
	v_cvt_pk_fp8_f32 v23, v30, v31 op_sel:[0,0,1]
	v_cvt_pk_bf16_f32 v29, v30, v31
	global_store_dwordx2 v[6:7], v[28:29], off nt
	v_lshl_add_u64 v[28:29], v[40:41], 0, s[38:39]
	global_store_dword v[28:29], v23, off nt
	global_load_dwordx4 v[28:31], v49, s[24:25]
	s_nop 0
	global_load_dwordx4 v[56:59], v34, s[20:21] offset:1024
	v_mov_b32_e32 v23, 0
	v_pk_mul_f32 v[26:27], v[26:27], v[22:23] op_sel_hi:[1,0]
	v_add_co_u32_e32 v60, vcc, s44, v32
	s_waitcnt vmcnt(1)
	v_pk_add_f32 v[28:29], v[28:29], 1.0 op_sel_hi:[1,0]
	s_waitcnt vmcnt(0)
	v_pk_fma_f32 v[26:27], v[28:29], v[26:27], v[56:57]
	v_pk_add_f32 v[30:31], v[30:31], 1.0 op_sel_hi:[1,0]
	v_cvt_pk_fp8_f32 v23, v26, v27
	v_cvt_pk_bf16_f32 v26, v26, v27
	v_addc_co_u32_e32 v61, vcc, 0, v33, vcc
	v_pk_mul_f32 v[28:29], v[64:65], v[22:23] op_sel_hi:[1,0]
	s_nop 0
	v_pk_fma_f32 v[28:29], v[30:31], v[28:29], v[58:59]
	s_nop 0
	v_cvt_pk_fp8_f32 v23, v28, v29 op_sel:[0,0,1]
	v_cvt_pk_bf16_f32 v27, v28, v29
	global_store_dwordx2 v[6:7], v[26:27], off offset:512 nt
	global_store_dword v[60:61], v23, off offset:256 nt
	global_load_dwordx4 v[26:29], v50, s[24:25]
	s_nop 0
	global_load_dwordx4 v[30:33], v34, s[20:21] offset:2048
	v_mov_b32_e32 v23, 0
	v_pk_mul_f32 v[56:57], v[66:67], v[22:23] op_sel_hi:[1,0]
	s_waitcnt vmcnt(1)
	v_pk_add_f32 v[26:27], v[26:27], 1.0 op_sel_hi:[1,0]
	s_waitcnt vmcnt(0)
	v_pk_fma_f32 v[26:27], v[56:57], v[26:27], v[30:31]
	v_pk_add_f32 v[28:29], v[28:29], 1.0 op_sel_hi:[1,0]
	v_cvt_pk_fp8_f32 v23, v26, v27
	v_cvt_pk_bf16_f32 v26, v26, v27
	v_pk_mul_f32 v[24:25], v[24:25], v[22:23] op_sel_hi:[1,0]
	s_nop 0
	v_pk_fma_f32 v[24:25], v[24:25], v[28:29], v[32:33]
	s_nop 0
	v_cvt_pk_fp8_f32 v23, v24, v25 op_sel:[0,0,1]
	v_cvt_pk_bf16_f32 v27, v24, v25
	global_store_dwordx2 v[6:7], v[26:27], off offset:1024 nt
	global_store_dword v[60:61], v23, off offset:512 nt
	global_load_dwordx4 v[24:27], v51, s[24:25]
	s_nop 0
	global_load_dwordx4 v[28:31], v34, s[20:21] offset:3072
	v_mov_b32_e32 v23, 0
	v_pk_mul_f32 v[32:33], v[68:69], v[22:23] op_sel_hi:[1,0]
	s_waitcnt vmcnt(1)
; __device__ __forceinline__ unsigned cvt_pk_bf16(float lo, float hi) { unsigned r; asm volatile("v_cvt_pk_bf16_f32 %0, %1, %2" : "=v"(r) : "v"(lo), "v"(hi)); return r; }
; __device__ __forceinline__ unsigned pk4_fp8(float a, float b, float c, float d) { int w = 0; w = __builtin_amdgcn_cvt_pk_fp8_f32(a, b, w, false); w = __builtin_amdgcn_cvt_pk_fp8_f32(c, d, w, true); return (unsigned)w; }
; __device__ __forceinline__ void p1_ln_mod(Frame& F) {
;     ...
;     for (int m = gw; m < MTOT; m += NGW) {
;     ...
;         for (int j = 0; j < 8; ++j) { const f32x4 sh = ((const f32x4*)md)[F.lane + 64 * j], sc = ((const f32x4*)(md + 2048))[F.lane + 64 * j];
;             const f32x4 y = v[j] * rstd * (sc + 1.0f) + sh; u32x2 w; w.x = cvt_pk_bf16(y[0], y[1]); w.y = cvt_pk_bf16(y[2], y[3]); o8[64 * j] = w;
;             ((unsigned*)(F.ws + WS_UF8 + (size_t)m * DM))[F.lane + 64 * j] = pk4_fp8(y[0], y[1], y[2], y[3]); }
	v_pk_add_f32 v[24:25], v[24:25], 1.0 op_sel_hi:[1,0]
	s_waitcnt vmcnt(0)
	v_pk_fma_f32 v[24:25], v[32:33], v[24:25], v[28:29]
	v_pk_add_f32 v[26:27], v[26:27], 1.0 op_sel_hi:[1,0]
	v_cvt_pk_fp8_f32 v23, v24, v25
	v_cvt_pk_bf16_f32 v24, v24, v25
	v_pk_mul_f32 v[20:21], v[20:21], v[22:23] op_sel_hi:[1,0]
	s_nop 0
	v_pk_fma_f32 v[20:21], v[20:21], v[26:27], v[30:31]
	s_nop 0
	v_cvt_pk_fp8_f32 v23, v20, v21 op_sel:[0,0,1]
	v_cvt_pk_bf16_f32 v25, v20, v21
	global_store_dwordx2 v[6:7], v[24:25], off offset:1536 nt
	global_store_dword v[60:61], v23, off offset:768 nt
	global_load_dwordx4 v[24:27], v52, s[24:25]
	s_nop 0
	global_load_dwordx4 v[28:31], v52, s[20:21]
	v_mov_b32_e32 v23, 0
	v_pk_mul_f32 v[14:15], v[14:15], v[22:23] op_sel_hi:[1,0]
	s_waitcnt vmcnt(1)
	v_pk_add_f32 v[20:21], v[24:25], 1.0 op_sel_hi:[1,0]
	s_waitcnt vmcnt(0)
	v_pk_fma_f32 v[14:15], v[14:15], v[20:21], v[28:29]
	v_pk_add_f32 v[20:21], v[26:27], 1.0 op_sel_hi:[1,0]
	v_cvt_pk_fp8_f32 v23, v14, v15
	v_cvt_pk_bf16_f32 v14, v14, v15
	v_pk_mul_f32 v[18:19], v[18:19], v[22:23] op_sel_hi:[1,0]
	s_nop 0
	v_pk_fma_f32 v[18:19], v[18:19], v[20:21], v[30:31]
	s_nop 0
	v_cvt_pk_fp8_f32 v23, v18, v19 op_sel:[0,0,1]
	v_cvt_pk_bf16_f32 v15, v18, v19
	global_store_dwordx2 v[6:7], v[14:15], off offset:2048 nt
	global_store_dword v[60:61], v23, off offset:1024 nt
	global_load_dwordx4 v[18:21], v53, s[24:25]
	global_load_dwordx4 v[24:27], v53, s[20:21]
	v_mov_b32_e32 v23, 0
	v_pk_mul_f32 v[10:11], v[10:11], v[22:23] op_sel_hi:[1,0]
	s_waitcnt vmcnt(1)
	v_pk_add_f32 v[14:15], v[18:19], 1.0 op_sel_hi:[1,0]
	s_waitcnt vmcnt(0)
	v_pk_fma_f32 v[10:11], v[10:11], v[14:15], v[24:25]
	v_pk_add_f32 v[14:15], v[20:21], 1.0 op_sel_hi:[1,0]
	v_cvt_pk_fp8_f32 v23, v10, v11
	v_cvt_pk_bf16_f32 v10, v10, v11
	v_pk_mul_f32 v[12:13], v[12:13], v[22:23] op_sel_hi:[1,0]
	s_nop 0
	v_pk_fma_f32 v[12:13], v[12:13], v[14:15], v[26:27]
	s_nop 0
	v_cvt_pk_fp8_f32 v23, v12, v13 op_sel:[0,0,1]
	v_cvt_pk_bf16_f32 v11, v12, v13
	global_store_dwordx2 v[6:7], v[10:11], off offset:2560 nt
	global_store_dword v[60:61], v23, off offset:1280 nt
	global_load_dwordx4 v[10:13], v54, s[24:25]
	s_nop 0
	global_load_dwordx4 v[18:21], v54, s[20:21]
	v_mov_b32_e32 v23, 0
	v_pk_mul_f32 v[14:15], v[16:17], v[22:23] op_sel_hi:[1,0]
	s_waitcnt vmcnt(1)
	v_pk_add_f32 v[10:11], v[10:11], 1.0 op_sel_hi:[1,0]
	s_waitcnt vmcnt(0)
	v_pk_fma_f32 v[10:11], v[14:15], v[10:11], v[18:19]
	v_pk_add_f32 v[12:13], v[12:13], 1.0 op_sel_hi:[1,0]
	v_cvt_pk_fp8_f32 v23, v10, v11
	v_cvt_pk_bf16_f32 v10, v10, v11
	v_pk_mul_f32 v[8:9], v[8:9], v[22:23] op_sel_hi:[1,0]
	s_nop 0
	v_pk_fma_f32 v[8:9], v[8:9], v[12:13], v[20:21]
	s_nop 0
	v_cvt_pk_fp8_f32 v23, v8, v9 op_sel:[0,0,1]
	v_cvt_pk_bf16_f32 v11, v8, v9
	global_store_dwordx2 v[6:7], v[10:11], off offset:3072 nt
	global_store_dword v[60:61], v23, off offset:1536 nt
	global_load_dwordx4 v[8:11], v55, s[24:25]
	s_nop 0
	global_load_dwordx4 v[12:15], v55, s[20:21]
	v_pk_mul_f32 v[2:3], v[2:3], v[22:23] op_sel_hi:[1,0]
	v_pk_mul_f32 v[4:5], v[4:5], v[22:23] op_sel_hi:[1,0]
	s_waitcnt vmcnt(1)
	v_pk_add_f32 v[8:9], v[8:9], 1.0 op_sel_hi:[1,0]
	s_waitcnt vmcnt(0)
	v_pk_fma_f32 v[2:3], v[2:3], v[8:9], v[12:13]
	v_mov_b32_e32 v8, 0
	v_cvt_pk_fp8_f32 v8, v2, v3
	v_pk_add_f32 v[10:11], v[10:11], 1.0 op_sel_hi:[1,0]
	v_cvt_pk_bf16_f32 v2, v2, v3
	s_nop 0
	v_pk_fma_f32 v[4:5], v[4:5], v[10:11], v[14:15]
	s_nop 0
	v_cvt_pk_fp8_f32 v8, v4, v5 op_sel:[0,0,1]
	v_cvt_pk_bf16_f32 v3, v4, v5
	global_store_dwordx2 v[6:7], v[2:3], off offset:3584 nt
	global_store_dword v[60:61], v8, off offset:1792 nt
	s_cbranch_scc0 .LBB0_194

; __device__ __forceinline__ float bf_lo(unsigned w) { return __uint_as_float(w << 16); }
; __device__ __forceinline__ float bf_hi(unsigned w) { return __uint_as_float(w & 0xffff0000u); }
; __device__ __forceinline__ void p6_router(Frame& F) {
;     const int t0 = blockIdx.x * 32; if (t0 >= NTOK) return;
;     const float* mod = (const float*)(F.ws + WS_MOD);
;     const int b = t0 >> 12, lane = F.lane, wave = F.wave, tid = F.tid;
;     const bf16_t* ZB = (const bf16_t*)(F.ws + WS_Z); bf16_t* X1 = (bf16_t*)(F.ws + WS_X1);
;     unsigned* U2F = (unsigned*)(F.ws + WS_U2F);
;     const bf16_t* WRH = (const bf16_t*)(F.ws + WS_WRT); const bf16_t* WRL = WRH + 65536;
;     const int fr = lane & 15, fq = lane >> 4;
;     f32x4 acc[2][2];
;     {
;         u32x2 zr[2][8];
; #pragma unroll
;         for (int q = 0; q < 2; ++q)
; #pragma unroll
;             for (int j = 0; j < 8; ++j) zr[q][j] = ((const u32x2*)(ZB + (size_t)(t0 + wave * 4 + q) * DM))[lane + 64 * j];
;         auto pass = [&](const int rp, f32x4 (&accp)[2]) __attribute__((always_inline)) {
;             const int ta = t0 + wave * 4 + 2 * rp;
;             f32x4 pw[8], pb[8];
;             int lop = lane; asm volatile("" : "+v"(lop));
; #pragma unroll
;             for (int j = 0; j < 8; ++j) { pw[j] = ((const f32x4*)F.in[I_LN1W])[lop + 64 * j]; pb[j] = ((const f32x4*)F.in[I_LN1B])[lop + 64 * j]; }
; #pragma unroll
;             for (int q = 0; q < 2; ++q) {
;                 const int t = ta + q; f32x4 v[8]; float s = 0.f;
; #pragma unroll
;                 for (int j = 0; j < 8; ++j) { const u32x2 zb = zr[q][j]; v[j] = (f32x4){bf_lo(zb.x), bf_hi(zb.x), bf_lo(zb.y), bf_hi(zb.y)}; s += (v[j][0] + v[j][1]) + (v[j][2] + v[j][3]); }
;                 float mean = wave_sum(s) * (1.f / DM), s2 = 0.f;
.LBB0_756:
	s_cmp_lt_i32 s34, 7
	s_cselect_b64 s[12:13], -1, 0
	s_and_b64 s[0:1], s[12:13], s[0:1]
	s_andn2_b64 vcc, exec, s[0:1]
	s_cbranch_vccnz .LBB0_931
	s_lshl_b32 s3, s2, 5
	s_cmpk_gt_i32 s3, 0x1fff
	s_cbranch_scc1 .LBB0_931
	s_add_u32 s6, s82, 0x4a600000
	s_addc_u32 s7, s83, 0
	s_add_u32 s42, s82, 0x4e600000
	v_readlane_b32 s46, v255, 8
	s_addc_u32 s43, s83, 0
	s_lshl_b32 s0, s46, 2
	s_add_i32 s4, s0, s3
	s_ashr_i32 s5, s4, 31
	s_lshl_b64 s[16:17], s[4:5], 12
	s_add_u32 s0, s6, s16
	s_addc_u32 s1, s7, s17
	v_lshlrev_b32_e32 v146, 3, v170
	global_load_dwordx2 v[2:3], v146, s[0:1] offset:512
	global_load_dwordx2 v[4:5], v146, s[0:1]
	global_load_dwordx2 v[6:7], v146, s[0:1] offset:1024
	global_load_dwordx2 v[8:9], v146, s[0:1] offset:1536
	global_load_dwordx2 v[10:11], v146, s[0:1] offset:2048
	global_load_dwordx2 v[12:13], v146, s[0:1] offset:2560
	global_load_dwordx2 v[14:15], v146, s[0:1] offset:3072
	global_load_dwordx2 v[16:17], v146, s[0:1] offset:3584
	v_mbcnt_lo_u32_b32 v1, -1, 0
	v_mbcnt_hi_u32_b32 v19, -1, v1
	v_and_b32_e32 v1, 64, v19
	v_xor_b32_e32 v20, 1, v19
	v_add_u32_e32 v26, 64, v1
	v_cmp_lt_i32_e32 vcc, v20, v26
	v_xor_b32_e32 v21, 2, v19
	v_xor_b32_e32 v22, 4, v19
	v_cndmask_b32_e32 v1, v19, v20, vcc
	v_lshlrev_b32_e32 v1, 2, v1
	v_cmp_lt_i32_e32 vcc, v21, v26
	v_xor_b32_e32 v23, 8, v19
	v_xor_b32_e32 v24, 16, v19
	v_cndmask_b32_e32 v20, v19, v21, vcc
	v_lshlrev_b32_e32 v142, 2, v20
	v_cmp_lt_i32_e32 vcc, v22, v26
	v_xor_b32_e32 v25, 32, v19
	s_or_b32 s24, s4, 1
	v_cndmask_b32_e32 v21, v19, v22, vcc
	v_lshlrev_b32_e32 v143, 2, v21
	v_cmp_lt_i32_e32 vcc, v23, v26
	s_ashr_i32 s25, s24, 31
	s_lshl_b64 s[36:37], s[24:25], 12
	v_cndmask_b32_e32 v22, v19, v23, vcc
	v_lshlrev_b32_e32 v144, 2, v22
	v_cmp_lt_i32_e32 vcc, v24, v26
	s_add_u32 s0, s6, s36
	v_mov_b32_e32 v18, v170
	v_cndmask_b32_e32 v23, v19, v24, vcc
	v_lshlrev_b32_e32 v145, 2, v23
	v_cmp_lt_i32_e32 vcc, v25, v26
	s_addc_u32 s1, s7, s37
	global_load_dwordx2 v[86:87], v146, s[0:1]
	global_load_dwordx2 v[88:89], v146, s[0:1] offset:512
	global_load_dwordx2 v[84:85], v146, s[0:1] offset:1024
	global_load_dwordx2 v[82:83], v146, s[0:1] offset:1536
	global_load_dwordx2 v[80:81], v146, s[0:1] offset:2048
	global_load_dwordx2 v[78:79], v146, s[0:1] offset:2560
	global_load_dwordx2 v[76:77], v146, s[0:1] offset:3072
	global_load_dwordx2 v[74:75], v146, s[0:1] offset:3584
	s_movk_i32 s41, 0x1000
	v_mov_b32_e32 v148, 0x358637bd
	s_mov_b32 s45, 0xf800000
	v_mov_b32_e32 v149, 0x260
	s_ashr_i32 s20, s3, 12
	s_add_u32 s40, s82, 0x2c000000
	s_addc_u32 s44, s83, 0
	v_lshlrev_b32_e32 v150, 2, v170
	v_and_b32_e32 v151, 15, v0
	v_lshrrev_b32_e32 v154, 4, v170
	s_waitcnt vmcnt(0)
	v_lshlrev_b32_e32 v111, 16, v2
	v_lshlrev_b32_e32 v110, 16, v4
	v_and_b32_e32 v113, 0xffff0000, v2
	v_and_b32_e32 v112, 0xffff0000, v4
	v_lshlrev_b32_e32 v107, 16, v3
	v_lshlrev_b32_e32 v106, 16, v5
	v_and_b32_e32 v109, 0xffff0000, v3
	v_and_b32_e32 v108, 0xffff0000, v5
	v_lshlrev_b32_e32 v105, 16, v7
	v_lshlrev_b32_e32 v104, 16, v6
	v_and_b32_e32 v7, 0xffff0000, v7
	v_and_b32_e32 v6, 0xffff0000, v6
	v_pk_add_f32 v[2:3], v[110:111], v[112:113]
	v_pk_add_f32 v[4:5], v[106:107], v[108:109]
	v_lshlrev_b32_e32 v117, 16, v10
	v_and_b32_e32 v69, 0xffff0000, v10
	v_lshlrev_b32_e32 v101, 16, v11
	v_and_b32_e32 v67, 0xffff0000, v11
	v_pk_add_f32 v[10:11], v[104:105], v[6:7]
	v_pk_add_f32 v[2:3], v[2:3], v[4:5]
	v_lshlrev_b32_e32 v70, 16, v8
	v_and_b32_e32 v71, 0xffff0000, v8
	v_lshlrev_b32_e32 v72, 16, v9
	v_and_b32_e32 v73, 0xffff0000, v9
	v_pk_add_f32 v[4:5], v[10:11], v[10:11] op_sel:[0,1] op_sel_hi:[1,0]
	v_add_f32_e32 v2, 0, v2
	v_add_f32_e32 v100, v70, v71
	v_add_f32_e32 v66, v72, v73
	v_mov_b32_e32 v5, v69
	v_add_f32_e32 v116, v2, v3
	v_lshlrev_b32_e32 v99, 16, v13
	v_lshlrev_b32_e32 v98, 16, v12
	v_and_b32_e32 v9, 0xffff0000, v13
	v_and_b32_e32 v8, 0xffff0000, v12
	v_pk_add_f32 v[10:11], v[100:101], v[66:67]
	v_pk_add_f32 v[2:3], v[116:117], v[4:5]
	v_pk_add_f32 v[12:13], v[98:99], v[8:9]
	v_pk_add_f32 v[2:3], v[2:3], v[10:11]
	v_lshlrev_b32_e32 v94, 16, v14
	v_and_b32_e32 v95, 0xffff0000, v14
	v_lshlrev_b32_e32 v96, 16, v15
	v_and_b32_e32 v97, 0xffff0000, v15
	v_lshlrev_b32_e32 v92, 16, v16
	v_and_b32_e32 v93, 0xffff0000, v16
	v_pk_add_f32 v[12:13], v[12:13], v[12:13] op_sel:[0,1] op_sel_hi:[1,0]
	v_pk_add_f32 v[2:3], v[2:3], v[2:3] op_sel:[0,1] op_sel_hi:[1,0]
	v_lshlrev_b32_e32 v103, 16, v17
	v_and_b32_e32 v91, 0xffff0000, v17
	v_add_f32_e32 v102, v94, v95
	v_add_f32_e32 v90, v96, v97
	v_mov_b32_e32 v13, v93
	v_mov_b32_e32 v3, v92
	v_pk_add_f32 v[14:15], v[102:103], v[90:91]
	v_pk_add_f32 v[2:3], v[2:3], v[12:13]
	v_cndmask_b32_e32 v4, v19, v25, vcc
	v_pk_add_f32 v[2:3], v[2:3], v[14:15]
	v_lshlrev_b32_e32 v147, 2, v4
	v_add_f32_e32 v2, v2, v3
	ds_bpermute_b32 v3, v1, v2
	v_ashrrev_i32_e32 v19, 31, v18
	v_and_b32_e32 v135, 0xffff0000, v79
	v_and_b32_e32 v134, 0xffff0000, v78
	s_waitcnt lgkmcnt(0)
	v_add_f32_e32 v2, v2, v3
	ds_bpermute_b32 v3, v142, v2
	s_waitcnt lgkmcnt(0)
	v_add_f32_e32 v2, v2, v3
	ds_bpermute_b32 v3, v143, v2
	s_waitcnt lgkmcnt(0)
	v_add_f32_e32 v2, v2, v3
	ds_bpermute_b32 v3, v144, v2
	s_waitcnt lgkmcnt(0)
	v_add_f32_e32 v2, v2, v3
	ds_bpermute_b32 v3, v145, v2
	s_waitcnt lgkmcnt(0)
	v_add_f32_e32 v14, v2, v3
	ds_bpermute_b32 v15, v147, v14
	v_lshlrev_b64 v[2:3], 4, v[18:19]
	v_lshl_add_u64 v[10:11], s[8:9], 0, v[2:3]
	v_lshl_add_u64 v[12:13], s[10:11], 0, v[2:3]
	global_load_dwordx4 v[2:5], v[10:11], off
	s_waitcnt lgkmcnt(0)
; __device__ __forceinline__ unsigned cvt_pk_bf16(float lo, float hi) { unsigned r; asm volatile("v_cvt_pk_bf16_f32 %0, %1, %2" : "=v"(r) : "v"(lo), "v"(hi)); return r; }
; __device__ __forceinline__ float bf_lo(unsigned w) { return __uint_as_float(w << 16); }
; __device__ __forceinline__ float bf_hi(unsigned w) { return __uint_as_float(w & 0xffff0000u); }
; __device__ __forceinline__ void p6_router(Frame& F) {
;     ...
;                 for (int j = 0; j < 8; ++j) { const u32x2 zb = zr[q][j]; v[j] = (f32x4){bf_lo(zb.x), bf_hi(zb.x), bf_lo(zb.y), bf_hi(zb.y)}; s += (v[j][0] + v[j][1]) + (v[j][2] + v[j][3]); }
;                 float mean = wave_sum(s) * (1.f / DM), s2 = 0.f;
; #pragma unroll
;                 for (int j = 0; j < 8; ++j) { v[j] = v[j] - mean; s2 += (v[j][0] * v[j][0] + v[j][1] * v[j][1]) + (v[j][2] * v[j][2] + v[j][3] * v[j][3]); }
;                 float rstd = 1.f / sqrtf(wave_sum(s2) * (1.f / DM) + LN_EPS);
;                 s = 0.f;
; #pragma unroll
;                 for (int j = 0; j < 8; ++j) { v[j] = v[j] * rstd * pw[j] + pb[j]; { u32x2 xb; xb.x = cvt_pk_bf16(v[j][0], v[j][1]); xb.y = cvt_pk_bf16(v[j][2], v[j][3]); ((u32x2*)(X1 + (size_t)t * DM))[lane + 64 * j] = xb; } s += (v[j][0] + v[j][1]) + (v[j][2] + v[j][3]); }
	v_add_f32_e32 v20, v14, v15
	v_fmac_f32_e32 v108, 0xba000000, v20
	v_fmac_f32_e32 v112, 0xba000000, v20
	v_fmac_f32_e32 v109, 0xba000000, v20
	v_fmac_f32_e32 v113, 0xba000000, v20
	v_fmac_f32_e32 v106, 0xba000000, v20
	v_fmac_f32_e32 v110, 0xba000000, v20
	v_fmac_f32_e32 v107, 0xba000000, v20
	v_fmac_f32_e32 v111, 0xba000000, v20
	v_pk_mul_f32 v[14:15], v[112:113], v[112:113]
	v_pk_mul_f32 v[16:17], v[108:109], v[108:109]
	v_fmac_f32_e32 v6, 0xba000000, v20
	v_fmac_f32_e32 v7, 0xba000000, v20
	v_fmac_f32_e32 v105, 0xba000000, v20
	v_pk_fma_f32 v[14:15], v[110:111], v[110:111], v[14:15]
	v_pk_fma_f32 v[16:17], v[106:107], v[106:107], v[16:17]
	v_fmac_f32_e32 v104, 0xba000000, v20
	v_mov_b32_e32 v120, v105
	v_mov_b32_e32 v121, v7
	v_mov_b32_e32 v105, v6
	v_pk_add_f32 v[14:15], v[14:15], v[16:17]
	v_pk_mul_f32 v[16:17], v[120:121], v[120:121]
	v_pk_mul_f32 v[6:7], v[104:105], v[104:105]
	v_fmac_f32_e32 v70, 0xba000000, v20
	v_pk_mov_b32 v[18:19], v[6:7], v[16:17] op_sel:[1,0]
	v_mov_b32_e32 v7, v17
	v_pk_add_f32 v[6:7], v[18:19], v[6:7]
	v_fmac_f32_e32 v71, 0xba000000, v20
	v_pk_add_f32 v[6:7], v[6:7], v[6:7] op_sel_hi:[0,1]
	v_fmac_f32_e32 v72, 0xba000000, v20
	v_mul_f32_e32 v6, v70, v70
	v_fmac_f32_e32 v73, 0xba000000, v20
	v_pk_fma_f32 v[16:17], v[70:71], v[70:71], v[6:7] op_sel_hi:[1,1,0]
	v_mul_f32_e32 v6, v72, v72
	v_pk_add_f32 v[14:15], v[14:15], v[14:15] op_sel_hi:[0,1]
	v_pk_fma_f32 v[18:19], v[72:73], v[72:73], v[6:7] op_sel_hi:[1,1,0]
	v_fmac_f32_e32 v67, 0xba000000, v20
	v_fmac_f32_e32 v101, 0xba000000, v20
	v_fmac_f32_e32 v69, 0xba000000, v20
	v_fmac_f32_e32 v117, 0xba000000, v20
	v_mul_f32_e32 v16, v117, v117
	v_mul_f32_e32 v18, v69, v69
	v_mul_f32_e32 v6, v101, v101
	v_mul_f32_e32 v14, v67, v67
	v_pk_add_f32 v[16:17], v[16:17], v[18:19]
	v_pk_add_f32 v[6:7], v[6:7], v[14:15]
	v_fmac_f32_e32 v8, 0xba000000, v20
	v_fmac_f32_e32 v9, 0xba000000, v20
	v_fmac_f32_e32 v99, 0xba000000, v20
	v_pk_add_f32 v[6:7], v[16:17], v[6:7]
	v_fmac_f32_e32 v98, 0xba000000, v20
	v_mov_b32_e32 v118, v99
	v_mov_b32_e32 v119, v9
	v_mov_b32_e32 v99, v8
	v_pk_add_f32 v[6:7], v[6:7], v[6:7] op_sel_hi:[0,1]
	v_pk_mul_f32 v[14:15], v[118:119], v[118:119]
	v_pk_mul_f32 v[8:9], v[98:99], v[98:99]
	v_fmac_f32_e32 v94, 0xba000000, v20
	v_pk_mov_b32 v[16:17], v[8:9], v[14:15] op_sel:[1,0]
	v_mov_b32_e32 v9, v15
	v_fmac_f32_e32 v95, 0xba000000, v20
	v_fmac_f32_e32 v96, 0xba000000, v20
	v_mul_f32_e32 v6, v94, v94
	v_pk_add_f32 v[8:9], v[16:17], v[8:9]
	v_fmac_f32_e32 v97, 0xba000000, v20
	v_pk_fma_f32 v[14:15], v[94:95], v[94:95], v[6:7] op_sel_hi:[1,1,0]
	v_mul_f32_e32 v6, v96, v96
	v_pk_add_f32 v[8:9], v[8:9], v[8:9] op_sel_hi:[0,1]
	v_pk_fma_f32 v[16:17], v[96:97], v[96:97], v[6:7] op_sel_hi:[1,1,0]
	v_fmac_f32_e32 v91, 0xba000000, v20
	v_fmac_f32_e32 v103, 0xba000000, v20
	v_fmac_f32_e32 v93, 0xba000000, v20
	v_fmac_f32_e32 v92, 0xba000000, v20
	v_mul_f32_e32 v14, v92, v92
	v_mul_f32_e32 v16, v93, v93
	v_mul_f32_e32 v8, v103, v103
	v_mul_f32_e32 v6, v91, v91
	v_pk_add_f32 v[14:15], v[14:15], v[16:17]
	v_pk_add_f32 v[6:7], v[8:9], v[6:7]
	global_load_dwordx4 v[62:65], v[12:13], off
	v_pk_add_f32 v[6:7], v[14:15], v[6:7]
	global_load_dwordx4 v[54:57], v[10:11], off offset:1024
	global_load_dwordx4 v[58:61], v[12:13], off offset:1024
	v_add_f32_e32 v6, v6, v7
	ds_bpermute_b32 v7, v1, v6
	global_load_dwordx4 v[46:49], v[10:11], off offset:2048
	global_load_dwordx4 v[38:41], v[10:11], off offset:3072
	global_load_dwordx4 v[50:53], v[12:13], off offset:2048
	global_load_dwordx4 v[42:45], v[12:13], off offset:3072
	v_mov_b32_e32 v124, v107
	v_mov_b32_e32 v107, v108
	v_mov_b32_e32 v122, v111
	s_waitcnt lgkmcnt(0)
	v_add_f32_e32 v6, v6, v7
	ds_bpermute_b32 v7, v142, v6
	v_mov_b32_e32 v123, v113
	v_mov_b32_e32 v111, v112
	v_mov_b32_e32 v125, v109
	s_waitcnt lgkmcnt(0)
	v_add_f32_e32 v8, v6, v7
	ds_bpermute_b32 v9, v143, v8
	v_add_co_u32_e32 v6, vcc, s41, v10
	s_waitcnt lgkmcnt(0)
	v_add_f32_e32 v8, v8, v9
	ds_bpermute_b32 v9, v144, v8
	v_addc_co_u32_e32 v7, vcc, 0, v11, vcc
	v_add_co_u32_e32 v10, vcc, s41, v12
	global_load_dwordx4 v[30:33], v[6:7], off
	global_load_dwordx4 v[22:25], v[6:7], off offset:1024
	v_addc_co_u32_e32 v11, vcc, 0, v13, vcc
	s_waitcnt lgkmcnt(0)
	v_add_f32_e32 v12, v8, v9
	ds_bpermute_b32 v13, v145, v12
	global_load_dwordx4 v[34:37], v[10:11], off
	global_load_dwordx4 v[26:29], v[10:11], off offset:1024
	global_load_dwordx4 v[14:17], v[6:7], off offset:2048
	s_nop 0
	global_load_dwordx4 v[6:9], v[6:7], off offset:3072
	s_waitcnt lgkmcnt(0)
	v_add_f32_e32 v66, v12, v13
	global_load_dwordx4 v[18:21], v[10:11], off offset:2048
	s_nop 0
	global_load_dwordx4 v[10:13], v[10:11], off offset:3072
	ds_bpermute_b32 v68, v147, v66
	s_waitcnt lgkmcnt(0)
	v_add_f32_e32 v66, v66, v68
	v_fmamk_f32 v66, v66, 0x3a000000, v148
	v_mul_f32_e32 v68, 0x4f800000, v66
	v_cmp_gt_f32_e32 vcc, s45, v66
	s_nop 1
	v_cndmask_b32_e32 v66, v66, v68, vcc
	v_sqrt_f32_e32 v68, v66
	s_nop 0
	v_add_u32_e32 v90, -1, v68
	v_fma_f32 v100, -v90, v68, v66
	v_cmp_ge_f32_e64 s[0:1], 0, v100
	v_add_u32_e32 v100, 1, v68
	s_nop 0
	v_cndmask_b32_e64 v90, v68, v90, s[0:1]
	v_fma_f32 v68, -v100, v68, v66
	v_cmp_lt_f32_e64 s[0:1], 0, v68
	s_nop 1
	v_cndmask_b32_e64 v68, v90, v100, s[0:1]
	v_mul_f32_e32 v90, 0x37800000, v68
	v_cndmask_b32_e32 v68, v68, v90, vcc
	v_cmp_class_f32_e32 vcc, v66, v149
	s_nop 1
	v_cndmask_b32_e32 v66, v68, v66, vcc
	v_div_scale_f32 v68, s[0:1], v66, v66, 1.0
	v_rcp_f32_e32 v90, v68
	s_add_u32 s0, s42, s16
	s_addc_u32 s1, s43, s17
	s_lshl_b64 s[38:39], s[4:5], 11
	v_fma_f32 v100, -v68, v90, 1.0
	v_fmac_f32_e32 v90, v100, v90
	v_div_scale_f32 v100, vcc, 1.0, v66, 1.0
	v_mul_f32_e32 v102, v100, v90
	v_fma_f32 v108, -v68, v102, v100
	v_fmac_f32_e32 v102, v108, v90
	v_fma_f32 v68, -v68, v102, v100
	v_div_fmas_f32 v68, v68, v90, v102
	v_div_fixup_f32 v102, v68, v66, 1.0
	v_pk_mul_f32 v[106:107], v[106:107], v[102:103] op_sel_hi:[1,0]
	v_pk_mul_f32 v[108:109], v[110:111], v[102:103] op_sel_hi:[1,0]
	s_waitcnt vmcnt(14)
; __device__ __forceinline__ unsigned cvt_pk_bf16(float lo, float hi) { unsigned r; asm volatile("v_cvt_pk_bf16_f32 %0, %1, %2" : "=v"(r) : "v"(lo), "v"(hi)); return r; }
; __device__ __forceinline__ void p6_router(Frame& F) {
;     ...
;                 for (int j = 0; j < 8; ++j) { v[j] = v[j] * rstd * pw[j] + pb[j]; { u32x2 xb; xb.x = cvt_pk_bf16(v[j][0], v[j][1]); xb.y = cvt_pk_bf16(v[j][2], v[j][3]); ((u32x2*)(X1 + (size_t)t * DM))[lane + 64 * j] = xb; } s += (v[j][0] + v[j][1]) + (v[j][2] + v[j][3]); }
;                 mean = wave_sum(s) * (1.f / DM); s2 = 0.f;
	v_pk_fma_f32 v[112:113], v[4:5], v[106:107], v[64:65]
	v_pk_mul_f32 v[106:107], v[122:123], v[102:103] op_sel_hi:[1,0]
	v_pk_fma_f32 v[114:115], v[2:3], v[108:109], v[62:63]
	v_pk_mul_f32 v[108:109], v[124:125], v[102:103] op_sel_hi:[1,0]
	s_waitcnt vmcnt(12)
	v_pk_fma_f32 v[110:111], v[54:55], v[106:107], v[58:59]
	v_pk_fma_f32 v[108:109], v[56:57], v[108:109], v[60:61]
	v_mov_b32_e32 v106, v110
	v_mov_b32_e32 v107, v114
	v_mov_b32_e32 v122, v111
	v_mov_b32_e32 v123, v115
	v_pk_add_f32 v[106:107], v[106:107], v[122:123]
	v_mov_b32_e32 v122, v109
	v_mov_b32_e32 v123, v113
	v_mov_b32_e32 v124, v108
	v_mov_b32_e32 v125, v112
	v_pk_add_f32 v[122:123], v[122:123], v[124:125]
	v_mov_b32_e32 v68, v117
	v_pk_add_f32 v[106:107], v[106:107], v[122:123]
	v_pk_mul_f32 v[68:69], v[68:69], v[102:103] op_sel_hi:[1,0]
	v_add_f32_e32 v66, 0, v107
	v_add_f32_e32 v123, v106, v66
	v_pk_mul_f32 v[106:107], v[104:105], v[102:103] op_sel_hi:[1,0]
	v_pk_mul_f32 v[104:105], v[120:121], v[102:103] op_sel_hi:[1,0]
	s_waitcnt vmcnt(9)
	v_pk_fma_f32 v[106:107], v[46:47], v[106:107], v[50:51]
	v_pk_fma_f32 v[104:105], v[48:49], v[104:105], v[52:53]
	v_mov_b32_e32 v120, v106
	v_mov_b32_e32 v121, v105
	v_pk_mov_b32 v[124:125], v[106:107], v[104:105] op_sel:[1,0]
	v_mov_b32_e32 v66, v101
	v_pk_add_f32 v[120:121], v[120:121], v[124:125]
	v_pk_mul_f32 v[124:125], v[70:71], v[102:103] op_sel_hi:[1,0]
	v_pk_mul_f32 v[70:71], v[72:73], v[102:103] op_sel_hi:[1,0]
	v_pk_mul_f32 v[66:67], v[66:67], v[102:103] op_sel_hi:[1,0]
	v_pk_add_f32 v[120:121], v[120:121], v[120:121] op_sel_hi:[0,1]
	s_waitcnt vmcnt(8)
	v_pk_fma_f32 v[70:71], v[40:41], v[70:71], v[44:45]
	v_pk_fma_f32 v[72:73], v[38:39], v[124:125], v[42:43]
	s_waitcnt vmcnt(5)
	v_pk_fma_f32 v[66:67], v[32:33], v[66:67], v[36:37]
	v_pk_fma_f32 v[68:69], v[30:31], v[68:69], v[34:35]
	v_add_f32_e32 v125, v72, v73
	v_add_f32_e32 v129, v71, v70
	v_mov_b32_e32 v124, v68
	v_mov_b32_e32 v128, v69
	v_mov_b32_e32 v120, v67
	v_mov_b32_e32 v122, v66
	v_pk_add_f32 v[100:101], v[124:125], v[128:129]
	v_pk_add_f32 v[116:117], v[120:121], v[122:123]
	v_mov_b32_e32 v90, v103
	v_pk_add_f32 v[100:101], v[100:101], v[116:117]
	v_pk_mul_f32 v[92:93], v[92:93], v[102:103] op_sel_hi:[1,0]
	v_pk_add_f32 v[116:117], v[100:101], v[100:101] op_sel_hi:[0,1]
	v_pk_mul_f32 v[100:101], v[98:99], v[102:103] op_sel_hi:[1,0]
	v_pk_mul_f32 v[98:99], v[118:119], v[102:103] op_sel_hi:[1,0]
	s_waitcnt vmcnt(4)
	v_pk_fma_f32 v[100:101], v[22:23], v[100:101], v[26:27]
	v_pk_fma_f32 v[98:99], v[24:25], v[98:99], v[28:29]
	v_mov_b32_e32 v118, v100
	v_mov_b32_e32 v119, v99
	v_pk_mov_b32 v[120:121], v[100:101], v[98:99] op_sel:[1,0]
	v_pk_mul_f32 v[90:91], v[90:91], v[102:103] op_sel_hi:[1,0]
	v_pk_add_f32 v[118:119], v[118:119], v[120:121]
	v_pk_mul_f32 v[120:121], v[94:95], v[102:103] op_sel_hi:[1,0]
	v_pk_mul_f32 v[94:95], v[96:97], v[102:103] op_sel_hi:[1,0]
	v_pk_add_f32 v[118:119], v[118:119], v[118:119] op_sel_hi:[0,1]
	s_waitcnt vmcnt(1)
	v_pk_fma_f32 v[94:95], v[16:17], v[94:95], v[20:21]
	v_pk_fma_f32 v[96:97], v[14:15], v[120:121], v[18:19]
	s_waitcnt vmcnt(0)
	v_pk_fma_f32 v[90:91], v[8:9], v[90:91], v[12:13]
	v_pk_fma_f32 v[92:93], v[6:7], v[92:93], v[10:11]
	v_add_f32_e32 v121, v96, v97
	v_add_f32_e32 v123, v95, v94
	v_mov_b32_e32 v120, v92
	v_mov_b32_e32 v122, v93
	v_mov_b32_e32 v118, v91
	v_mov_b32_e32 v116, v90
	v_pk_add_f32 v[102:103], v[120:121], v[122:123]
	v_pk_add_f32 v[116:117], v[118:119], v[116:117]
	v_cvt_pk_bf16_f32 v126, v114, v115
	v_cvt_pk_bf16_f32 v127, v112, v113
	global_store_dwordx2 v146, v[126:127], s[0:1] nt
	v_pk_add_f32 v[102:103], v[102:103], v[116:117]
	s_nop 0
	v_add_f32_e32 v103, v102, v103
	ds_bpermute_b32 v116, v1, v103
	v_cvt_pk_bf16_f32 v102, v110, v111
	s_waitcnt lgkmcnt(0)
	v_add_f32_e32 v116, v103, v116
	ds_bpermute_b32 v117, v142, v116
	v_cvt_pk_bf16_f32 v103, v108, v109
	global_store_dwordx2 v146, v[102:103], s[0:1] offset:512 nt
	v_cvt_pk_bf16_f32 v102, v106, v107
	v_cvt_pk_bf16_f32 v103, v104, v105
	s_waitcnt lgkmcnt(0)
	v_add_f32_e32 v116, v116, v117
	ds_bpermute_b32 v117, v143, v116
	global_store_dwordx2 v146, v[102:103], s[0:1] offset:1024 nt
	v_cvt_pk_bf16_f32 v102, v72, v73
	v_cvt_pk_bf16_f32 v103, v70, v71
	global_store_dwordx2 v146, v[102:103], s[0:1] offset:1536 nt
	s_waitcnt lgkmcnt(0)
	v_add_f32_e32 v116, v116, v117
	ds_bpermute_b32 v117, v144, v116
	v_cvt_pk_bf16_f32 v102, v68, v69
	v_cvt_pk_bf16_f32 v103, v66, v67
	global_store_dwordx2 v146, v[102:103], s[0:1] offset:2048 nt
	v_cvt_pk_bf16_f32 v102, v100, v101
	s_waitcnt lgkmcnt(0)
	v_add_f32_e32 v116, v116, v117
	ds_bpermute_b32 v117, v145, v116
	v_cvt_pk_bf16_f32 v103, v98, v99
	global_store_dwordx2 v146, v[102:103], s[0:1] offset:2560 nt
	v_cvt_pk_bf16_f32 v102, v96, v97
	v_cvt_pk_bf16_f32 v103, v94, v95
	s_waitcnt lgkmcnt(0)
	v_add_f32_e32 v116, v116, v117
	ds_bpermute_b32 v117, v147, v116
	global_store_dwordx2 v146, v[102:103], s[0:1] offset:3072 nt
	v_cvt_pk_bf16_f32 v102, v92, v93
	v_cvt_pk_bf16_f32 v103, v90, v91
	global_store_dwordx2 v146, v[102:103], s[0:1] offset:3584 nt
	s_waitcnt lgkmcnt(0)
; __device__ __forceinline__ void p6_router(Frame& F) {
;     ...
;                 mean = wave_sum(s) * (1.f / DM); s2 = 0.f;
; #pragma unroll
;                 for (int j = 0; j < 8; ++j) { v[j] = v[j] - mean; s2 += (v[j][0] * v[j][0] + v[j][1] * v[j][1]) + (v[j][2] * v[j][2] + v[j][3] * v[j][3]); }
;                 rstd = 1.f / sqrtf(wave_sum(s2) * (1.f / DM) + LN_EPS);
;                 int loq = lane; asm volatile("" : "+v"(loq));
; #pragma unroll
;                 for (int j = 0; j < 8; ++j) { const f32x4 sh = ((const f32x4*)(mod + (size_t)b * 12288 + 6144))[loq + 64 * j], sc = ((const f32x4*)(mod + (size_t)b * 12288 + 8192))[loq + 64 * j];
	v_add_f32_e32 v122, v116, v117
	v_fmamk_f32 v115, v122, 0xba000000, v115
	v_fmamk_f32 v111, v122, 0xba000000, v111
	v_fmamk_f32 v113, v122, 0xba000000, v113
	v_fmac_f32_e32 v114, 0xba000000, v122
	v_fmamk_f32 v109, v122, 0xba000000, v109
	v_fmac_f32_e32 v110, 0xba000000, v122
	v_mov_b32_e32 v116, v115
	v_mov_b32_e32 v117, v111
	v_fmac_f32_e32 v112, 0xba000000, v122
	v_fmac_f32_e32 v108, 0xba000000, v122
	v_mov_b32_e32 v102, v114
	v_mov_b32_e32 v103, v110
	v_pk_mul_f32 v[116:117], v[116:117], v[116:117]
	v_mov_b32_e32 v118, v113
	v_mov_b32_e32 v119, v109
	v_pk_fma_f32 v[102:103], v[102:103], v[102:103], v[116:117]
	v_mov_b32_e32 v116, v112
	v_mov_b32_e32 v117, v108
	v_pk_mul_f32 v[118:119], v[118:119], v[118:119]
	v_fmamk_f32 v107, v122, 0xba000000, v107
	v_pk_fma_f32 v[116:117], v[116:117], v[116:117], v[118:119]
	v_fmac_f32_e32 v106, 0xba000000, v122
	v_pk_add_f32 v[102:103], v[102:103], v[116:117]
	v_fmamk_f32 v105, v122, 0xba000000, v105
	v_fmac_f32_e32 v104, 0xba000000, v122
	v_pk_add_f32 v[102:103], v[102:103], v[102:103] op_sel_hi:[0,1]
	v_pk_mul_f32 v[116:117], v[104:105], v[104:105]
	v_pk_mul_f32 v[118:119], v[106:107], v[106:107]
	v_fmac_f32_e32 v72, 0xba000000, v122
	v_pk_mov_b32 v[120:121], v[118:119], v[116:117] op_sel:[1,0]
	v_mov_b32_e32 v119, v117
	v_fmamk_f32 v73, v122, 0xba000000, v73
	v_fmac_f32_e32 v70, 0xba000000, v122
	v_mul_f32_e32 v102, v72, v72
	v_pk_add_f32 v[116:117], v[120:121], v[118:119]
	v_fmamk_f32 v71, v122, 0xba000000, v71
	v_pk_fma_f32 v[118:119], v[72:73], v[72:73], v[102:103] op_sel_hi:[1,1,0]
	v_mul_f32_e32 v102, v70, v70
	v_pk_add_f32 v[116:117], v[116:117], v[116:117] op_sel_hi:[0,1]
	v_pk_fma_f32 v[120:121], v[70:71], v[70:71], v[102:103] op_sel_hi:[1,1,0]
	v_fmamk_f32 v67, v122, 0xba000000, v67
	v_fmac_f32_e32 v66, 0xba000000, v122
	v_fmamk_f32 v69, v122, 0xba000000, v69
	v_fmac_f32_e32 v68, 0xba000000, v122
	v_mul_f32_e32 v118, v68, v68
	v_mul_f32_e32 v120, v69, v69
	v_mul_f32_e32 v116, v66, v66
	v_mul_f32_e32 v102, v67, v67
	v_pk_add_f32 v[118:119], v[118:119], v[120:121]
	v_pk_add_f32 v[102:103], v[116:117], v[102:103]
	v_fmamk_f32 v101, v122, 0xba000000, v101
	v_fmac_f32_e32 v100, 0xba000000, v122
	v_fmamk_f32 v99, v122, 0xba000000, v99
	v_fmac_f32_e32 v98, 0xba000000, v122
	v_pk_add_f32 v[102:103], v[118:119], v[102:103]
	v_pk_mul_f32 v[116:117], v[98:99], v[98:99]
	v_pk_mul_f32 v[118:119], v[100:101], v[100:101]
	s_mul_hi_i32 s0, s20, 0xc000
	s_mul_i32 s20, s20, 0xc000
	v_pk_mov_b32 v[120:121], v[118:119], v[116:117] op_sel:[1,0]
	v_mov_b32_e32 v119, v117
	s_add_u32 s1, s82, s20
	v_pk_add_f32 v[116:117], v[120:121], v[118:119]
	s_addc_u32 s0, s83, s0
	v_pk_add_f32 v[128:129], v[116:117], v[116:117] op_sel_hi:[0,1]
	v_mov_b32_e32 v116, v170
	s_add_u32 s16, s1, 0x106000
	s_addc_u32 s17, s0, 0
	v_ashrrev_i32_e32 v117, 31, v116
	v_lshlrev_b64 v[118:119], 4, v[116:117]
	s_add_u32 s20, s1, 0x108000
	v_lshl_add_u64 v[116:117], s[16:17], 0, v[118:119]
	s_addc_u32 s21, s0, 0
	v_fmamk_f32 v97, v122, 0xba000000, v97
	v_fmac_f32_e32 v96, 0xba000000, v122
	v_fmamk_f32 v95, v122, 0xba000000, v95
	v_fmac_f32_e32 v94, 0xba000000, v122
	v_fmamk_f32 v91, v122, 0xba000000, v91
	v_fmac_f32_e32 v90, 0xba000000, v122
	v_fmamk_f32 v93, v122, 0xba000000, v93
	v_fmac_f32_e32 v92, 0xba000000, v122
	v_lshl_add_u64 v[118:119], s[20:21], 0, v[118:119]
	global_load_dwordx4 v[120:123], v[116:117], off
	global_load_dwordx4 v[124:127], v[118:119], off
	v_pk_add_f32 v[102:103], v[102:103], v[102:103] op_sel_hi:[0,1]
	v_mul_f32_e32 v102, v96, v96
	v_pk_fma_f32 v[130:131], v[96:97], v[96:97], v[102:103] op_sel_hi:[1,1,0]
	v_mul_f32_e32 v102, v94, v94
	v_pk_fma_f32 v[132:133], v[94:95], v[94:95], v[102:103] op_sel_hi:[1,1,0]
	v_mul_f32_e32 v130, v92, v92
	v_mul_f32_e32 v132, v93, v93
	v_mul_f32_e32 v128, v90, v90
	v_mul_f32_e32 v102, v91, v91
	v_pk_add_f32 v[130:131], v[130:131], v[132:133]
	v_pk_add_f32 v[102:103], v[128:129], v[102:103]
	s_lshl_b32 s5, s46, 5
	v_pk_add_f32 v[102:103], v[130:131], v[102:103]
	v_and_b32_e32 v133, 0xffff0000, v85
	v_add_f32_e32 v102, v102, v103
	ds_bpermute_b32 v103, v1, v102
	v_and_b32_e32 v132, 0xffff0000, v84
	s_waitcnt lgkmcnt(0)
	v_add_f32_e32 v102, v102, v103
	ds_bpermute_b32 v103, v142, v102
	s_waitcnt lgkmcnt(0)
	v_add_f32_e32 v102, v102, v103
	ds_bpermute_b32 v103, v143, v102
	s_waitcnt lgkmcnt(0)
	v_add_f32_e32 v102, v102, v103
	ds_bpermute_b32 v103, v144, v102
	s_waitcnt lgkmcnt(0)
	v_add_f32_e32 v102, v102, v103
	ds_bpermute_b32 v103, v145, v102
	s_waitcnt lgkmcnt(0)
	v_add_f32_e32 v102, v102, v103
	ds_bpermute_b32 v103, v147, v102
	s_waitcnt lgkmcnt(0)
	v_add_f32_e32 v102, v102, v103
	v_fmamk_f32 v102, v102, 0x3a000000, v148
	v_mul_f32_e32 v103, 0x4f800000, v102
	v_cmp_gt_f32_e32 vcc, s45, v102
	s_waitcnt vmcnt(0)
; #define LAS __attribute__((address_space(3)))
; __device__ __forceinline__ unsigned cvt_pk_bf16(float lo, float hi) { unsigned r; asm volatile("v_cvt_pk_bf16_f32 %0, %1, %2" : "=v"(r) : "v"(lo), "v"(hi)); return r; }
; __device__ __forceinline__ unsigned pk4_fp8(float a, float b, float c, float d) { int w = 0; w = __builtin_amdgcn_cvt_pk_fp8_f32(a, b, w, false); w = __builtin_amdgcn_cvt_pk_fp8_f32(c, d, w, true); return (unsigned)w; }
; __device__ __forceinline__ float bf_lo(unsigned w) { return __uint_as_float(w << 16); }
; __device__ __forceinline__ float bf_hi(unsigned w) { return __uint_as_float(w & 0xffff0000u); }
; __device__ __forceinline__ void p6_router(Frame& F) {
;     ...
;                 rstd = 1.f / sqrtf(wave_sum(s2) * (1.f / DM) + LN_EPS);
;                 int loq = lane; asm volatile("" : "+v"(loq));
; #pragma unroll
;                 for (int j = 0; j < 8; ++j) { const f32x4 sh = ((const f32x4*)(mod + (size_t)b * 12288 + 6144))[loq + 64 * j], sc = ((const f32x4*)(mod + (size_t)b * 12288 + 8192))[loq + 64 * j];
;                     const f32x4 y = v[j] * rstd * (sc + 1.0f) + sh;
;                     u32x2 wh; wh.x = cvt_pk_bf16(y[0], y[1]); wh.y = cvt_pk_bf16(y[2], y[3]);
;                     const f32x4 yl = {y[0] - bf_lo(wh.x), y[1] - bf_hi(wh.x), y[2] - bf_lo(wh.y), y[3] - bf_hi(wh.y)};
;                     u32x2 wl; wl.x = cvt_pk_bf16(yl[0], yl[1]); wl.y = cvt_pk_bf16(yl[2], yl[3]);
;                     { const int r = 2 * wave + q; LAS unsigned char* rowp = F.lds + r * 4096 + ((((lane >> 1) + 32 * j) ^ r) << 4) + (lane & 1) * 8;
;                       *(LAS u32x2*)rowp = wh; *(LAS u32x2*)(rowp + 65536) = wl; }
;                     U2F[(size_t)t * (DM / 4) + lane + 64 * j] = pk4_fp8(y[0], y[1], y[2], y[3]); }
	v_pk_add_f32 v[124:125], v[124:125], 1.0 op_sel_hi:[1,0]
	v_cndmask_b32_e32 v102, v102, v103, vcc
	v_sqrt_f32_e32 v103, v102
	v_pk_add_f32 v[126:127], v[126:127], 1.0 op_sel_hi:[1,0]
	v_add_u32_e32 v128, -1, v103
	v_fma_f32 v129, -v128, v103, v102
	v_cmp_ge_f32_e64 s[0:1], 0, v129
	v_add_u32_e32 v129, 1, v103
	s_nop 0
	v_cndmask_b32_e64 v128, v103, v128, s[0:1]
	v_fma_f32 v103, -v129, v103, v102
	v_cmp_lt_f32_e64 s[0:1], 0, v103
	s_nop 1
	v_cndmask_b32_e64 v103, v128, v129, s[0:1]
	v_mul_f32_e32 v128, 0x37800000, v103
	v_cndmask_b32_e32 v103, v103, v128, vcc
	v_cmp_class_f32_e32 vcc, v102, v149
	s_nop 1
	v_cndmask_b32_e32 v102, v103, v102, vcc
	v_div_scale_f32 v103, s[0:1], v102, v102, 1.0
	v_rcp_f32_e32 v128, v103
	s_lshl_b32 s0, s46, 13
	s_add_i32 s0, s0, 0
	s_add_u32 s38, s40, s38
	v_fma_f32 v129, -v103, v128, 1.0
	v_fmac_f32_e32 v128, v129, v128
	v_div_scale_f32 v129, vcc, 1.0, v102, 1.0
	v_mul_f32_e32 v130, v129, v128
	v_fma_f32 v131, -v103, v130, v129
	v_fmac_f32_e32 v130, v131, v128
	v_fma_f32 v103, -v103, v130, v129
	v_div_fmas_f32 v103, v103, v128, v130
	v_div_fixup_f32 v102, v103, v102, 1.0
	v_pk_mul_f32 v[114:115], v[114:115], v[102:103] op_sel_hi:[1,0]
	v_pk_mul_f32 v[112:113], v[112:113], v[102:103] op_sel_hi:[1,0]
	v_pk_fma_f32 v[114:115], v[124:125], v[114:115], v[120:121]
	v_pk_fma_f32 v[112:113], v[126:127], v[112:113], v[122:123]
	v_cvt_pk_bf16_f32 v124, v114, v115
	s_addc_u32 s39, s44, s39
	v_lshlrev_b32_e32 v103, 16, v124
	v_sub_f32_e32 v103, v114, v103
	v_and_b32_e32 v120, 0xffff0000, v124
	v_cvt_pk_bf16_f32 v125, v112, v113
	v_sub_f32_e32 v120, v115, v120
	v_cvt_pk_bf16_f32 v126, v103, v120
	v_mov_b32_e32 v103, 0
	v_cvt_pk_fp8_f32 v103, v114, v115
	v_lshlrev_b32_e32 v121, 16, v125
	v_and_b32_e32 v122, 0xffff0000, v125
	v_sub_f32_e32 v121, v112, v121
	v_cvt_pk_fp8_f32 v103, v112, v113 op_sel:[0,0,1]
	v_sub_f32_e32 v122, v113, v122
	v_cvt_pk_bf16_f32 v127, v121, v122
	v_and_b32_e32 v130, 0x1f0, v146
	global_store_dword v150, v103, s[38:39] nt
	global_load_dwordx4 v[112:115], v[118:119], off offset:1024
	global_load_dwordx4 v[120:123], v[116:117], off offset:1024
	v_mov_b32_e32 v103, 0x1f0
	v_bitop3_b32 v128, s5, v146, v103 bitop3:0x78
	v_and_b32_e32 v103, 8, v146
	v_pk_mul_f32 v[110:111], v[110:111], v[102:103] op_sel_hi:[1,0]
	v_pk_mul_f32 v[108:109], v[108:109], v[102:103] op_sel_hi:[1,0]
	v_add3_u32 v159, s0, v128, v103
	v_add_u32_e32 v160, 0x10000, v159
	ds_write_b64 v159, v[124:125]
	ds_write_b64 v160, v[126:127]
	v_pk_mul_f32 v[106:107], v[106:107], v[102:103] op_sel_hi:[1,0]
	v_pk_mul_f32 v[104:105], v[104:105], v[102:103] op_sel_hi:[1,0]
	v_mov_b32_e32 v124, 0x200
	v_bitop3_b32 v124, v130, s5, v124 bitop3:0x36
	v_add3_u32 v161, s0, v124, v103
	v_add_u32_e32 v162, 0x10000, v161
	v_pk_mul_f32 v[72:73], v[72:73], v[102:103] op_sel_hi:[1,0]
	v_pk_mul_f32 v[70:71], v[70:71], v[102:103] op_sel_hi:[1,0]
	v_pk_mul_f32 v[68:69], v[68:69], v[102:103] op_sel_hi:[1,0]
	v_pk_mul_f32 v[66:67], v[66:67], v[102:103] op_sel_hi:[1,0]
	v_and_b32_e32 v125, 0xffff0000, v88
	v_and_b32_e32 v124, 0xffff0000, v86
	v_pk_mul_f32 v[100:101], v[100:101], v[102:103] op_sel_hi:[1,0]
	v_pk_mul_f32 v[98:99], v[98:99], v[102:103] op_sel_hi:[1,0]
	v_pk_mul_f32 v[96:97], v[96:97], v[102:103] op_sel_hi:[1,0]
	v_pk_mul_f32 v[94:95], v[94:95], v[102:103] op_sel_hi:[1,0]
	v_pk_mul_f32 v[92:93], v[92:93], v[102:103] op_sel_hi:[1,0]
	v_pk_mul_f32 v[90:91], v[90:91], v[102:103] op_sel_hi:[1,0]
	s_waitcnt vmcnt(1)
	v_pk_add_f32 v[114:115], v[114:115], 1.0 op_sel_hi:[1,0]
	v_pk_add_f32 v[112:113], v[112:113], 1.0 op_sel_hi:[1,0]
	s_waitcnt vmcnt(0)
	v_pk_fma_f32 v[108:109], v[114:115], v[108:109], v[122:123]
	v_pk_fma_f32 v[110:111], v[112:113], v[110:111], v[120:121]
	v_mov_b32_e32 v114, 0
	v_cvt_pk_fp8_f32 v114, v110, v111
	v_cvt_pk_bf16_f32 v120, v110, v111
	v_cvt_pk_bf16_f32 v121, v108, v109
	v_cvt_pk_fp8_f32 v114, v108, v109 op_sel:[0,0,1]
	v_lshlrev_b32_e32 v112, 16, v120
	v_and_b32_e32 v113, 0xffff0000, v120
	v_sub_f32_e32 v112, v110, v112
	v_sub_f32_e32 v113, v111, v113
	v_lshlrev_b32_e32 v110, 16, v121
	v_and_b32_e32 v111, 0xffff0000, v121
	v_sub_f32_e32 v110, v108, v110
	v_sub_f32_e32 v108, v109, v111
	v_cvt_pk_bf16_f32 v122, v112, v113
	v_cvt_pk_bf16_f32 v123, v110, v108
	global_store_dword v150, v114, s[38:39] offset:256 nt
	global_load_dwordx4 v[108:111], v[118:119], off offset:2048
	s_nop 0
	global_load_dwordx4 v[112:115], v[116:117], off offset:2048
	ds_write_b64 v161, v[120:121]
	ds_write_b64 v162, v[122:123]
	v_mov_b32_e32 v120, 0x400
	v_bitop3_b32 v120, v130, s5, v120 bitop3:0x36
	v_add3_u32 v165, s0, v120, v103
	v_add_u32_e32 v166, 0x10000, v165
	v_lshlrev_b32_e32 v123, 16, v88
	v_lshlrev_b32_e32 v122, 16, v86
	v_and_b32_e32 v121, 0xffff0000, v89
	v_and_b32_e32 v120, 0xffff0000, v87
	v_pk_add_f32 v[136:137], v[122:123], v[124:125]
	v_mov_b32_e32 v88, 0
	s_waitcnt vmcnt(1)
	v_pk_add_f32 v[110:111], v[110:111], 1.0 op_sel_hi:[1,0]
	v_pk_add_f32 v[108:109], v[108:109], 1.0 op_sel_hi:[1,0]
	s_waitcnt vmcnt(0)
	v_pk_fma_f32 v[104:105], v[110:111], v[104:105], v[114:115]
	v_pk_fma_f32 v[106:107], v[108:109], v[106:107], v[112:113]
	v_mov_b32_e32 v110, 0
	v_cvt_pk_fp8_f32 v110, v106, v107
	v_cvt_pk_bf16_f32 v112, v106, v107
	v_cvt_pk_bf16_f32 v113, v104, v105
	v_cvt_pk_fp8_f32 v110, v104, v105 op_sel:[0,0,1]
	v_lshlrev_b32_e32 v108, 16, v112
	v_and_b32_e32 v109, 0xffff0000, v112
	v_sub_f32_e32 v108, v106, v108
	v_sub_f32_e32 v109, v107, v109
	v_lshlrev_b32_e32 v106, 16, v113
	v_and_b32_e32 v107, 0xffff0000, v113
	v_sub_f32_e32 v106, v104, v106
	v_sub_f32_e32 v104, v105, v107
	v_cvt_pk_bf16_f32 v114, v108, v109
	v_cvt_pk_bf16_f32 v115, v106, v104
	global_store_dword v150, v110, s[38:39] offset:512 nt
	global_load_dwordx4 v[104:107], v[118:119], off offset:3072
	s_nop 0
	global_load_dwordx4 v[108:111], v[116:117], off offset:3072
	ds_write_b64 v165, v[112:113]
	ds_write_b64 v166, v[114:115]
	s_waitcnt vmcnt(1)
; #define LAS __attribute__((address_space(3)))
; __device__ __forceinline__ unsigned cvt_pk_bf16(float lo, float hi) { unsigned r; asm volatile("v_cvt_pk_bf16_f32 %0, %1, %2" : "=v"(r) : "v"(lo), "v"(hi)); return r; }
; __device__ __forceinline__ unsigned pk4_fp8(float a, float b, float c, float d) { int w = 0; w = __builtin_amdgcn_cvt_pk_fp8_f32(a, b, w, false); w = __builtin_amdgcn_cvt_pk_fp8_f32(c, d, w, true); return (unsigned)w; }
; __device__ __forceinline__ float bf_lo(unsigned w) { return __uint_as_float(w << 16); }
; __device__ __forceinline__ float bf_hi(unsigned w) { return __uint_as_float(w & 0xffff0000u); }
; __device__ __forceinline__ void p6_router(Frame& F) {
;     ...
;                 for (int j = 0; j < 8; ++j) { const u32x2 zb = zr[q][j]; v[j] = (f32x4){bf_lo(zb.x), bf_hi(zb.x), bf_lo(zb.y), bf_hi(zb.y)}; s += (v[j][0] + v[j][1]) + (v[j][2] + v[j][3]); }
;     ...
;                 for (int j = 0; j < 8; ++j) { const f32x4 sh = ((const f32x4*)(mod + (size_t)b * 12288 + 6144))[loq + 64 * j], sc = ((const f32x4*)(mod + (size_t)b * 12288 + 8192))[loq + 64 * j];
;                     const f32x4 y = v[j] * rstd * (sc + 1.0f) + sh;
;                     u32x2 wh; wh.x = cvt_pk_bf16(y[0], y[1]); wh.y = cvt_pk_bf16(y[2], y[3]);
;                     const f32x4 yl = {y[0] - bf_lo(wh.x), y[1] - bf_hi(wh.x), y[2] - bf_lo(wh.y), y[3] - bf_hi(wh.y)};
;                     u32x2 wl; wl.x = cvt_pk_bf16(yl[0], yl[1]); wl.y = cvt_pk_bf16(yl[2], yl[3]);
;                     { const int r = 2 * wave + q; LAS unsigned char* rowp = F.lds + r * 4096 + ((((lane >> 1) + 32 * j) ^ r) << 4) + (lane & 1) * 8;
;                       *(LAS u32x2*)rowp = wh; *(LAS u32x2*)(rowp + 65536) = wl; }
;                     U2F[(size_t)t * (DM / 4) + lane + 64 * j] = pk4_fp8(y[0], y[1], y[2], y[3]); }
	v_pk_add_f32 v[106:107], v[106:107], 1.0 op_sel_hi:[1,0]
	v_pk_add_f32 v[104:105], v[104:105], 1.0 op_sel_hi:[1,0]
	s_waitcnt vmcnt(0)
	v_pk_fma_f32 v[70:71], v[70:71], v[106:107], v[110:111]
	v_pk_fma_f32 v[72:73], v[72:73], v[104:105], v[108:109]
	v_mov_b32_e32 v106, 0
	v_cvt_pk_fp8_f32 v106, v72, v73
	v_cvt_pk_bf16_f32 v112, v72, v73
	v_cvt_pk_bf16_f32 v113, v70, v71
	v_cvt_pk_fp8_f32 v106, v70, v71 op_sel:[0,0,1]
	v_lshlrev_b32_e32 v104, 16, v112
	v_sub_f32_e32 v104, v72, v104
	v_and_b32_e32 v105, 0xffff0000, v112
	v_sub_f32_e32 v105, v73, v105
	v_cvt_pk_bf16_f32 v114, v104, v105
	v_add_co_u32_e32 v104, vcc, s41, v118
	v_lshlrev_b32_e32 v72, 16, v113
	v_and_b32_e32 v73, 0xffff0000, v113
	v_addc_co_u32_e32 v105, vcc, 0, v119, vcc
	v_sub_f32_e32 v72, v70, v72
	v_sub_f32_e32 v70, v71, v73
	v_cvt_pk_bf16_f32 v115, v72, v70
	global_store_dword v150, v106, s[38:39] offset:768 nt
	v_add_co_u32_e32 v106, vcc, s41, v116
	global_load_dwordx4 v[70:73], v[104:105], off
	s_nop 0
	v_addc_co_u32_e32 v107, vcc, 0, v117, vcc
	global_load_dwordx4 v[108:111], v[106:107], off
	v_mov_b32_e32 v117, 0
	v_mov_b32_e32 v116, 0x600
	v_bitop3_b32 v116, v130, s5, v116 bitop3:0x36
	v_add3_u32 v155, s0, v116, v103
	v_add_u32_e32 v156, 0x10000, v155
	ds_write_b64 v155, v[112:113]
	ds_write_b64 v156, v[114:115]
	v_lshlrev_b32_e32 v119, 16, v89
	v_lshlrev_b32_e32 v118, 16, v87
	v_lshlrev_b32_e32 v116, 16, v84
	v_lshlrev_b32_e32 v112, 16, v82
	v_and_b32_e32 v113, 0xffff0000, v82
	v_lshlrev_b32_e32 v114, 16, v83
	v_and_b32_e32 v115, 0xffff0000, v83
	v_and_b32_e32 v89, 0xffff0000, v80
	v_and_b32_e32 v87, 0xffff0000, v81
	v_lshlrev_b32_e32 v82, 16, v77
	v_and_b32_e32 v83, 0xffff0000, v77
	v_pk_add_f32 v[138:139], v[118:119], v[120:121]
	v_lshlrev_b32_e32 v84, 16, v78
	v_and_b32_e32 v77, 0xffff0000, v74
	v_pk_add_f32 v[136:137], v[136:137], v[138:139]
	v_add_f32_e32 v86, v114, v115
	s_waitcnt vmcnt(1)
	v_pk_add_f32 v[70:71], v[70:71], 1.0 op_sel_hi:[1,0]
	v_pk_add_f32 v[72:73], v[72:73], 1.0 op_sel_hi:[1,0]
	s_waitcnt vmcnt(0)
	v_pk_fma_f32 v[68:69], v[68:69], v[70:71], v[108:109]
	s_nop 0
	v_cvt_pk_fp8_f32 v117, v68, v69
	v_pk_fma_f32 v[66:67], v[66:67], v[72:73], v[110:111]
	v_cvt_pk_bf16_f32 v126, v68, v69
	v_lshlrev_b32_e32 v111, 16, v80
	v_cvt_pk_fp8_f32 v117, v66, v67 op_sel:[0,0,1]
	v_cvt_pk_bf16_f32 v127, v66, v67
	v_lshlrev_b32_e32 v70, 16, v126
	v_and_b32_e32 v71, 0xffff0000, v126
	v_lshlrev_b32_e32 v72, 16, v127
	v_and_b32_e32 v73, 0xffff0000, v127
	v_sub_f32_e32 v68, v68, v70
	v_sub_f32_e32 v69, v69, v71
	v_sub_f32_e32 v70, v66, v72
	v_sub_f32_e32 v66, v67, v73
	v_cvt_pk_bf16_f32 v128, v68, v69
	v_cvt_pk_bf16_f32 v129, v70, v66
	global_store_dword v150, v117, s[38:39] offset:1024 nt
	global_load_dwordx4 v[70:73], v[104:105], off offset:1024
	global_load_dwordx4 v[66:69], v[106:107], off offset:1024
	v_lshlrev_b32_e32 v117, 16, v85
	v_lshlrev_b32_e32 v109, 16, v81
	v_lshlrev_b32_e32 v80, 16, v76
	v_and_b32_e32 v81, 0xffff0000, v76
	v_lshlrev_b32_e32 v85, 16, v79
	v_lshlrev_b32_e32 v76, 16, v74
	v_lshlrev_b32_e32 v79, 16, v75
	v_and_b32_e32 v75, 0xffff0000, v75
	v_pk_add_f32 v[140:141], v[116:117], v[132:133]
	v_add_f32_e32 v78, v80, v81
	v_add_f32_e32 v74, v82, v83
	v_pk_add_f32 v[138:139], v[140:141], v[140:141] op_sel:[0,1] op_sel_hi:[1,0]
	v_pk_add_f32 v[168:169], v[78:79], v[74:75]
	v_add_f32_e32 v74, 0, v136
	v_add_f32_e32 v108, v112, v113
	v_mov_b32_e32 v139, v89
	v_add_f32_e32 v110, v74, v137
	v_pk_add_f32 v[140:141], v[108:109], v[86:87]
	v_pk_add_f32 v[136:137], v[110:111], v[138:139]
	v_pk_add_f32 v[152:153], v[84:85], v[134:135]
	v_pk_add_f32 v[136:137], v[136:137], v[140:141]
	v_pk_add_f32 v[152:153], v[152:153], v[152:153] op_sel:[0,1] op_sel_hi:[1,0]
	v_pk_add_f32 v[136:137], v[136:137], v[136:137] op_sel:[0,1] op_sel_hi:[1,0]
	v_mov_b32_e32 v153, v77
	v_mov_b32_e32 v137, v76
	v_pk_add_f32 v[136:137], v[136:137], v[152:153]
	v_mov_b32_e32 v86, 0x800
	v_pk_add_f32 v[136:137], v[136:137], v[168:169]
	v_bitop3_b32 v86, v130, s5, v86 bitop3:0x36
	v_add_f32_e32 v74, v136, v137
	ds_bpermute_b32 v78, v1, v74
	v_add3_u32 v169, s0, v86, v103
	v_add_u32_e32 v171, 0x10000, v169
	ds_write_b64 v169, v[126:127]
	ds_write_b64 v171, v[128:129]
	s_waitcnt lgkmcnt(2)
	v_add_f32_e32 v74, v74, v78
	ds_bpermute_b32 v78, v142, v74
	s_waitcnt lgkmcnt(0)
	v_add_f32_e32 v74, v74, v78
	ds_bpermute_b32 v78, v143, v74
	s_waitcnt lgkmcnt(0)
	v_add_f32_e32 v74, v74, v78
	s_waitcnt vmcnt(1)
	v_pk_add_f32 v[70:71], v[70:71], 1.0 op_sel_hi:[1,0]
	s_waitcnt vmcnt(0)
	v_pk_fma_f32 v[66:67], v[100:101], v[70:71], v[66:67]
	v_pk_add_f32 v[72:73], v[72:73], 1.0 op_sel_hi:[1,0]
	v_cvt_pk_fp8_f32 v88, v66, v67
	v_pk_fma_f32 v[68:69], v[98:99], v[72:73], v[68:69]
	v_cvt_pk_bf16_f32 v72, v66, v67
	s_nop 0
	v_cvt_pk_fp8_f32 v88, v68, v69 op_sel:[0,0,1]
	v_cvt_pk_bf16_f32 v73, v68, v69
	v_lshlrev_b32_e32 v70, 16, v72
	v_and_b32_e32 v71, 0xffff0000, v72
	v_lshlrev_b32_e32 v78, 16, v73
	v_and_b32_e32 v86, 0xffff0000, v73
	v_sub_f32_e32 v66, v66, v70
	v_sub_f32_e32 v67, v67, v71
	v_sub_f32_e32 v70, v68, v78
	v_sub_f32_e32 v68, v69, v86
	v_cvt_pk_bf16_f32 v126, v66, v67
	v_cvt_pk_bf16_f32 v127, v70, v68
	global_store_dword v150, v88, s[38:39] offset:1280 nt
	global_load_dwordx4 v[68:71], v[104:105], off offset:2048
	global_load_dwordx4 v[98:101], v[106:107], off offset:2048
	ds_bpermute_b32 v66, v144, v74
	v_mov_b32_e32 v86, 0
	s_waitcnt lgkmcnt(0)
	v_add_f32_e32 v66, v74, v66
	ds_bpermute_b32 v67, v145, v66
	v_mov_b32_e32 v74, 0xa00
	v_bitop3_b32 v74, v130, s5, v74 bitop3:0x36
	v_add3_u32 v152, s0, v74, v103
	v_add_u32_e32 v153, 0x10000, v152
	s_waitcnt lgkmcnt(0)
; #define LAS __attribute__((address_space(3)))
; __device__ __forceinline__ unsigned cvt_pk_bf16(float lo, float hi) { unsigned r; asm volatile("v_cvt_pk_bf16_f32 %0, %1, %2" : "=v"(r) : "v"(lo), "v"(hi)); return r; }
; __device__ __forceinline__ unsigned pk4_fp8(float a, float b, float c, float d) { int w = 0; w = __builtin_amdgcn_cvt_pk_fp8_f32(a, b, w, false); w = __builtin_amdgcn_cvt_pk_fp8_f32(c, d, w, true); return (unsigned)w; }
; __device__ __forceinline__ float bf_lo(unsigned w) { return __uint_as_float(w << 16); }
; __device__ __forceinline__ float bf_hi(unsigned w) { return __uint_as_float(w & 0xffff0000u); }
; __device__ __forceinline__ void p6_router(Frame& F) {
;     ...
;                 float mean = wave_sum(s) * (1.f / DM), s2 = 0.f;
; #pragma unroll
;                 for (int j = 0; j < 8; ++j) { v[j] = v[j] - mean; s2 += (v[j][0] * v[j][0] + v[j][1] * v[j][1]) + (v[j][2] * v[j][2] + v[j][3] * v[j][3]); }
;                 float rstd = 1.f / sqrtf(wave_sum(s2) * (1.f / DM) + LN_EPS);
;     ...
;                 for (int j = 0; j < 8; ++j) { const f32x4 sh = ((const f32x4*)(mod + (size_t)b * 12288 + 6144))[loq + 64 * j], sc = ((const f32x4*)(mod + (size_t)b * 12288 + 8192))[loq + 64 * j];
;                     const f32x4 y = v[j] * rstd * (sc + 1.0f) + sh;
;                     u32x2 wh; wh.x = cvt_pk_bf16(y[0], y[1]); wh.y = cvt_pk_bf16(y[2], y[3]);
;                     const f32x4 yl = {y[0] - bf_lo(wh.x), y[1] - bf_hi(wh.x), y[2] - bf_lo(wh.y), y[3] - bf_hi(wh.y)};
;                     u32x2 wl; wl.x = cvt_pk_bf16(yl[0], yl[1]); wl.y = cvt_pk_bf16(yl[2], yl[3]);
;                     { const int r = 2 * wave + q; LAS unsigned char* rowp = F.lds + r * 4096 + ((((lane >> 1) + 32 * j) ^ r) << 4) + (lane & 1) * 8;
;                       *(LAS u32x2*)rowp = wh; *(LAS u32x2*)(rowp + 65536) = wl; }
;                     U2F[(size_t)t * (DM / 4) + lane + 64 * j] = pk4_fp8(y[0], y[1], y[2], y[3]); }
	v_add_f32_e32 v66, v66, v67
	ds_bpermute_b32 v67, v147, v66
	ds_write_b64 v152, v[72:73]
	ds_write_b64 v153, v[126:127]
	s_waitcnt lgkmcnt(2)
	v_add_f32_e32 v88, v66, v67
	v_fmac_f32_e32 v112, 0xba000000, v88
	v_fmac_f32_e32 v114, 0xba000000, v88
	v_fmac_f32_e32 v113, 0xba000000, v88
	v_fmac_f32_e32 v115, 0xba000000, v88
	v_mul_f32_e32 v74, v112, v112
	v_mul_f32_e32 v78, v114, v114
	v_pk_fma_f32 v[140:141], v[112:113], v[112:113], v[74:75] op_sel_hi:[1,1,0]
	v_pk_fma_f32 v[172:173], v[114:115], v[114:115], v[78:79] op_sel_hi:[1,1,0]
	v_fmac_f32_e32 v120, 0xba000000, v88
	v_fmac_f32_e32 v124, 0xba000000, v88
	v_fmac_f32_e32 v121, 0xba000000, v88
	v_fmac_f32_e32 v125, 0xba000000, v88
	v_fmac_f32_e32 v132, 0xba000000, v88
	v_fmac_f32_e32 v133, 0xba000000, v88
	v_fmac_f32_e32 v117, 0xba000000, v88
	v_fmac_f32_e32 v118, 0xba000000, v88
	v_fmac_f32_e32 v122, 0xba000000, v88
	v_fmac_f32_e32 v119, 0xba000000, v88
	v_fmac_f32_e32 v123, 0xba000000, v88
	v_fmac_f32_e32 v116, 0xba000000, v88
	v_fmac_f32_e32 v134, 0xba000000, v88
	v_fmac_f32_e32 v135, 0xba000000, v88
	v_fmac_f32_e32 v85, 0xba000000, v88
	v_pk_mul_f32 v[128:129], v[124:125], v[124:125]
	v_pk_mul_f32 v[136:137], v[120:121], v[120:121]
	v_mov_b32_e32 v138, v117
	v_mov_b32_e32 v139, v133
	v_mov_b32_e32 v117, v132
	v_mov_b32_e32 v66, v85
	v_mov_b32_e32 v67, v135
	v_mov_b32_e32 v85, v134
	v_pk_fma_f32 v[128:129], v[122:123], v[122:123], v[128:129]
	v_pk_fma_f32 v[132:133], v[118:119], v[118:119], v[136:137]
	v_pk_mul_f32 v[134:135], v[138:139], v[138:139]
	v_pk_mul_f32 v[136:137], v[116:117], v[116:117]
	v_pk_add_f32 v[128:129], v[128:129], v[132:133]
	v_pk_mov_b32 v[132:133], v[136:137], v[134:135] op_sel:[1,0]
	v_mov_b32_e32 v137, v135
	v_pk_add_f32 v[132:133], v[132:133], v[136:137]
	v_fmac_f32_e32 v87, 0xba000000, v88
	v_fmac_f32_e32 v109, 0xba000000, v88
	v_fmac_f32_e32 v89, 0xba000000, v88
	v_fmac_f32_e32 v111, 0xba000000, v88
	v_fmac_f32_e32 v84, 0xba000000, v88
	v_pk_add_f32 v[128:129], v[128:129], v[128:129] op_sel_hi:[0,1]
	v_pk_add_f32 v[132:133], v[132:133], v[132:133] op_sel_hi:[0,1]
	v_pk_mul_f32 v[174:175], v[66:67], v[66:67]
	v_pk_mul_f32 v[176:177], v[84:85], v[84:85]
	v_mul_f32_e32 v140, v111, v111
	v_mul_f32_e32 v172, v89, v89
	v_mul_f32_e32 v128, v87, v87
	v_mul_f32_e32 v132, v109, v109
	v_fmac_f32_e32 v80, 0xba000000, v88
	v_pk_mov_b32 v[134:135], v[176:177], v[174:175] op_sel:[1,0]
	v_pk_add_f32 v[136:137], v[140:141], v[172:173]
	v_pk_add_f32 v[128:129], v[132:133], v[128:129]
	v_mov_b32_e32 v177, v175
	v_fmac_f32_e32 v81, 0xba000000, v88
	v_fmac_f32_e32 v82, 0xba000000, v88
	v_pk_add_f32 v[128:129], v[136:137], v[128:129]
	s_waitcnt vmcnt(1)
	v_pk_add_f32 v[68:69], v[68:69], 1.0 op_sel_hi:[1,0]
	v_pk_add_f32 v[70:71], v[70:71], 1.0 op_sel_hi:[1,0]
	s_waitcnt vmcnt(0)
	v_pk_fma_f32 v[68:69], v[96:97], v[68:69], v[98:99]
	v_pk_fma_f32 v[70:71], v[94:95], v[70:71], v[100:101]
	v_cvt_pk_fp8_f32 v86, v68, v69
	v_cvt_pk_bf16_f32 v72, v68, v69
	v_cvt_pk_bf16_f32 v73, v70, v71
	v_pk_add_f32 v[100:101], v[134:135], v[176:177]
	v_cvt_pk_fp8_f32 v86, v70, v71 op_sel:[0,0,1]
	v_lshlrev_b32_e32 v74, 16, v72
	v_and_b32_e32 v78, 0xffff0000, v72
	v_lshlrev_b32_e32 v94, 16, v73
	v_and_b32_e32 v95, 0xffff0000, v73
	v_sub_f32_e32 v68, v68, v74
	v_sub_f32_e32 v69, v69, v78
	v_sub_f32_e32 v74, v70, v94
	v_sub_f32_e32 v70, v71, v95
	v_cvt_pk_bf16_f32 v98, v68, v69
	v_cvt_pk_bf16_f32 v99, v74, v70
	global_store_dword v150, v86, s[38:39] offset:1536 nt
	global_load_dwordx4 v[68:71], v[106:107], off offset:3072
	global_load_dwordx4 v[94:97], v[104:105], off offset:3072
	v_mul_f32_e32 v74, v80, v80
	v_fmac_f32_e32 v83, 0xba000000, v88
	v_pk_fma_f32 v[104:105], v[80:81], v[80:81], v[74:75] op_sel_hi:[1,1,0]
	v_mul_f32_e32 v74, v82, v82
	v_pk_add_f32 v[128:129], v[128:129], v[128:129] op_sel_hi:[0,1]
	v_pk_add_f32 v[100:101], v[100:101], v[100:101] op_sel_hi:[0,1]
	v_pk_fma_f32 v[106:107], v[82:83], v[82:83], v[74:75] op_sel_hi:[1,1,0]
	v_fmac_f32_e32 v75, 0xba000000, v88
	v_fmac_f32_e32 v79, 0xba000000, v88
	v_fmac_f32_e32 v77, 0xba000000, v88
	v_fmac_f32_e32 v76, 0xba000000, v88
	v_mul_f32_e32 v104, v76, v76
	v_mul_f32_e32 v106, v77, v77
	v_mul_f32_e32 v100, v79, v79
	v_mul_f32_e32 v128, v75, v75
	v_pk_add_f32 v[104:105], v[104:105], v[106:107]
	v_pk_add_f32 v[100:101], v[100:101], v[128:129]
	v_mov_b32_e32 v86, 0xc00
	v_pk_add_f32 v[100:101], v[104:105], v[100:101]
	v_mov_b32_e32 v88, 0xe00
	v_add_f32_e32 v74, v100, v101
	ds_bpermute_b32 v78, v1, v74
	v_bitop3_b32 v86, v130, s5, v86 bitop3:0x36
	v_bitop3_b32 v88, v130, s5, v88 bitop3:0x36
	v_add3_u32 v163, s0, v86, v103
	v_add3_u32 v157, s0, v88, v103
	s_waitcnt lgkmcnt(0)
	v_add_f32_e32 v74, v74, v78
	ds_bpermute_b32 v78, v142, v74
	v_add_u32_e32 v164, 0x10000, v163
	ds_write_b64 v163, v[72:73]
	ds_write_b64 v164, v[98:99]
	v_mov_b32_e32 v105, 0
	v_add_u32_e32 v158, 0x10000, v157
	s_waitcnt lgkmcnt(2)
	v_add_f32_e32 v74, v74, v78
	ds_bpermute_b32 v78, v143, v74
	v_mov_b32_e32 v100, v123
	v_mov_b32_e32 v123, v124
	v_mov_b32_e32 v101, v125
	v_mov_b32_e32 v104, v119
	s_waitcnt lgkmcnt(0)
	v_add_f32_e32 v74, v74, v78
	ds_bpermute_b32 v78, v144, v74
	v_mov_b32_e32 v119, v120
	s_waitcnt lgkmcnt(0)
	v_add_f32_e32 v74, v74, v78
	ds_bpermute_b32 v78, v145, v74
	s_waitcnt lgkmcnt(0)
	v_add_f32_e32 v74, v74, v78
	ds_bpermute_b32 v78, v147, v74
	s_waitcnt lgkmcnt(0)
	v_add_f32_e32 v74, v74, v78
	v_fmamk_f32 v74, v74, 0x3a000000, v148
	v_mul_f32_e32 v78, 0x4f800000, v74
	v_cmp_gt_f32_e32 vcc, s45, v74
	s_waitcnt vmcnt(0)
; __device__ __forceinline__ unsigned cvt_pk_bf16(float lo, float hi) { unsigned r; asm volatile("v_cvt_pk_bf16_f32 %0, %1, %2" : "=v"(r) : "v"(lo), "v"(hi)); return r; }
; __device__ __forceinline__ void p6_router(Frame& F) {
;     ...
;                 float rstd = 1.f / sqrtf(wave_sum(s2) * (1.f / DM) + LN_EPS);
;                 s = 0.f;
; #pragma unroll
;                 for (int j = 0; j < 8; ++j) { v[j] = v[j] * rstd * pw[j] + pb[j]; { u32x2 xb; xb.x = cvt_pk_bf16(v[j][0], v[j][1]); xb.y = cvt_pk_bf16(v[j][2], v[j][3]); ((u32x2*)(X1 + (size_t)t * DM))[lane + 64 * j] = xb; } s += (v[j][0] + v[j][1]) + (v[j][2] + v[j][3]); }
	v_pk_add_f32 v[72:73], v[96:97], 1.0 op_sel_hi:[1,0]
	v_cndmask_b32_e32 v74, v74, v78, vcc
	v_sqrt_f32_e32 v78, v74
	v_pk_add_f32 v[94:95], v[94:95], 1.0 op_sel_hi:[1,0]
	v_pk_fma_f32 v[70:71], v[90:91], v[72:73], v[70:71]
	v_pk_fma_f32 v[68:69], v[92:93], v[94:95], v[68:69]
	v_add_u32_e32 v86, -1, v78
	v_add_u32_e32 v88, 1, v78
	v_fma_f32 v106, -v86, v78, v74
	v_fma_f32 v107, -v88, v78, v74
	v_cmp_ge_f32_e64 s[0:1], 0, v106
	v_cvt_pk_bf16_f32 v72, v68, v69
	v_cvt_pk_fp8_f32 v105, v68, v69
	v_cvt_pk_bf16_f32 v73, v70, v71
	v_cvt_pk_fp8_f32 v105, v70, v71 op_sel:[0,0,1]
	v_cndmask_b32_e64 v78, v78, v86, s[0:1]
	v_cmp_lt_f32_e64 s[0:1], 0, v107
	v_lshlrev_b32_e32 v90, 16, v73
	v_and_b32_e32 v91, 0xffff0000, v73
	v_cndmask_b32_e64 v78, v78, v88, s[0:1]
	v_mul_f32_e32 v86, 0x37800000, v78
	v_cndmask_b32_e32 v78, v78, v86, vcc
	v_lshlrev_b32_e32 v86, 16, v72
	v_and_b32_e32 v88, 0xffff0000, v72
	v_sub_f32_e32 v68, v68, v86
	v_sub_f32_e32 v69, v69, v88
	v_cvt_pk_bf16_f32 v68, v68, v69
	v_cmp_class_f32_e32 vcc, v74, v149
	v_sub_f32_e32 v86, v70, v90
	v_sub_f32_e32 v88, v71, v91
	v_cvt_pk_bf16_f32 v69, v86, v88
	ds_write_b64 v157, v[72:73]
	ds_write_b64 v158, v[68:69]
	v_cndmask_b32_e32 v68, v78, v74, vcc
	v_div_scale_f32 v69, s[0:1], v68, v68, 1.0
	v_rcp_f32_e32 v70, v69
	global_store_dword v150, v105, s[38:39] offset:1792 nt
	v_mov_b32_e32 v105, v121
	v_mov_b32_e32 v88, v111
	v_fma_f32 v71, -v69, v70, 1.0
	v_fmac_f32_e32 v70, v71, v70
	v_div_scale_f32 v71, vcc, 1.0, v68, 1.0
	v_mul_f32_e32 v72, v71, v70
	v_fma_f32 v73, -v69, v72, v71
	v_fmac_f32_e32 v72, v73, v70
	v_fma_f32 v69, -v69, v72, v71
	v_div_fmas_f32 v69, v69, v70, v72
	v_div_fixup_f32 v68, v69, v68, 1.0
	v_pk_mul_f32 v[70:71], v[122:123], v[68:69] op_sel_hi:[1,0]
	v_pk_mul_f32 v[72:73], v[118:119], v[68:69] op_sel_hi:[1,0]
	v_pk_fma_f32 v[62:63], v[2:3], v[70:71], v[62:63]
	v_pk_mul_f32 v[2:3], v[100:101], v[68:69] op_sel_hi:[1,0]
	v_pk_fma_f32 v[64:65], v[4:5], v[72:73], v[64:65]
	v_pk_mul_f32 v[4:5], v[104:105], v[68:69] op_sel_hi:[1,0]
	v_pk_fma_f32 v[54:55], v[54:55], v[2:3], v[58:59]
	v_pk_fma_f32 v[56:57], v[56:57], v[4:5], v[60:61]
	v_mov_b32_e32 v2, v54
	v_mov_b32_e32 v3, v62
	v_mov_b32_e32 v4, v55
	v_mov_b32_e32 v5, v63
	v_pk_add_f32 v[2:3], v[2:3], v[4:5]
	v_mov_b32_e32 v4, v57
	v_mov_b32_e32 v5, v65
	v_mov_b32_e32 v58, v56
	v_mov_b32_e32 v59, v64
	v_pk_add_f32 v[4:5], v[4:5], v[58:59]
	v_pk_mul_f32 v[58:59], v[138:139], v[68:69] op_sel_hi:[1,0]
	v_pk_add_f32 v[2:3], v[2:3], v[4:5]
	v_pk_mul_f32 v[4:5], v[116:117], v[68:69] op_sel_hi:[1,0]
	v_pk_fma_f32 v[48:49], v[48:49], v[58:59], v[52:53]
	v_pk_fma_f32 v[46:47], v[46:47], v[4:5], v[50:51]
	v_mov_b32_e32 v5, v49
	v_mov_b32_e32 v4, v46
	v_pk_mov_b32 v[50:51], v[46:47], v[48:49] op_sel:[1,0]
	v_pk_mul_f32 v[52:53], v[114:115], v[68:69] op_sel_hi:[1,0]
	v_pk_add_f32 v[4:5], v[4:5], v[50:51]
	v_pk_mul_f32 v[50:51], v[112:113], v[68:69] op_sel_hi:[1,0]
	v_mov_b32_e32 v86, v109
	v_pk_fma_f32 v[40:41], v[40:41], v[52:53], v[44:45]
	v_pk_fma_f32 v[38:39], v[38:39], v[50:51], v[42:43]
	v_pk_mul_f32 v[50:51], v[88:89], v[68:69] op_sel_hi:[1,0]
	v_pk_mul_f32 v[52:53], v[86:87], v[68:69] op_sel_hi:[1,0]
	v_add_f32_e32 v3, 0, v3
	v_pk_add_f32 v[4:5], v[4:5], v[4:5] op_sel_hi:[0,1]
	v_pk_fma_f32 v[32:33], v[32:33], v[52:53], v[36:37]
	v_pk_fma_f32 v[30:31], v[30:31], v[50:51], v[34:35]
	v_add_f32_e32 v3, v2, v3
	v_add_f32_e32 v43, v38, v39
	v_add_f32_e32 v45, v41, v40
	v_mov_b32_e32 v42, v30
	v_mov_b32_e32 v44, v31
	v_mov_b32_e32 v4, v33
	v_mov_b32_e32 v2, v32
	v_pk_add_f32 v[34:35], v[42:43], v[44:45]
	v_pk_add_f32 v[2:3], v[4:5], v[2:3]
	v_pk_mul_f32 v[4:5], v[66:67], v[68:69] op_sel_hi:[1,0]
	v_pk_add_f32 v[2:3], v[34:35], v[2:3]
	v_pk_fma_f32 v[24:25], v[24:25], v[4:5], v[28:29]
	v_pk_add_f32 v[34:35], v[2:3], v[2:3] op_sel_hi:[0,1]
	v_pk_mul_f32 v[2:3], v[84:85], v[68:69] op_sel_hi:[1,0]
	v_mov_b32_e32 v74, v79
	v_pk_fma_f32 v[22:23], v[22:23], v[2:3], v[26:27]
	v_mov_b32_e32 v3, v25
	v_mov_b32_e32 v2, v22
	v_pk_mov_b32 v[4:5], v[22:23], v[24:25] op_sel:[1,0]
	s_add_u32 s0, s42, s36
	v_pk_add_f32 v[2:3], v[2:3], v[4:5]
	v_pk_mul_f32 v[4:5], v[82:83], v[68:69] op_sel_hi:[1,0]
	v_pk_add_f32 v[26:27], v[2:3], v[2:3] op_sel_hi:[0,1]
	v_pk_mul_f32 v[2:3], v[80:81], v[68:69] op_sel_hi:[1,0]
	v_pk_fma_f32 v[16:17], v[16:17], v[4:5], v[20:21]
	v_pk_fma_f32 v[14:15], v[14:15], v[2:3], v[18:19]
	v_pk_mul_f32 v[4:5], v[76:77], v[68:69] op_sel_hi:[1,0]
	v_pk_mul_f32 v[2:3], v[74:75], v[68:69] op_sel_hi:[1,0]
	v_pk_fma_f32 v[4:5], v[6:7], v[4:5], v[10:11]
	v_pk_fma_f32 v[2:3], v[8:9], v[2:3], v[12:13]
	v_add_f32_e32 v19, v14, v15
	v_add_f32_e32 v21, v17, v16
	v_mov_b32_e32 v18, v4
	v_mov_b32_e32 v20, v5
	v_mov_b32_e32 v26, v3
	v_mov_b32_e32 v34, v2
	v_pk_add_f32 v[6:7], v[18:19], v[20:21]
	v_pk_add_f32 v[8:9], v[26:27], v[34:35]
	s_addc_u32 s1, s43, s37
	v_pk_add_f32 v[6:7], v[6:7], v[8:9]
	v_cvt_pk_bf16_f32 v70, v62, v63
	v_cvt_pk_bf16_f32 v71, v64, v65
	global_store_dwordx2 v146, v[70:71], s[0:1] nt
	v_add_f32_e32 v7, v6, v7
	ds_bpermute_b32 v8, v1, v7
	v_cvt_pk_bf16_f32 v6, v54, v55
	s_mov_b32 s37, 0
	v_mov_b32_e32 v79, 0
	s_waitcnt lgkmcnt(0)
	v_add_f32_e32 v8, v7, v8
	ds_bpermute_b32 v9, v142, v8
	v_cvt_pk_bf16_f32 v7, v56, v57
	global_store_dwordx2 v146, v[6:7], s[0:1] offset:512 nt
	v_cvt_pk_bf16_f32 v6, v46, v47
	v_cvt_pk_bf16_f32 v7, v48, v49
	s_waitcnt lgkmcnt(0)
	v_add_f32_e32 v8, v8, v9
	ds_bpermute_b32 v9, v143, v8
	global_store_dwordx2 v146, v[6:7], s[0:1] offset:1024 nt
	v_cvt_pk_bf16_f32 v6, v38, v39
	v_cvt_pk_bf16_f32 v7, v40, v41
	global_store_dwordx2 v146, v[6:7], s[0:1] offset:1536 nt
	s_waitcnt lgkmcnt(0)
; __device__ __forceinline__ unsigned cvt_pk_bf16(float lo, float hi) { unsigned r; asm volatile("v_cvt_pk_bf16_f32 %0, %1, %2" : "=v"(r) : "v"(lo), "v"(hi)); return r; }
; __device__ __forceinline__ void p6_router(Frame& F) {
;     ...
;                 for (int j = 0; j < 8; ++j) { v[j] = v[j] * rstd * pw[j] + pb[j]; { u32x2 xb; xb.x = cvt_pk_bf16(v[j][0], v[j][1]); xb.y = cvt_pk_bf16(v[j][2], v[j][3]); ((u32x2*)(X1 + (size_t)t * DM))[lane + 64 * j] = xb; } s += (v[j][0] + v[j][1]) + (v[j][2] + v[j][3]); }
;                 mean = wave_sum(s) * (1.f / DM); s2 = 0.f;
; #pragma unroll
;                 for (int j = 0; j < 8; ++j) { v[j] = v[j] - mean; s2 += (v[j][0] * v[j][0] + v[j][1] * v[j][1]) + (v[j][2] * v[j][2] + v[j][3] * v[j][3]); }
;                 rstd = 1.f / sqrtf(wave_sum(s2) * (1.f / DM) + LN_EPS);
	v_add_f32_e32 v8, v8, v9
	ds_bpermute_b32 v9, v144, v8
	v_cvt_pk_bf16_f32 v6, v30, v31
	v_cvt_pk_bf16_f32 v7, v32, v33
	global_store_dwordx2 v146, v[6:7], s[0:1] offset:2048 nt
	v_cvt_pk_bf16_f32 v6, v22, v23
	s_waitcnt lgkmcnt(0)
	v_add_f32_e32 v8, v8, v9
	ds_bpermute_b32 v9, v145, v8
	v_cvt_pk_bf16_f32 v7, v24, v25
	global_store_dwordx2 v146, v[6:7], s[0:1] offset:2560 nt
	v_cvt_pk_bf16_f32 v6, v14, v15
	v_cvt_pk_bf16_f32 v7, v16, v17
	s_waitcnt lgkmcnt(0)
	v_add_f32_e32 v8, v8, v9
	ds_bpermute_b32 v9, v147, v8
	global_store_dwordx2 v146, v[6:7], s[0:1] offset:3072 nt
	v_cvt_pk_bf16_f32 v6, v4, v5
	v_cvt_pk_bf16_f32 v7, v2, v3
	global_store_dwordx2 v146, v[6:7], s[0:1] offset:3584 nt
	s_waitcnt lgkmcnt(0)
	v_add_f32_e32 v18, v8, v9
	v_fmamk_f32 v63, v18, 0xba000000, v63
	v_fmamk_f32 v55, v18, 0xba000000, v55
	v_fmamk_f32 v65, v18, 0xba000000, v65
	v_fmac_f32_e32 v62, 0xba000000, v18
	v_fmamk_f32 v57, v18, 0xba000000, v57
	v_fmac_f32_e32 v54, 0xba000000, v18
	v_mov_b32_e32 v8, v63
	v_mov_b32_e32 v9, v55
	v_fmac_f32_e32 v64, 0xba000000, v18
	v_fmac_f32_e32 v56, 0xba000000, v18
	v_mov_b32_e32 v6, v62
	v_mov_b32_e32 v7, v54
	v_pk_mul_f32 v[8:9], v[8:9], v[8:9]
	v_mov_b32_e32 v10, v65
	v_mov_b32_e32 v11, v57
	v_pk_fma_f32 v[6:7], v[6:7], v[6:7], v[8:9]
	v_mov_b32_e32 v8, v64
	v_mov_b32_e32 v9, v56
	v_pk_mul_f32 v[10:11], v[10:11], v[10:11]
	v_fmamk_f32 v47, v18, 0xba000000, v47
	v_pk_fma_f32 v[8:9], v[8:9], v[8:9], v[10:11]
	v_fmac_f32_e32 v46, 0xba000000, v18
	v_pk_add_f32 v[6:7], v[6:7], v[8:9]
	v_fmamk_f32 v49, v18, 0xba000000, v49
	v_fmac_f32_e32 v48, 0xba000000, v18
	v_pk_add_f32 v[6:7], v[6:7], v[6:7] op_sel_hi:[0,1]
	v_pk_mul_f32 v[8:9], v[48:49], v[48:49]
	v_pk_mul_f32 v[10:11], v[46:47], v[46:47]
	v_fmac_f32_e32 v38, 0xba000000, v18
	v_pk_mov_b32 v[12:13], v[10:11], v[8:9] op_sel:[1,0]
	v_mov_b32_e32 v11, v9
	v_fmamk_f32 v39, v18, 0xba000000, v39
	v_fmac_f32_e32 v40, 0xba000000, v18
	v_mul_f32_e32 v6, v38, v38
	v_pk_add_f32 v[8:9], v[12:13], v[10:11]
	v_fmamk_f32 v41, v18, 0xba000000, v41
	v_pk_fma_f32 v[10:11], v[38:39], v[38:39], v[6:7] op_sel_hi:[1,1,0]
	v_mul_f32_e32 v6, v40, v40
	v_pk_add_f32 v[8:9], v[8:9], v[8:9] op_sel_hi:[0,1]
	v_pk_fma_f32 v[12:13], v[40:41], v[40:41], v[6:7] op_sel_hi:[1,1,0]
	v_fmamk_f32 v33, v18, 0xba000000, v33
	v_fmac_f32_e32 v32, 0xba000000, v18
	v_fmamk_f32 v31, v18, 0xba000000, v31
	v_fmac_f32_e32 v30, 0xba000000, v18
	v_mul_f32_e32 v10, v30, v30
	v_mul_f32_e32 v12, v31, v31
	v_mul_f32_e32 v8, v32, v32
	v_mul_f32_e32 v6, v33, v33
	v_pk_add_f32 v[10:11], v[10:11], v[12:13]
	v_pk_add_f32 v[6:7], v[8:9], v[6:7]
	v_fmamk_f32 v23, v18, 0xba000000, v23
	v_fmac_f32_e32 v22, 0xba000000, v18
	v_fmamk_f32 v25, v18, 0xba000000, v25
	v_fmac_f32_e32 v24, 0xba000000, v18
	v_pk_add_f32 v[6:7], v[10:11], v[6:7]
	v_pk_mul_f32 v[8:9], v[24:25], v[24:25]
	v_pk_mul_f32 v[10:11], v[22:23], v[22:23]
	v_pk_add_f32 v[6:7], v[6:7], v[6:7] op_sel_hi:[0,1]
	v_pk_mov_b32 v[12:13], v[10:11], v[8:9] op_sel:[1,0]
	v_mov_b32_e32 v11, v9
	v_fmac_f32_e32 v14, 0xba000000, v18
	v_pk_add_f32 v[8:9], v[12:13], v[10:11]
	v_fmamk_f32 v15, v18, 0xba000000, v15
	v_fmac_f32_e32 v16, 0xba000000, v18
	v_mul_f32_e32 v6, v14, v14
	v_pk_add_f32 v[12:13], v[8:9], v[8:9] op_sel_hi:[0,1]
	v_fmamk_f32 v17, v18, 0xba000000, v17
	v_pk_fma_f32 v[8:9], v[14:15], v[14:15], v[6:7] op_sel_hi:[1,1,0]
	v_mul_f32_e32 v6, v16, v16
	v_pk_fma_f32 v[10:11], v[16:17], v[16:17], v[6:7] op_sel_hi:[1,1,0]
	v_fmamk_f32 v5, v18, 0xba000000, v5
	v_fmac_f32_e32 v4, 0xba000000, v18
	v_mul_f32_e32 v8, v4, v4
	v_mul_f32_e32 v10, v5, v5
	v_pk_add_f32 v[34:35], v[8:9], v[10:11]
	v_mov_b32_e32 v8, v170
	v_fmamk_f32 v3, v18, 0xba000000, v3
	v_ashrrev_i32_e32 v9, 31, v8
	v_lshlrev_b64 v[10:11], 4, v[8:9]
	v_lshl_add_u64 v[8:9], s[16:17], 0, v[10:11]
	v_fmac_f32_e32 v2, 0xba000000, v18
	v_lshl_add_u64 v[10:11], s[20:21], 0, v[10:11]
	global_load_dwordx4 v[18:21], v[8:9], off
	global_load_dwordx4 v[26:29], v[10:11], off
	v_mul_f32_e32 v12, v2, v2
	v_mul_f32_e32 v6, v3, v3
	v_pk_add_f32 v[6:7], v[12:13], v[6:7]
	s_waitcnt vmcnt(0)
	v_pk_add_f32 v[28:29], v[28:29], 1.0 op_sel_hi:[1,0]
	v_pk_add_f32 v[6:7], v[34:35], v[6:7]
	v_pk_add_f32 v[26:27], v[26:27], 1.0 op_sel_hi:[1,0]
	v_add_f32_e32 v6, v6, v7
	ds_bpermute_b32 v7, v1, v6
	s_waitcnt lgkmcnt(0)
	v_add_f32_e32 v6, v6, v7
	ds_bpermute_b32 v7, v142, v6
	s_waitcnt lgkmcnt(0)
	v_add_f32_e32 v6, v6, v7
	ds_bpermute_b32 v7, v143, v6
	s_waitcnt lgkmcnt(0)
	v_add_f32_e32 v6, v6, v7
	ds_bpermute_b32 v7, v144, v6
	s_waitcnt lgkmcnt(0)
	v_add_f32_e32 v6, v6, v7
	ds_bpermute_b32 v7, v145, v6
	s_waitcnt lgkmcnt(0)
	v_add_f32_e32 v6, v6, v7
	ds_bpermute_b32 v7, v147, v6
	s_waitcnt lgkmcnt(0)
; #define LAS __attribute__((address_space(3)))
; __device__ __forceinline__ unsigned cvt_pk_bf16(float lo, float hi) { unsigned r; asm volatile("v_cvt_pk_bf16_f32 %0, %1, %2" : "=v"(r) : "v"(lo), "v"(hi)); return r; }
; __device__ __forceinline__ unsigned pk4_fp8(float a, float b, float c, float d) { int w = 0; w = __builtin_amdgcn_cvt_pk_fp8_f32(a, b, w, false); w = __builtin_amdgcn_cvt_pk_fp8_f32(c, d, w, true); return (unsigned)w; }
; __device__ __forceinline__ float bf_lo(unsigned w) { return __uint_as_float(w << 16); }
; __device__ __forceinline__ float bf_hi(unsigned w) { return __uint_as_float(w & 0xffff0000u); }
; __device__ __forceinline__ void p6_router(Frame& F) {
;     ...
;                 rstd = 1.f / sqrtf(wave_sum(s2) * (1.f / DM) + LN_EPS);
;                 int loq = lane; asm volatile("" : "+v"(loq));
; #pragma unroll
;                 for (int j = 0; j < 8; ++j) { const f32x4 sh = ((const f32x4*)(mod + (size_t)b * 12288 + 6144))[loq + 64 * j], sc = ((const f32x4*)(mod + (size_t)b * 12288 + 8192))[loq + 64 * j];
;                     const f32x4 y = v[j] * rstd * (sc + 1.0f) + sh;
;                     u32x2 wh; wh.x = cvt_pk_bf16(y[0], y[1]); wh.y = cvt_pk_bf16(y[2], y[3]);
;                     const f32x4 yl = {y[0] - bf_lo(wh.x), y[1] - bf_hi(wh.x), y[2] - bf_lo(wh.y), y[3] - bf_hi(wh.y)};
;                     u32x2 wl; wl.x = cvt_pk_bf16(yl[0], yl[1]); wl.y = cvt_pk_bf16(yl[2], yl[3]);
;                     { const int r = 2 * wave + q; LAS unsigned char* rowp = F.lds + r * 4096 + ((((lane >> 1) + 32 * j) ^ r) << 4) + (lane & 1) * 8;
;                       *(LAS u32x2*)rowp = wh; *(LAS u32x2*)(rowp + 65536) = wl; }
;                     U2F[(size_t)t * (DM / 4) + lane + 64 * j] = pk4_fp8(y[0], y[1], y[2], y[3]); }
	v_add_f32_e32 v6, v6, v7
	v_fmamk_f32 v6, v6, 0x3a000000, v148
	v_mul_f32_e32 v7, 0x4f800000, v6
	v_cmp_gt_f32_e32 vcc, s45, v6
	s_nop 1
	v_cndmask_b32_e32 v6, v6, v7, vcc
	v_sqrt_f32_e32 v7, v6
	s_nop 0
	v_add_u32_e32 v12, -1, v7
	v_fma_f32 v13, -v12, v7, v6
	v_cmp_ge_f32_e64 s[0:1], 0, v13
	v_add_u32_e32 v13, 1, v7
	s_nop 0
	v_cndmask_b32_e64 v12, v7, v12, s[0:1]
	v_fma_f32 v7, -v13, v7, v6
	v_cmp_lt_f32_e64 s[0:1], 0, v7
	s_nop 1
	v_cndmask_b32_e64 v7, v12, v13, s[0:1]
	v_mul_f32_e32 v12, 0x37800000, v7
	v_cndmask_b32_e32 v7, v7, v12, vcc
	v_cmp_class_f32_e32 vcc, v6, v149
	s_nop 1
	v_cndmask_b32_e32 v6, v7, v6, vcc
	v_div_scale_f32 v7, s[0:1], v6, v6, 1.0
	v_rcp_f32_e32 v12, v7
	s_lshl_b64 s[0:1], s[24:25], 11
	s_lshl_b32 s25, s46, 1
	s_or_b32 s24, s25, 1
	v_fma_f32 v13, -v7, v12, 1.0
	v_fmac_f32_e32 v12, v13, v12
	v_div_scale_f32 v13, vcc, 1.0, v6, 1.0
	v_mul_f32_e32 v34, v13, v12
	v_fma_f32 v35, -v7, v34, v13
	v_fmac_f32_e32 v34, v35, v12
	v_fma_f32 v7, -v7, v34, v13
	v_div_fmas_f32 v7, v7, v12, v34
	v_div_fixup_f32 v6, v7, v6, 1.0
	v_pk_mul_f32 v[12:13], v[62:63], v[6:7] op_sel_hi:[1,0]
	v_pk_mul_f32 v[34:35], v[64:65], v[6:7] op_sel_hi:[1,0]
	v_pk_fma_f32 v[12:13], v[26:27], v[12:13], v[18:19]
	v_pk_fma_f32 v[20:21], v[28:29], v[34:35], v[20:21]
	v_cvt_pk_bf16_f32 v34, v12, v13
	s_lshl_b32 s24, s24, 12
	v_lshlrev_b32_e32 v7, 16, v34
	v_sub_f32_e32 v7, v12, v7
	v_and_b32_e32 v18, 0xffff0000, v34
	v_cvt_pk_bf16_f32 v35, v20, v21
	v_sub_f32_e32 v18, v13, v18
	v_cvt_pk_bf16_f32 v36, v7, v18
	v_mov_b32_e32 v7, 0
	v_cvt_pk_fp8_f32 v7, v12, v13
	s_add_i32 s24, s24, 0
	s_add_u32 s0, s40, s0
	v_lshlrev_b32_e32 v19, 16, v35
	v_cvt_pk_fp8_f32 v7, v20, v21 op_sel:[0,0,1]
	v_and_b32_e32 v26, 0xffff0000, v35
	s_addc_u32 s1, s44, s1
	v_sub_f32_e32 v19, v20, v19
	v_sub_f32_e32 v26, v21, v26
	v_cvt_pk_bf16_f32 v37, v19, v26
	global_store_dword v150, v7, s[0:1] nt
	global_load_dwordx4 v[18:21], v[10:11], off offset:1024
	global_load_dwordx4 v[26:29], v[8:9], off offset:1024
	v_lshrrev_b32_e32 v7, 1, v170
	v_bitop3_b32 v12, s25, v7, 1 bitop3:0x36
	v_lshlrev_b32_e32 v12, 4, v12
	v_add3_u32 v172, s24, v12, v103
	v_pk_mul_f32 v[12:13], v[54:55], v[6:7] op_sel_hi:[1,0]
	ds_write_b64 v172, v[34:35]
	v_pk_mul_f32 v[34:35], v[56:57], v[6:7] op_sel_hi:[1,0]
	v_add_u32_e32 v173, 0x10000, v172
	ds_write_b64 v173, v[36:37]
	v_or_b32_e32 v36, 32, v7
	v_bitop3_b32 v36, s25, v36, 1 bitop3:0x36
	v_lshlrev_b32_e32 v36, 4, v36
	v_add3_u32 v174, s24, v36, v103
	v_add_u32_e32 v175, 0x10000, v174
	v_or_b32_e32 v36, 64, v7
	v_bitop3_b32 v36, s25, v36, 1 bitop3:0x36
	v_lshlrev_b32_e32 v36, 4, v36
	v_add3_u32 v167, s24, v36, v103
	v_add_u32_e32 v168, 0x10000, v167
	v_pk_mul_f32 v[22:23], v[22:23], v[6:7] op_sel_hi:[1,0]
	v_pk_mul_f32 v[24:25], v[24:25], v[6:7] op_sel_hi:[1,0]
	v_pk_mul_f32 v[14:15], v[14:15], v[6:7] op_sel_hi:[1,0]
	v_pk_mul_f32 v[16:17], v[16:17], v[6:7] op_sel_hi:[1,0]
	s_waitcnt vmcnt(1)
	v_pk_add_f32 v[18:19], v[18:19], 1.0 op_sel_hi:[1,0]
	s_waitcnt vmcnt(0)
	v_pk_fma_f32 v[12:13], v[18:19], v[12:13], v[26:27]
	v_mov_b32_e32 v26, 0
	v_cvt_pk_fp8_f32 v26, v12, v13
	v_pk_add_f32 v[20:21], v[20:21], 1.0 op_sel_hi:[1,0]
	s_nop 0
	v_pk_fma_f32 v[20:21], v[20:21], v[34:35], v[28:29]
	v_cvt_pk_bf16_f32 v34, v12, v13
	s_nop 0
	v_cvt_pk_fp8_f32 v26, v20, v21 op_sel:[0,0,1]
	v_lshlrev_b32_e32 v18, 16, v34
	v_cvt_pk_bf16_f32 v35, v20, v21
	v_sub_f32_e32 v18, v12, v18
	v_and_b32_e32 v19, 0xffff0000, v34
	v_lshlrev_b32_e32 v12, 16, v35
	v_sub_f32_e32 v19, v13, v19
	v_sub_f32_e32 v13, v20, v12
	v_and_b32_e32 v12, 0xffff0000, v35
	v_sub_f32_e32 v20, v21, v12
	v_cvt_pk_bf16_f32 v12, v18, v19
	v_cvt_pk_bf16_f32 v13, v13, v20
	global_store_dword v150, v26, s[0:1] offset:256 nt
	global_load_dwordx4 v[18:21], v[10:11], off offset:2048
	s_nop 0
	global_load_dwordx4 v[26:29], v[8:9], off offset:2048
	ds_write_b64 v175, v[12:13]
	v_pk_mul_f32 v[12:13], v[46:47], v[6:7] op_sel_hi:[1,0]
	ds_write_b64 v174, v[34:35]
	v_pk_mul_f32 v[34:35], v[48:49], v[6:7] op_sel_hi:[1,0]
	s_waitcnt vmcnt(1)
	v_pk_add_f32 v[18:19], v[18:19], 1.0 op_sel_hi:[1,0]
	s_waitcnt vmcnt(0)
	v_pk_fma_f32 v[12:13], v[18:19], v[12:13], v[26:27]
	v_mov_b32_e32 v26, 0
	v_cvt_pk_fp8_f32 v26, v12, v13
	v_pk_add_f32 v[20:21], v[20:21], 1.0 op_sel_hi:[1,0]
	s_nop 0
	v_pk_fma_f32 v[20:21], v[20:21], v[34:35], v[28:29]
	v_cvt_pk_bf16_f32 v34, v12, v13
	s_nop 0
	v_cvt_pk_fp8_f32 v26, v20, v21 op_sel:[0,0,1]
	v_lshlrev_b32_e32 v18, 16, v34
	v_cvt_pk_bf16_f32 v35, v20, v21
	v_sub_f32_e32 v18, v12, v18
	v_and_b32_e32 v19, 0xffff0000, v34
	v_lshlrev_b32_e32 v12, 16, v35
	v_sub_f32_e32 v19, v13, v19
	v_sub_f32_e32 v13, v20, v12
	v_and_b32_e32 v12, 0xffff0000, v35
	v_sub_f32_e32 v20, v21, v12
	v_cvt_pk_bf16_f32 v12, v18, v19
	v_cvt_pk_bf16_f32 v13, v13, v20
	global_store_dword v150, v26, s[0:1] offset:512 nt
	global_load_dwordx4 v[18:21], v[10:11], off offset:3072
	s_nop 0
	global_load_dwordx4 v[26:29], v[8:9], off offset:3072
	ds_write_b64 v167, v[34:35]
	ds_write_b64 v168, v[12:13]
	v_pk_mul_f32 v[12:13], v[38:39], v[6:7] op_sel_hi:[1,0]
	v_pk_mul_f32 v[34:35], v[40:41], v[6:7] op_sel_hi:[1,0]
	v_mov_b32_e32 v38, 0
	s_waitcnt vmcnt(1)
	v_pk_add_f32 v[20:21], v[20:21], 1.0 op_sel_hi:[1,0]
	v_pk_add_f32 v[18:19], v[18:19], 1.0 op_sel_hi:[1,0]
	s_waitcnt vmcnt(0)
; #define LAS __attribute__((address_space(3)))
; __device__ __forceinline__ unsigned cvt_pk_bf16(float lo, float hi) { unsigned r; asm volatile("v_cvt_pk_bf16_f32 %0, %1, %2" : "=v"(r) : "v"(lo), "v"(hi)); return r; }
; __device__ __forceinline__ unsigned pk4_fp8(float a, float b, float c, float d) { int w = 0; w = __builtin_amdgcn_cvt_pk_fp8_f32(a, b, w, false); w = __builtin_amdgcn_cvt_pk_fp8_f32(c, d, w, true); return (unsigned)w; }
; __device__ __forceinline__ float bf_lo(unsigned w) { return __uint_as_float(w << 16); }
; __device__ __forceinline__ float bf_hi(unsigned w) { return __uint_as_float(w & 0xffff0000u); }
; __device__ __forceinline__ void p6_router(Frame& F) {
;     ...
;                 for (int j = 0; j < 8; ++j) { const f32x4 sh = ((const f32x4*)(mod + (size_t)b * 12288 + 6144))[loq + 64 * j], sc = ((const f32x4*)(mod + (size_t)b * 12288 + 8192))[loq + 64 * j];
;                     const f32x4 y = v[j] * rstd * (sc + 1.0f) + sh;
;                     u32x2 wh; wh.x = cvt_pk_bf16(y[0], y[1]); wh.y = cvt_pk_bf16(y[2], y[3]);
;                     const f32x4 yl = {y[0] - bf_lo(wh.x), y[1] - bf_hi(wh.x), y[2] - bf_lo(wh.y), y[3] - bf_hi(wh.y)};
;                     u32x2 wl; wl.x = cvt_pk_bf16(yl[0], yl[1]); wl.y = cvt_pk_bf16(yl[2], yl[3]);
;                     { const int r = 2 * wave + q; LAS unsigned char* rowp = F.lds + r * 4096 + ((((lane >> 1) + 32 * j) ^ r) << 4) + (lane & 1) * 8;
;                       *(LAS u32x2*)rowp = wh; *(LAS u32x2*)(rowp + 65536) = wl; }
;                     U2F[(size_t)t * (DM / 4) + lane + 64 * j] = pk4_fp8(y[0], y[1], y[2], y[3]); }
	v_pk_fma_f32 v[20:21], v[34:35], v[20:21], v[28:29]
	v_pk_fma_f32 v[12:13], v[12:13], v[18:19], v[26:27]
	v_mov_b32_e32 v34, 0
	v_cvt_pk_fp8_f32 v34, v12, v13
	v_cvt_pk_bf16_f32 v26, v12, v13
	v_cvt_pk_bf16_f32 v27, v20, v21
	v_cvt_pk_fp8_f32 v34, v20, v21 op_sel:[0,0,1]
	v_lshlrev_b32_e32 v18, 16, v26
	v_and_b32_e32 v19, 0xffff0000, v26
	v_sub_f32_e32 v18, v12, v18
	v_sub_f32_e32 v19, v13, v19
	v_lshlrev_b32_e32 v12, 16, v27
	v_and_b32_e32 v13, 0xffff0000, v27
	v_sub_f32_e32 v12, v20, v12
	v_sub_f32_e32 v13, v21, v13
	v_cvt_pk_bf16_f32 v28, v18, v19
	v_cvt_pk_bf16_f32 v29, v12, v13
	global_store_dword v150, v34, s[0:1] offset:768 nt
	v_add_co_u32_e32 v34, vcc, s41, v10
	s_nop 1
	v_addc_co_u32_e32 v35, vcc, 0, v11, vcc
	v_add_co_u32_e32 v36, vcc, s41, v8
	global_load_dwordx4 v[10:13], v[34:35], off
	s_nop 0
	v_addc_co_u32_e32 v37, vcc, 0, v9, vcc
	global_load_dwordx4 v[18:21], v[36:37], off
	v_or_b32_e32 v8, 0x60, v7
	v_bitop3_b32 v8, s25, v8, 1 bitop3:0x36
	v_lshlrev_b32_e32 v8, 4, v8
	v_add3_u32 v176, s24, v8, v103
	v_pk_mul_f32 v[8:9], v[30:31], v[6:7] op_sel_hi:[1,0]
	v_pk_mul_f32 v[30:31], v[32:33], v[6:7] op_sel_hi:[1,0]
	v_add_u32_e32 v177, 0x10000, v176
	ds_write_b64 v176, v[26:27]
	ds_write_b64 v177, v[28:29]
	v_mov_b32_e32 v28, 0
	v_or_b32_e32 v29, 0x80, v7
	v_bitop3_b32 v29, s25, v29, 1 bitop3:0x36
	v_lshlrev_b32_e32 v29, 4, v29
	v_add3_u32 v178, s24, v29, v103
	v_add_u32_e32 v179, 0x10000, v178
	s_waitcnt vmcnt(1)
	v_pk_add_f32 v[10:11], v[10:11], 1.0 op_sel_hi:[1,0]
	v_pk_add_f32 v[12:13], v[12:13], 1.0 op_sel_hi:[1,0]
	s_waitcnt vmcnt(0)
	v_pk_fma_f32 v[8:9], v[8:9], v[10:11], v[18:19]
	s_nop 0
	v_cvt_pk_fp8_f32 v38, v8, v9
	v_pk_fma_f32 v[12:13], v[30:31], v[12:13], v[20:21]
	v_cvt_pk_bf16_f32 v26, v8, v9
	s_nop 0
	v_cvt_pk_fp8_f32 v38, v12, v13 op_sel:[0,0,1]
	v_cvt_pk_bf16_f32 v27, v12, v13
	v_lshlrev_b32_e32 v10, 16, v26
	v_and_b32_e32 v11, 0xffff0000, v26
	v_lshlrev_b32_e32 v18, 16, v27
	v_and_b32_e32 v19, 0xffff0000, v27
	v_sub_f32_e32 v8, v8, v10
	v_sub_f32_e32 v9, v9, v11
	v_sub_f32_e32 v10, v12, v18
	v_sub_f32_e32 v11, v13, v19
	v_cvt_pk_bf16_f32 v12, v8, v9
	v_cvt_pk_bf16_f32 v13, v10, v11
	global_store_dword v150, v38, s[0:1] offset:1024 nt
	global_load_dwordx4 v[8:11], v[34:35], off offset:1024
	global_load_dwordx4 v[18:21], v[36:37], off offset:1024
	ds_write_b64 v178, v[26:27]
	ds_write_b64 v179, v[12:13]
	s_waitcnt vmcnt(1)
	v_pk_add_f32 v[8:9], v[8:9], 1.0 op_sel_hi:[1,0]
	s_waitcnt vmcnt(0)
	v_pk_fma_f32 v[8:9], v[22:23], v[8:9], v[18:19]
	v_pk_add_f32 v[10:11], v[10:11], 1.0 op_sel_hi:[1,0]
	v_cvt_pk_fp8_f32 v28, v8, v9
	v_pk_fma_f32 v[10:11], v[24:25], v[10:11], v[20:21]
	v_cvt_pk_bf16_f32 v12, v8, v9
	v_mov_b32_e32 v24, 0
	v_cvt_pk_fp8_f32 v28, v10, v11 op_sel:[0,0,1]
	v_cvt_pk_bf16_f32 v13, v10, v11
	v_lshlrev_b32_e32 v18, 16, v12
	v_and_b32_e32 v19, 0xffff0000, v12
	v_lshlrev_b32_e32 v20, 16, v13
	v_and_b32_e32 v21, 0xffff0000, v13
	v_sub_f32_e32 v8, v8, v18
	v_sub_f32_e32 v9, v9, v19
	v_sub_f32_e32 v18, v10, v20
	v_sub_f32_e32 v10, v11, v21
	v_cvt_pk_bf16_f32 v22, v8, v9
	v_cvt_pk_bf16_f32 v23, v18, v10
	global_store_dword v150, v28, s[0:1] offset:1280 nt
	global_load_dwordx4 v[8:11], v[34:35], off offset:2048
	global_load_dwordx4 v[18:21], v[36:37], off offset:2048
	v_or_b32_e32 v25, 0xa0, v7
	v_bitop3_b32 v25, s25, v25, 1 bitop3:0x36
	v_lshlrev_b32_e32 v25, 4, v25
	v_add3_u32 v180, s24, v25, v103
	v_add_u32_e32 v181, 0x10000, v180
	ds_write_b64 v180, v[12:13]
	ds_write_b64 v181, v[22:23]
	s_waitcnt vmcnt(1)
	v_pk_add_f32 v[8:9], v[8:9], 1.0 op_sel_hi:[1,0]
	s_waitcnt vmcnt(0)
	v_pk_fma_f32 v[8:9], v[14:15], v[8:9], v[18:19]
	v_pk_add_f32 v[10:11], v[10:11], 1.0 op_sel_hi:[1,0]
	v_cvt_pk_fp8_f32 v24, v8, v9
	v_pk_fma_f32 v[10:11], v[16:17], v[10:11], v[20:21]
	v_cvt_pk_bf16_f32 v16, v8, v9
	v_or_b32_e32 v21, 0xc0, v7
	v_cvt_pk_fp8_f32 v24, v10, v11 op_sel:[0,0,1]
	v_cvt_pk_bf16_f32 v17, v10, v11
	v_lshlrev_b32_e32 v12, 16, v16
	v_and_b32_e32 v13, 0xffff0000, v16
	v_lshlrev_b32_e32 v14, 16, v17
	v_and_b32_e32 v15, 0xffff0000, v17
	v_sub_f32_e32 v8, v8, v12
	v_sub_f32_e32 v9, v9, v13
	v_sub_f32_e32 v12, v10, v14
	v_sub_f32_e32 v10, v11, v15
	v_cvt_pk_bf16_f32 v18, v8, v9
	v_cvt_pk_bf16_f32 v19, v12, v10
	global_store_dword v150, v24, s[0:1] offset:1536 nt
	global_load_dwordx4 v[8:11], v[34:35], off offset:3072
	global_load_dwordx4 v[12:15], v[36:37], off offset:3072
	v_or_b32_e32 v7, 0xe0, v7
	v_bitop3_b32 v7, s25, v7, 1 bitop3:0x36
	v_pk_mul_f32 v[4:5], v[4:5], v[6:7] op_sel_hi:[1,0]
	v_mov_b32_e32 v20, 0
	v_lshlrev_b32_e32 v22, 4, v7
	v_pk_mul_f32 v[2:3], v[2:3], v[6:7] op_sel_hi:[1,0]
	v_bitop3_b32 v21, s25, v21, 1 bitop3:0x36
	v_lshlrev_b32_e32 v21, 4, v21
	v_add3_u32 v184, s24, v21, v103
	v_add_u32_e32 v185, 0x10000, v184
	ds_write_b64 v184, v[16:17]
	ds_write_b64 v185, v[18:19]
	v_add3_u32 v182, s24, v22, v103
	v_add_u32_e32 v183, 0x10000, v182
	s_waitcnt vmcnt(1)
	v_pk_add_f32 v[8:9], v[8:9], 1.0 op_sel_hi:[1,0]
	s_waitcnt vmcnt(0)
; #define LAS __attribute__((address_space(3)))
; __device__ __forceinline__ unsigned pk4_fp8(float a, float b, float c, float d) { int w = 0; w = __builtin_amdgcn_cvt_pk_fp8_f32(a, b, w, false); w = __builtin_amdgcn_cvt_pk_fp8_f32(c, d, w, true); return (unsigned)w; }
; __device__ __forceinline__ void p6_router(Frame& F) {
;     ...
;                     U2F[(size_t)t * (DM / 4) + lane + 64 * j] = pk4_fp8(y[0], y[1], y[2], y[3]); }
;             }
;             __builtin_amdgcn_sched_barrier(0);
;             bf16x8 bh[2][2], bl[2][2]; f32x4 cur[2] = {(f32x4){0.f, 0.f, 0.f, 0.f}, (f32x4){0.f, 0.f, 0.f, 0.f}};
;             const bf16_t* wbh = WRH + (size_t)fr * DM + wave * 256 + fq * 8; const bf16_t* wbl = WRL + (size_t)fr * DM + wave * 256 + fq * 8;
; #pragma unroll
;             for (int n = 0; n < 2; ++n) { bh[0][n] = *(const bf16x8*)(wbh + (size_t)(16 * n) * DM); bl[0][n] = *(const bf16x8*)(wbl + (size_t)(16 * n) * DM); }
;             if (rp == 0) {
; #pragma unroll
;                 for (int q = 0; q < 2; ++q)
; #pragma unroll
;                     for (int j = 0; j < 8; ++j) zr[q][j] = ((const u32x2*)(ZB + (size_t)(ta + 2 + q) * DM))[lane + 64 * j];
;             }
;             __syncthreads();
; #pragma unroll
;             for (int ks = 0; ks < 8; ++ks) {
;                 if (ks < 7) {
; #pragma unroll
;                     for (int n = 0; n < 2; ++n) { bh[(ks + 1) & 1][n] = *(const bf16x8*)(wbh + (size_t)(16 * n) * DM + (ks + 1) * 32); bl[(ks + 1) & 1][n] = *(const bf16x8*)(wbl + (size_t)(16 * n) * DM + (ks + 1) * 32); }
;                 }
;                 const LAS unsigned char* ap = F.lds + fr * 4096 + (((wave * 32 + ks * 4 + fq) ^ fr) << 4);
;                 const bf16x8 ah = *(const LAS bf16x8*)ap, al = *(const LAS bf16x8*)(ap + 65536);
; #pragma unroll
;                 for (int n = 0; n < 2; ++n) {
;                     cur[n] = __builtin_amdgcn_mfma_f32_16x16x32_bf16(ah, bh[ks & 1][n], cur[n], 0, 0, 0);
;                     cur[n] = __builtin_amdgcn_mfma_f32_16x16x32_bf16(ah, bl[ks & 1][n], cur[n], 0, 0, 0);
;                     cur[n] = __builtin_amdgcn_mfma_f32_16x16x32_bf16(al, bh[ks & 1][n], cur[n], 0, 0, 0);
;                 }
	v_pk_fma_f32 v[4:5], v[4:5], v[8:9], v[12:13]
	v_pk_add_f32 v[6:7], v[10:11], 1.0 op_sel_hi:[1,0]
	v_cvt_pk_fp8_f32 v20, v4, v5
	v_pk_fma_f32 v[2:3], v[2:3], v[6:7], v[14:15]
	v_cvt_pk_bf16_f32 v6, v4, v5
	s_nop 0
	v_cvt_pk_fp8_f32 v20, v2, v3 op_sel:[0,0,1]
	v_lshlrev_b32_e32 v8, 16, v6
	v_and_b32_e32 v9, 0xffff0000, v6
	v_cvt_pk_bf16_f32 v7, v2, v3
	v_sub_f32_e32 v4, v4, v8
	v_lshlrev_b32_e32 v10, 16, v7
	v_and_b32_e32 v11, 0xffff0000, v7
	v_sub_f32_e32 v5, v5, v9
	v_sub_f32_e32 v8, v2, v10
	v_sub_f32_e32 v9, v3, v11
	v_cvt_pk_bf16_f32 v4, v4, v5
	v_cvt_pk_bf16_f32 v5, v8, v9
	ds_write_b64 v182, v[6:7]
	ds_write_b64 v183, v[4:5]
	global_store_dword v150, v20, s[0:1] offset:1792 nt
	v_lshlrev_b32_e32 v78, 12, v151
	s_lshl_b32 s36, s46, 9
	v_lshl_add_u64 v[4:5], s[82:83], 0, v[78:79]
	v_and_b32_e32 v2, 48, v170
	v_mov_b32_e32 v3, v79
	v_lshl_add_u64 v[4:5], v[4:5], 0, s[36:37]
	v_lshl_add_u64 v[44:45], v[4:5], 0, v[2:3]
	s_mov_b32 s0, 0x3c00000
	v_add_co_u32_e32 v84, vcc, s0, v44
	s_mov_b32 s1, 0x3c10000
	s_nop 0
	v_addc_co_u32_e32 v85, vcc, 0, v45, vcc
	global_load_dwordx4 v[2:5], v[84:85], off
	v_add_co_u32_e32 v74, vcc, s1, v44
	s_mov_b32 s0, 0x3c20000
	s_nop 0
	v_addc_co_u32_e32 v75, vcc, 0, v45, vcc
	v_add_co_u32_e32 v86, vcc, s0, v44
	global_load_dwordx4 v[6:9], v[74:75], off
	s_nop 0
	v_addc_co_u32_e32 v87, vcc, 0, v45, vcc
	global_load_dwordx4 v[20:23], v[86:87], off
	s_mov_b32 s0, 0x3c30000
	v_add_co_u32_e32 v76, vcc, s0, v44
	s_or_b32 s0, s4, 2
	s_nop 0
	v_addc_co_u32_e32 v77, vcc, 0, v45, vcc
	global_load_dwordx4 v[24:27], v[76:77], off
	s_ashr_i32 s1, s0, 31
	s_lshl_b64 s[0:1], s[0:1], 12
	s_add_u32 s0, s6, s0
	s_addc_u32 s1, s7, s1
	s_or_b32 s24, s4, 3
	v_bitop3_b32 v10, s5, v151, v154 bitop3:0x36
	v_add_u32_e32 v52, 0, v78
	s_ashr_i32 s25, s24, 31
	v_lshl_add_u32 v186, v10, 4, v52
	global_load_dwordx2 v[46:47], v146, s[0:1]
	global_load_dwordx2 v[48:49], v146, s[0:1] offset:512
	global_load_dwordx2 v[50:51], v146, s[0:1] offset:1024
	global_load_dwordx2 v[18:19], v146, s[0:1] offset:1536
	global_load_dwordx2 v[16:17], v146, s[0:1] offset:2048
	global_load_dwordx2 v[14:15], v146, s[0:1] offset:2560
	global_load_dwordx2 v[12:13], v146, s[0:1] offset:3072
	global_load_dwordx2 v[10:11], v146, s[0:1] offset:3584
	s_lshl_b64 s[0:1], s[24:25], 12
	s_add_u32 s0, s6, s0
	s_addc_u32 s1, s7, s1
	global_load_dwordx2 v[100:101], v146, s[0:1]
	global_load_dwordx2 v[102:103], v146, s[0:1] offset:512
	global_load_dwordx2 v[98:99], v146, s[0:1] offset:1024
	global_load_dwordx2 v[96:97], v146, s[0:1] offset:1536
	global_load_dwordx2 v[94:95], v146, s[0:1] offset:2048
	global_load_dwordx2 v[92:93], v146, s[0:1] offset:2560
	global_load_dwordx2 v[90:91], v146, s[0:1] offset:3072
	global_load_dwordx2 v[88:89], v146, s[0:1] offset:3584
	s_waitcnt lgkmcnt(0)
	s_barrier
	ds_read_b128 v[28:31], v186
	v_add_u32_e32 v187, 0x10000, v186
	ds_read_b128 v[32:35], v187
	s_mov_b64 s[0:1], 0x3c00000
	s_mov_b64 s[6:7], 0x3c20000
	v_lshl_add_u64 v[80:81], v[44:45], 0, s[0:1]
	v_lshl_add_u64 v[82:83], v[44:45], 0, s[6:7]
	v_or_b32_e32 v44, s5, v154
	s_waitcnt vmcnt(19) lgkmcnt(1)
	v_mfma_f32_16x16x32_bf16 v[36:39], v[28:31], v[2:5], 0
	s_waitcnt vmcnt(18)
	v_mfma_f32_16x16x32_bf16 v[40:43], v[28:31], v[6:9], 0
	s_waitcnt vmcnt(17)
	v_mfma_f32_16x16x32_bf16 v[20:23], v[28:31], v[20:23], v[36:39]
	s_waitcnt vmcnt(16)
	v_mfma_f32_16x16x32_bf16 v[24:27], v[28:31], v[24:27], v[40:43]
	global_load_dwordx4 v[28:31], v[80:81], off offset:64
	s_nop 0
	global_load_dwordx4 v[36:39], v[82:83], off offset:64
	s_waitcnt lgkmcnt(0)
	v_mfma_f32_16x16x32_bf16 v[2:5], v[32:35], v[2:5], v[20:23]
	s_nop 2
	global_load_dwordx4 v[20:23], v[74:75], off offset:64
	global_load_dwordx4 v[40:43], v[76:77], off offset:64
	v_mfma_f32_16x16x32_bf16 v[6:9], v[32:35], v[6:9], v[24:27]
	s_nop 2
	v_bitop3_b32 v24, v44, v151, 4 bitop3:0x36
	v_lshl_add_u32 v188, v24, 4, v52
	ds_read_b128 v[24:27], v188
	v_add_u32_e32 v189, 0x10000, v188
	ds_read_b128 v[32:35], v189
	s_waitcnt vmcnt(3) lgkmcnt(1)
	v_mfma_f32_16x16x32_bf16 v[2:5], v[24:27], v[28:31], v[2:5]
	s_waitcnt vmcnt(1)
	v_mfma_f32_16x16x32_bf16 v[6:9], v[24:27], v[20:23], v[6:9]
	v_mfma_f32_16x16x32_bf16 v[2:5], v[24:27], v[36:39], v[2:5]
	s_waitcnt vmcnt(0)
	v_mfma_f32_16x16x32_bf16 v[6:9], v[24:27], v[40:43], v[6:9]
	global_load_dwordx4 v[24:27], v[80:81], off offset:128
	global_load_dwordx4 v[36:39], v[82:83], off offset:128
	s_waitcnt lgkmcnt(0)
	v_mfma_f32_16x16x32_bf16 v[2:5], v[32:35], v[28:31], v[2:5]
	global_load_dwordx4 v[28:31], v[74:75], off offset:128
	global_load_dwordx4 v[40:43], v[76:77], off offset:128
	v_mfma_f32_16x16x32_bf16 v[6:9], v[32:35], v[20:23], v[6:9]
	v_bitop3_b32 v20, v44, v151, 8 bitop3:0x36
	v_lshl_add_u32 v190, v20, 4, v52
	ds_read_b128 v[20:23], v190
	v_add_u32_e32 v191, 0x10000, v190
	ds_read_b128 v[32:35], v191
	s_waitcnt vmcnt(3) lgkmcnt(1)
	v_mfma_f32_16x16x32_bf16 v[2:5], v[20:23], v[24:27], v[2:5]
	s_waitcnt vmcnt(1)
	v_mfma_f32_16x16x32_bf16 v[6:9], v[20:23], v[28:31], v[6:9]
	v_mfma_f32_16x16x32_bf16 v[2:5], v[20:23], v[36:39], v[2:5]
	s_waitcnt vmcnt(0)
	v_mfma_f32_16x16x32_bf16 v[6:9], v[20:23], v[40:43], v[6:9]
	global_load_dwordx4 v[20:23], v[80:81], off offset:192
	global_load_dwordx4 v[36:39], v[82:83], off offset:192
	s_waitcnt lgkmcnt(0)
	v_mfma_f32_16x16x32_bf16 v[2:5], v[32:35], v[24:27], v[2:5]
	global_load_dwordx4 v[24:27], v[74:75], off offset:192
	global_load_dwordx4 v[40:43], v[76:77], off offset:192
	v_mfma_f32_16x16x32_bf16 v[6:9], v[32:35], v[28:31], v[6:9]
	v_bitop3_b32 v28, v44, v151, 12 bitop3:0x36
	v_lshl_add_u32 v192, v28, 4, v52
	ds_read_b128 v[28:31], v192
	v_add_u32_e32 v193, 0x10000, v192
	ds_read_b128 v[32:35], v193
	s_waitcnt vmcnt(3) lgkmcnt(1)
; #define LAS __attribute__((address_space(3)))
; __device__ __forceinline__ float bf_lo(unsigned w) { return __uint_as_float(w << 16); }
; __device__ __forceinline__ float bf_hi(unsigned w) { return __uint_as_float(w & 0xffff0000u); }
; __device__ __forceinline__ void p6_router(Frame& F) {
;     ...
;                 for (int j = 0; j < 8; ++j) { const u32x2 zb = zr[q][j]; v[j] = (f32x4){bf_lo(zb.x), bf_hi(zb.x), bf_lo(zb.y), bf_hi(zb.y)}; s += (v[j][0] + v[j][1]) + (v[j][2] + v[j][3]); }
;     ...
; #pragma unroll
;             for (int ks = 0; ks < 8; ++ks) {
;                 if (ks < 7) {
; #pragma unroll
;                     for (int n = 0; n < 2; ++n) { bh[(ks + 1) & 1][n] = *(const bf16x8*)(wbh + (size_t)(16 * n) * DM + (ks + 1) * 32); bl[(ks + 1) & 1][n] = *(const bf16x8*)(wbl + (size_t)(16 * n) * DM + (ks + 1) * 32); }
;                 }
;                 const LAS unsigned char* ap = F.lds + fr * 4096 + (((wave * 32 + ks * 4 + fq) ^ fr) << 4);
;                 const bf16x8 ah = *(const LAS bf16x8*)ap, al = *(const LAS bf16x8*)(ap + 65536);
; #pragma unroll
;                 for (int n = 0; n < 2; ++n) {
;                     cur[n] = __builtin_amdgcn_mfma_f32_16x16x32_bf16(ah, bh[ks & 1][n], cur[n], 0, 0, 0);
;                     cur[n] = __builtin_amdgcn_mfma_f32_16x16x32_bf16(ah, bl[ks & 1][n], cur[n], 0, 0, 0);
;                     cur[n] = __builtin_amdgcn_mfma_f32_16x16x32_bf16(al, bh[ks & 1][n], cur[n], 0, 0, 0);
;                 }
;                 __builtin_amdgcn_sched_barrier(0);
;             }
;             accp[0] = cur[0]; accp[1] = cur[1];
;             __syncthreads();
;         };
;         pass(0, acc[0]); pass(1, acc[1]);
	v_mfma_f32_16x16x32_bf16 v[2:5], v[28:31], v[20:23], v[2:5]
	s_waitcnt vmcnt(1)
	v_mfma_f32_16x16x32_bf16 v[6:9], v[28:31], v[24:27], v[6:9]
	v_mfma_f32_16x16x32_bf16 v[2:5], v[28:31], v[36:39], v[2:5]
	s_waitcnt vmcnt(0)
	v_mfma_f32_16x16x32_bf16 v[6:9], v[28:31], v[40:43], v[6:9]
	global_load_dwordx4 v[28:31], v[80:81], off offset:256
	global_load_dwordx4 v[36:39], v[82:83], off offset:256
	s_waitcnt lgkmcnt(0)
	v_mfma_f32_16x16x32_bf16 v[2:5], v[32:35], v[20:23], v[2:5]
	global_load_dwordx4 v[20:23], v[74:75], off offset:256
	global_load_dwordx4 v[40:43], v[76:77], off offset:256
	v_mfma_f32_16x16x32_bf16 v[6:9], v[32:35], v[24:27], v[6:9]
	v_bitop3_b32 v24, v44, v151, 16 bitop3:0x36
	v_lshl_add_u32 v194, v24, 4, v52
	ds_read_b128 v[24:27], v194
	v_add_u32_e32 v195, 0x10000, v194
	ds_read_b128 v[32:35], v195
	s_waitcnt vmcnt(3) lgkmcnt(1)
	v_mfma_f32_16x16x32_bf16 v[2:5], v[24:27], v[28:31], v[2:5]
	s_waitcnt vmcnt(1)
	v_mfma_f32_16x16x32_bf16 v[6:9], v[24:27], v[20:23], v[6:9]
	v_mfma_f32_16x16x32_bf16 v[2:5], v[24:27], v[36:39], v[2:5]
	s_waitcnt vmcnt(0)
	v_mfma_f32_16x16x32_bf16 v[6:9], v[24:27], v[40:43], v[6:9]
	global_load_dwordx4 v[24:27], v[80:81], off offset:320
	global_load_dwordx4 v[36:39], v[82:83], off offset:320
	s_waitcnt lgkmcnt(0)
	v_mfma_f32_16x16x32_bf16 v[2:5], v[32:35], v[28:31], v[2:5]
	global_load_dwordx4 v[28:31], v[74:75], off offset:320
	global_load_dwordx4 v[40:43], v[76:77], off offset:320
	v_mfma_f32_16x16x32_bf16 v[6:9], v[32:35], v[20:23], v[6:9]
	v_bitop3_b32 v20, v44, v151, 20 bitop3:0x36
	v_lshl_add_u32 v196, v20, 4, v52
	ds_read_b128 v[20:23], v196
	v_add_u32_e32 v197, 0x10000, v196
	ds_read_b128 v[32:35], v197
	s_waitcnt vmcnt(3) lgkmcnt(1)
	v_mfma_f32_16x16x32_bf16 v[2:5], v[20:23], v[24:27], v[2:5]
	s_waitcnt vmcnt(1)
	v_mfma_f32_16x16x32_bf16 v[6:9], v[20:23], v[28:31], v[6:9]
	v_mfma_f32_16x16x32_bf16 v[2:5], v[20:23], v[36:39], v[2:5]
	s_waitcnt vmcnt(0)
	v_mfma_f32_16x16x32_bf16 v[6:9], v[20:23], v[40:43], v[6:9]
	global_load_dwordx4 v[20:23], v[80:81], off offset:384
	global_load_dwordx4 v[36:39], v[82:83], off offset:384
	s_waitcnt lgkmcnt(0)
	v_mfma_f32_16x16x32_bf16 v[2:5], v[32:35], v[24:27], v[2:5]
	global_load_dwordx4 v[24:27], v[74:75], off offset:384
	global_load_dwordx4 v[40:43], v[76:77], off offset:384
	v_mfma_f32_16x16x32_bf16 v[6:9], v[32:35], v[28:31], v[6:9]
	v_bitop3_b32 v28, v44, v151, 24 bitop3:0x36
	v_lshl_add_u32 v199, v28, 4, v52
	ds_read_b128 v[28:31], v199
	v_add_u32_e32 v201, 0x10000, v199
	ds_read_b128 v[32:35], v201
	s_waitcnt vmcnt(3) lgkmcnt(1)
	v_mfma_f32_16x16x32_bf16 v[2:5], v[28:31], v[20:23], v[2:5]
	s_waitcnt vmcnt(1)
	v_mfma_f32_16x16x32_bf16 v[6:9], v[28:31], v[24:27], v[6:9]
	v_mfma_f32_16x16x32_bf16 v[2:5], v[28:31], v[36:39], v[2:5]
	s_waitcnt vmcnt(0)
	v_mfma_f32_16x16x32_bf16 v[6:9], v[28:31], v[40:43], v[6:9]
	global_load_dwordx4 v[28:31], v[80:81], off offset:448
	global_load_dwordx4 v[36:39], v[82:83], off offset:448
	s_waitcnt lgkmcnt(0)
	v_mfma_f32_16x16x32_bf16 v[2:5], v[32:35], v[20:23], v[2:5]
	global_load_dwordx4 v[20:23], v[74:75], off offset:448
	global_load_dwordx4 v[40:43], v[76:77], off offset:448
	v_mfma_f32_16x16x32_bf16 v[6:9], v[32:35], v[24:27], v[6:9]
	v_bitop3_b32 v24, v44, v151, 28 bitop3:0x36
	v_lshl_add_u32 v198, v24, 4, v52
	ds_read_b128 v[24:27], v198
	v_add_u32_e32 v200, 0x10000, v198
	ds_read_b128 v[32:35], v200
	s_waitcnt vmcnt(3) lgkmcnt(1)
	v_mfma_f32_16x16x32_bf16 v[2:5], v[24:27], v[28:31], v[2:5]
	s_waitcnt vmcnt(1)
	v_mfma_f32_16x16x32_bf16 v[6:9], v[24:27], v[20:23], v[6:9]
	v_mfma_f32_16x16x32_bf16 v[2:5], v[24:27], v[36:39], v[2:5]
	s_waitcnt vmcnt(0)
	v_mfma_f32_16x16x32_bf16 v[6:9], v[24:27], v[40:43], v[6:9]
	s_waitcnt lgkmcnt(0)
	v_mfma_f32_16x16x32_bf16 v[2:5], v[32:35], v[28:31], v[2:5]
	v_mfma_f32_16x16x32_bf16 v[6:9], v[32:35], v[20:23], v[6:9]
	v_lshlrev_b32_e32 v131, 16, v48
	v_lshlrev_b32_e32 v130, 16, v46
	v_and_b32_e32 v133, 0xffff0000, v48
	v_and_b32_e32 v132, 0xffff0000, v46
	v_lshlrev_b32_e32 v127, 16, v49
	v_lshlrev_b32_e32 v126, 16, v47
	v_and_b32_e32 v129, 0xffff0000, v49
	v_and_b32_e32 v128, 0xffff0000, v47
	v_pk_add_f32 v[20:21], v[130:131], v[132:133]
	v_pk_add_f32 v[22:23], v[126:127], v[128:129]
	v_lshlrev_b32_e32 v125, 16, v51
	v_pk_add_f32 v[20:21], v[20:21], v[22:23]
	v_lshlrev_b32_e32 v124, 16, v50
	v_add_f32_e32 v20, 0, v20
	v_add_f32_e32 v114, v20, v21
	v_and_b32_e32 v21, 0xffff0000, v51
	v_and_b32_e32 v20, 0xffff0000, v50
	v_pk_add_f32 v[22:23], v[124:125], v[20:21]
	v_lshlrev_b32_e32 v120, 16, v18
	v_and_b32_e32 v121, 0xffff0000, v18
	v_lshlrev_b32_e32 v122, 16, v19
	v_and_b32_e32 v123, 0xffff0000, v19
	v_lshlrev_b32_e32 v115, 16, v16
	v_and_b32_e32 v139, 0xffff0000, v16
	v_lshlrev_b32_e32 v119, 16, v17
	v_and_b32_e32 v117, 0xffff0000, v17
	v_pk_add_f32 v[16:17], v[22:23], v[22:23] op_sel:[0,1] op_sel_hi:[1,0]
	v_add_f32_e32 v118, v120, v121
	v_add_f32_e32 v116, v122, v123
	v_mov_b32_e32 v17, v139
	v_pk_add_f32 v[16:17], v[114:115], v[16:17]
	v_pk_add_f32 v[18:19], v[118:119], v[116:117]
	v_lshlrev_b32_e32 v113, 16, v15
	v_lshlrev_b32_e32 v112, 16, v14
	v_and_b32_e32 v15, 0xffff0000, v15
	v_and_b32_e32 v14, 0xffff0000, v14
	v_pk_add_f32 v[16:17], v[16:17], v[18:19]
	v_pk_add_f32 v[18:19], v[112:113], v[14:15]
	v_lshlrev_b32_e32 v108, 16, v12
	v_and_b32_e32 v109, 0xffff0000, v12
	v_lshlrev_b32_e32 v110, 16, v13
	v_and_b32_e32 v111, 0xffff0000, v13
	v_lshlrev_b32_e32 v136, 16, v10
	v_and_b32_e32 v137, 0xffff0000, v10
	v_lshlrev_b32_e32 v107, 16, v11
	v_and_b32_e32 v105, 0xffff0000, v11
	v_pk_add_f32 v[10:11], v[16:17], v[16:17] op_sel:[0,1] op_sel_hi:[1,0]
	v_pk_add_f32 v[12:13], v[18:19], v[18:19] op_sel:[0,1] op_sel_hi:[1,0]
	v_add_f32_e32 v106, v108, v109
	v_add_f32_e32 v104, v110, v111
	v_mov_b32_e32 v11, v136
	v_mov_b32_e32 v13, v137
	v_pk_add_f32 v[10:11], v[10:11], v[12:13]
	v_pk_add_f32 v[12:13], v[106:107], v[104:105]
	s_nop 0
	v_pk_add_f32 v[10:11], v[10:11], v[12:13]
	s_barrier
; __device__ __forceinline__ float bf_lo(unsigned w) { return __uint_as_float(w << 16); }
; __device__ __forceinline__ float bf_hi(unsigned w) { return __uint_as_float(w & 0xffff0000u); }
; __device__ __forceinline__ void p6_router(Frame& F) {
;     ...
;             for (int j = 0; j < 8; ++j) { pw[j] = ((const f32x4*)F.in[I_LN1W])[lop + 64 * j]; pb[j] = ((const f32x4*)F.in[I_LN1B])[lop + 64 * j]; }
; #pragma unroll
;             for (int q = 0; q < 2; ++q) {
;                 const int t = ta + q; f32x4 v[8]; float s = 0.f;
; #pragma unroll
;                 for (int j = 0; j < 8; ++j) { const u32x2 zb = zr[q][j]; v[j] = (f32x4){bf_lo(zb.x), bf_hi(zb.x), bf_lo(zb.y), bf_hi(zb.y)}; s += (v[j][0] + v[j][1]) + (v[j][2] + v[j][3]); }
;                 float mean = wave_sum(s) * (1.f / DM), s2 = 0.f;
; #pragma unroll
;                 for (int j = 0; j < 8; ++j) { v[j] = v[j] - mean; s2 += (v[j][0] * v[j][0] + v[j][1] * v[j][1]) + (v[j][2] * v[j][2] + v[j][3] * v[j][3]); }
;                 float rstd = 1.f / sqrtf(wave_sum(s2) * (1.f / DM) + LN_EPS);
	v_add_f32_e32 v10, v10, v11
	ds_bpermute_b32 v11, v1, v10
	s_waitcnt lgkmcnt(0)
	v_and_b32_e32 v215, 0xffff0000, v93
	v_and_b32_e32 v214, 0xffff0000, v92
	v_add_f32_e32 v10, v10, v11
	ds_bpermute_b32 v11, v142, v10
	s_waitcnt lgkmcnt(0)
	v_add_f32_e32 v10, v10, v11
	ds_bpermute_b32 v11, v143, v10
	s_waitcnt lgkmcnt(0)
	v_add_f32_e32 v10, v10, v11
	ds_bpermute_b32 v11, v144, v10
	s_waitcnt lgkmcnt(0)
	v_add_f32_e32 v12, v10, v11
	ds_bpermute_b32 v13, v145, v12
	v_mov_b32_e32 v10, v170
	s_waitcnt lgkmcnt(0)
	v_add_f32_e32 v22, v12, v13
	ds_bpermute_b32 v23, v147, v22
	v_ashrrev_i32_e32 v11, 31, v10
	v_lshlrev_b64 v[10:11], 4, v[10:11]
	v_lshl_add_u64 v[18:19], s[10:11], 0, v[10:11]
	v_lshl_add_u64 v[16:17], s[8:9], 0, v[10:11]
	s_waitcnt lgkmcnt(0)
	v_add_f32_e32 v28, v22, v23
	v_fmac_f32_e32 v128, 0xba000000, v28
	v_fmac_f32_e32 v132, 0xba000000, v28
	v_fmac_f32_e32 v129, 0xba000000, v28
	v_fmac_f32_e32 v133, 0xba000000, v28
	v_fmac_f32_e32 v126, 0xba000000, v28
	v_fmac_f32_e32 v130, 0xba000000, v28
	v_fmac_f32_e32 v127, 0xba000000, v28
	v_fmac_f32_e32 v131, 0xba000000, v28
	v_pk_mul_f32 v[22:23], v[132:133], v[132:133]
	v_pk_mul_f32 v[24:25], v[128:129], v[128:129]
	v_fmac_f32_e32 v20, 0xba000000, v28
	v_fmac_f32_e32 v21, 0xba000000, v28
	v_fmac_f32_e32 v125, 0xba000000, v28
	v_pk_fma_f32 v[22:23], v[130:131], v[130:131], v[22:23]
	v_pk_fma_f32 v[24:25], v[126:127], v[126:127], v[24:25]
	v_fmac_f32_e32 v124, 0xba000000, v28
	v_mov_b32_e32 v202, v125
	v_mov_b32_e32 v203, v21
	v_mov_b32_e32 v125, v20
	v_pk_add_f32 v[22:23], v[22:23], v[24:25]
	v_pk_mul_f32 v[24:25], v[202:203], v[202:203]
	v_pk_mul_f32 v[20:21], v[124:125], v[124:125]
	v_fmac_f32_e32 v120, 0xba000000, v28
	v_pk_mov_b32 v[26:27], v[20:21], v[24:25] op_sel:[1,0]
	v_mov_b32_e32 v21, v25
	v_pk_add_f32 v[20:21], v[26:27], v[20:21]
	v_fmac_f32_e32 v121, 0xba000000, v28
	v_pk_add_f32 v[20:21], v[20:21], v[20:21] op_sel_hi:[0,1]
	v_fmac_f32_e32 v122, 0xba000000, v28
	v_mul_f32_e32 v20, v120, v120
	v_fmac_f32_e32 v123, 0xba000000, v28
	v_pk_fma_f32 v[24:25], v[120:121], v[120:121], v[20:21] op_sel_hi:[1,1,0]
	v_mul_f32_e32 v20, v122, v122
	v_pk_add_f32 v[22:23], v[22:23], v[22:23] op_sel_hi:[0,1]
	v_pk_fma_f32 v[26:27], v[122:123], v[122:123], v[20:21] op_sel_hi:[1,1,0]
	v_fmac_f32_e32 v117, 0xba000000, v28
	v_fmac_f32_e32 v119, 0xba000000, v28
	v_fmac_f32_e32 v139, 0xba000000, v28
	v_fmac_f32_e32 v115, 0xba000000, v28
	v_fmac_f32_e32 v14, 0xba000000, v28
	v_fmac_f32_e32 v15, 0xba000000, v28
	v_fmac_f32_e32 v113, 0xba000000, v28
	v_mul_f32_e32 v24, v115, v115
	v_mul_f32_e32 v26, v139, v139
	v_mul_f32_e32 v20, v119, v119
	v_mul_f32_e32 v22, v117, v117
	v_fmac_f32_e32 v112, 0xba000000, v28
	v_mov_b32_e32 v140, v113
	v_mov_b32_e32 v141, v15
	v_mov_b32_e32 v113, v14
	v_pk_add_f32 v[24:25], v[24:25], v[26:27]
	v_pk_add_f32 v[20:21], v[20:21], v[22:23]
	v_pk_mul_f32 v[22:23], v[140:141], v[140:141]
	v_pk_mul_f32 v[14:15], v[112:113], v[112:113]
	v_pk_add_f32 v[20:21], v[24:25], v[20:21]
	v_pk_mov_b32 v[24:25], v[14:15], v[22:23] op_sel:[1,0]
	v_mov_b32_e32 v15, v23
	v_pk_add_f32 v[14:15], v[24:25], v[14:15]
	v_fmac_f32_e32 v108, 0xba000000, v28
	v_pk_add_f32 v[14:15], v[14:15], v[14:15] op_sel_hi:[0,1]
	v_fmac_f32_e32 v109, 0xba000000, v28
	v_fmac_f32_e32 v110, 0xba000000, v28
	v_mul_f32_e32 v14, v108, v108
	v_fmac_f32_e32 v111, 0xba000000, v28
	v_pk_fma_f32 v[22:23], v[108:109], v[108:109], v[14:15] op_sel_hi:[1,1,0]
	v_mul_f32_e32 v14, v110, v110
	v_pk_add_f32 v[20:21], v[20:21], v[20:21] op_sel_hi:[0,1]
	v_pk_fma_f32 v[24:25], v[110:111], v[110:111], v[14:15] op_sel_hi:[1,1,0]
	v_fmac_f32_e32 v105, 0xba000000, v28
	v_fmac_f32_e32 v107, 0xba000000, v28
	v_fmac_f32_e32 v137, 0xba000000, v28
	v_fmac_f32_e32 v136, 0xba000000, v28
	v_mul_f32_e32 v22, v136, v136
	v_mul_f32_e32 v24, v137, v137
	v_mul_f32_e32 v14, v107, v107
	v_mul_f32_e32 v20, v105, v105
	v_pk_add_f32 v[22:23], v[22:23], v[24:25]
	v_pk_add_f32 v[14:15], v[14:15], v[20:21]
	global_load_dwordx4 v[10:13], v[18:19], off
	v_pk_add_f32 v[14:15], v[22:23], v[14:15]
	global_load_dwordx4 v[70:73], v[16:17], off
	global_load_dwordx4 v[62:65], v[16:17], off offset:1024
	global_load_dwordx4 v[66:69], v[18:19], off offset:1024
	v_add_f32_e32 v14, v14, v15
	ds_bpermute_b32 v15, v1, v14
	global_load_dwordx4 v[54:57], v[16:17], off offset:2048
	global_load_dwordx4 v[46:49], v[16:17], off offset:3072
	global_load_dwordx4 v[58:61], v[18:19], off offset:2048
	global_load_dwordx4 v[50:53], v[18:19], off offset:3072
	v_mov_b32_e32 v206, v127
	v_mov_b32_e32 v127, v128
	v_mov_b32_e32 v204, v131
	s_waitcnt lgkmcnt(0)
	v_add_f32_e32 v14, v14, v15
	ds_bpermute_b32 v15, v142, v14
	v_mov_b32_e32 v205, v133
	v_mov_b32_e32 v131, v132
	v_mov_b32_e32 v207, v129
	v_mov_b32_e32 v138, v115
	s_waitcnt lgkmcnt(0)
	v_add_f32_e32 v20, v14, v15
	ds_bpermute_b32 v21, v143, v20
	v_add_co_u32_e32 v14, vcc, s41, v16
	s_add_i32 s8, s4, 2
	s_nop 0
	v_addc_co_u32_e32 v15, vcc, 0, v17, vcc
	s_waitcnt lgkmcnt(0)
	v_add_f32_e32 v16, v20, v21
	ds_bpermute_b32 v17, v144, v16
	v_add_co_u32_e32 v18, vcc, s41, v18
	global_load_dwordx4 v[38:41], v[14:15], off
	global_load_dwordx4 v[30:33], v[14:15], off offset:1024
	v_addc_co_u32_e32 v19, vcc, 0, v19, vcc
	s_waitcnt lgkmcnt(0)
	v_add_f32_e32 v20, v16, v17
	ds_bpermute_b32 v21, v145, v20
	global_load_dwordx4 v[42:45], v[18:19], off
	global_load_dwordx4 v[34:37], v[18:19], off offset:1024
	global_load_dwordx4 v[22:25], v[14:15], off offset:2048
	s_nop 0
	global_load_dwordx4 v[14:17], v[14:15], off offset:3072
	s_ashr_i32 s9, s8, 31
	s_waitcnt lgkmcnt(0)
; __device__ __forceinline__ unsigned cvt_pk_bf16(float lo, float hi) { unsigned r; asm volatile("v_cvt_pk_bf16_f32 %0, %1, %2" : "=v"(r) : "v"(lo), "v"(hi)); return r; }
; __device__ __forceinline__ void p6_router(Frame& F) {
;     ...
;                 float rstd = 1.f / sqrtf(wave_sum(s2) * (1.f / DM) + LN_EPS);
;                 s = 0.f;
; #pragma unroll
;                 for (int j = 0; j < 8; ++j) { v[j] = v[j] * rstd * pw[j] + pb[j]; { u32x2 xb; xb.x = cvt_pk_bf16(v[j][0], v[j][1]); xb.y = cvt_pk_bf16(v[j][2], v[j][3]); ((u32x2*)(X1 + (size_t)t * DM))[lane + 64 * j] = xb; } s += (v[j][0] + v[j][1]) + (v[j][2] + v[j][3]); }
;                 mean = wave_sum(s) * (1.f / DM); s2 = 0.f;
	v_add_f32_e32 v78, v20, v21
	global_load_dwordx4 v[26:29], v[18:19], off offset:2048
	s_nop 0
	global_load_dwordx4 v[18:21], v[18:19], off offset:3072
	ds_bpermute_b32 v104, v147, v78
	s_waitcnt lgkmcnt(0)
	v_add_f32_e32 v78, v78, v104
	v_fmamk_f32 v78, v78, 0x3a000000, v148
	v_mul_f32_e32 v104, 0x4f800000, v78
	v_cmp_gt_f32_e32 vcc, s45, v78
	s_nop 1
	v_cndmask_b32_e32 v78, v78, v104, vcc
	v_sqrt_f32_e32 v104, v78
	s_nop 0
	v_add_u32_e32 v106, -1, v104
	v_fma_f32 v114, -v106, v104, v78
	v_cmp_ge_f32_e64 s[0:1], 0, v114
	v_add_u32_e32 v114, 1, v104
	s_nop 0
	v_cndmask_b32_e64 v106, v104, v106, s[0:1]
	v_fma_f32 v104, -v114, v104, v78
	v_cmp_lt_f32_e64 s[0:1], 0, v104
	s_nop 1
	v_cndmask_b32_e64 v104, v106, v114, s[0:1]
	v_mul_f32_e32 v106, 0x37800000, v104
	v_cndmask_b32_e32 v104, v104, v106, vcc
	v_cmp_class_f32_e32 vcc, v78, v149
	s_nop 1
	v_cndmask_b32_e32 v78, v104, v78, vcc
	v_div_scale_f32 v104, s[0:1], v78, v78, 1.0
	v_rcp_f32_e32 v106, v104
	s_lshl_b64 s[0:1], s[8:9], 12
	s_add_u32 s0, s42, s0
	s_addc_u32 s1, s43, s1
	v_fma_f32 v114, -v104, v106, 1.0
	v_fmac_f32_e32 v106, v114, v106
	v_div_scale_f32 v114, vcc, 1.0, v78, 1.0
	v_mul_f32_e32 v116, v114, v106
	v_fma_f32 v118, -v104, v116, v114
	v_fmac_f32_e32 v116, v118, v106
	v_fma_f32 v104, -v104, v116, v114
	v_div_fmas_f32 v104, v104, v106, v116
	v_div_fixup_f32 v78, v104, v78, 1.0
	v_pk_mul_f32 v[126:127], v[126:127], v[78:79] op_sel_hi:[1,0]
	v_pk_mul_f32 v[128:129], v[130:131], v[78:79] op_sel_hi:[1,0]
	s_waitcnt vmcnt(14)
	v_pk_fma_f32 v[132:133], v[72:73], v[126:127], v[12:13]
	v_pk_mul_f32 v[126:127], v[204:205], v[78:79] op_sel_hi:[1,0]
	v_pk_fma_f32 v[134:135], v[70:71], v[128:129], v[10:11]
	v_pk_mul_f32 v[128:129], v[206:207], v[78:79] op_sel_hi:[1,0]
	s_waitcnt vmcnt(12)
	v_pk_fma_f32 v[130:131], v[62:63], v[126:127], v[66:67]
	v_pk_fma_f32 v[128:129], v[64:65], v[128:129], v[68:69]
	v_mov_b32_e32 v126, v130
	v_mov_b32_e32 v127, v134
	v_mov_b32_e32 v204, v131
	v_mov_b32_e32 v205, v135
	v_pk_add_f32 v[126:127], v[126:127], v[204:205]
	v_mov_b32_e32 v204, v129
	v_mov_b32_e32 v205, v133
	v_mov_b32_e32 v206, v128
	v_mov_b32_e32 v207, v132
	v_pk_add_f32 v[204:205], v[204:205], v[206:207]
	v_mov_b32_e32 v116, v119
	v_pk_add_f32 v[126:127], v[126:127], v[204:205]
	v_pk_mul_f32 v[114:115], v[138:139], v[78:79] op_sel_hi:[1,0]
	v_add_f32_e32 v104, 0, v127
	v_add_f32_e32 v205, v126, v104
	v_pk_mul_f32 v[126:127], v[124:125], v[78:79] op_sel_hi:[1,0]
	v_pk_mul_f32 v[124:125], v[202:203], v[78:79] op_sel_hi:[1,0]
	s_waitcnt vmcnt(9)
	v_pk_fma_f32 v[126:127], v[54:55], v[126:127], v[58:59]
	v_pk_fma_f32 v[124:125], v[56:57], v[124:125], v[60:61]
	v_mov_b32_e32 v202, v126
	v_mov_b32_e32 v203, v125
	v_pk_mov_b32 v[206:207], v[126:127], v[124:125] op_sel:[1,0]
	v_pk_mul_f32 v[116:117], v[116:117], v[78:79] op_sel_hi:[1,0]
	v_pk_add_f32 v[202:203], v[202:203], v[206:207]
	v_pk_mul_f32 v[206:207], v[120:121], v[78:79] op_sel_hi:[1,0]
	v_pk_mul_f32 v[120:121], v[122:123], v[78:79] op_sel_hi:[1,0]
	v_pk_add_f32 v[202:203], v[202:203], v[202:203] op_sel_hi:[0,1]
	s_waitcnt vmcnt(8)
	v_pk_fma_f32 v[120:121], v[48:49], v[120:121], v[52:53]
	v_pk_fma_f32 v[122:123], v[46:47], v[206:207], v[50:51]
	s_waitcnt vmcnt(5)
	v_pk_fma_f32 v[116:117], v[40:41], v[116:117], v[44:45]
	v_pk_fma_f32 v[118:119], v[38:39], v[114:115], v[42:43]
	v_add_f32_e32 v207, v122, v123
	v_add_f32_e32 v211, v121, v120
	v_mov_b32_e32 v206, v118
	v_mov_b32_e32 v210, v119
	v_mov_b32_e32 v202, v117
	v_mov_b32_e32 v204, v116
	v_pk_add_f32 v[114:115], v[206:207], v[210:211]
	v_pk_add_f32 v[138:139], v[202:203], v[204:205]
	v_mov_b32_e32 v104, v107
	v_pk_add_f32 v[114:115], v[114:115], v[138:139]
	v_pk_mul_f32 v[136:137], v[136:137], v[78:79] op_sel_hi:[1,0]
	v_pk_add_f32 v[138:139], v[114:115], v[114:115] op_sel_hi:[0,1]
	v_pk_mul_f32 v[114:115], v[112:113], v[78:79] op_sel_hi:[1,0]
	v_pk_mul_f32 v[112:113], v[140:141], v[78:79] op_sel_hi:[1,0]
	s_waitcnt vmcnt(4)
	v_pk_fma_f32 v[114:115], v[30:31], v[114:115], v[34:35]
	v_pk_fma_f32 v[112:113], v[32:33], v[112:113], v[36:37]
	v_mov_b32_e32 v140, v114
	v_mov_b32_e32 v141, v113
	v_pk_mov_b32 v[202:203], v[114:115], v[112:113] op_sel:[1,0]
	v_pk_mul_f32 v[104:105], v[104:105], v[78:79] op_sel_hi:[1,0]
	v_pk_add_f32 v[140:141], v[140:141], v[202:203]
	v_pk_mul_f32 v[202:203], v[108:109], v[78:79] op_sel_hi:[1,0]
	v_pk_mul_f32 v[108:109], v[110:111], v[78:79] op_sel_hi:[1,0]
	v_pk_add_f32 v[140:141], v[140:141], v[140:141] op_sel_hi:[0,1]
	s_waitcnt vmcnt(1)
	v_pk_fma_f32 v[108:109], v[24:25], v[108:109], v[28:29]
	v_pk_fma_f32 v[110:111], v[22:23], v[202:203], v[26:27]
	s_waitcnt vmcnt(0)
	v_pk_fma_f32 v[104:105], v[16:17], v[104:105], v[20:21]
	v_pk_fma_f32 v[106:107], v[14:15], v[136:137], v[18:19]
	v_add_f32_e32 v203, v110, v111
	v_add_f32_e32 v205, v109, v108
	v_mov_b32_e32 v202, v106
	v_mov_b32_e32 v204, v107
	v_mov_b32_e32 v140, v105
	v_mov_b32_e32 v138, v104
	v_pk_add_f32 v[136:137], v[202:203], v[204:205]
	v_pk_add_f32 v[138:139], v[140:141], v[138:139]
	v_cvt_pk_bf16_f32 v208, v134, v135
	v_cvt_pk_bf16_f32 v209, v132, v133
	global_store_dwordx2 v146, v[208:209], s[0:1] nt
	v_pk_add_f32 v[136:137], v[136:137], v[138:139]
	s_nop 0
	v_add_f32_e32 v78, v136, v137
	ds_bpermute_b32 v137, v1, v78
	v_cvt_pk_bf16_f32 v136, v130, v131
	s_waitcnt lgkmcnt(0)
	v_add_f32_e32 v78, v78, v137
	ds_bpermute_b32 v138, v142, v78
	v_cvt_pk_bf16_f32 v137, v128, v129
	global_store_dwordx2 v146, v[136:137], s[0:1] offset:512 nt
	v_cvt_pk_bf16_f32 v136, v126, v127
	v_cvt_pk_bf16_f32 v137, v124, v125
	s_waitcnt lgkmcnt(0)
; __device__ __forceinline__ unsigned cvt_pk_bf16(float lo, float hi) { unsigned r; asm volatile("v_cvt_pk_bf16_f32 %0, %1, %2" : "=v"(r) : "v"(lo), "v"(hi)); return r; }
; __device__ __forceinline__ void p6_router(Frame& F) {
;     ...
;                 for (int j = 0; j < 8; ++j) { v[j] = v[j] * rstd * pw[j] + pb[j]; { u32x2 xb; xb.x = cvt_pk_bf16(v[j][0], v[j][1]); xb.y = cvt_pk_bf16(v[j][2], v[j][3]); ((u32x2*)(X1 + (size_t)t * DM))[lane + 64 * j] = xb; } s += (v[j][0] + v[j][1]) + (v[j][2] + v[j][3]); }
;                 mean = wave_sum(s) * (1.f / DM); s2 = 0.f;
; #pragma unroll
;                 for (int j = 0; j < 8; ++j) { v[j] = v[j] - mean; s2 += (v[j][0] * v[j][0] + v[j][1] * v[j][1]) + (v[j][2] * v[j][2] + v[j][3] * v[j][3]); }
;                 rstd = 1.f / sqrtf(wave_sum(s2) * (1.f / DM) + LN_EPS);
	v_add_f32_e32 v78, v78, v138
	ds_bpermute_b32 v138, v143, v78
	global_store_dwordx2 v146, v[136:137], s[0:1] offset:1024 nt
	v_cvt_pk_bf16_f32 v136, v122, v123
	v_cvt_pk_bf16_f32 v137, v120, v121
	global_store_dwordx2 v146, v[136:137], s[0:1] offset:1536 nt
	s_waitcnt lgkmcnt(0)
	v_add_f32_e32 v78, v78, v138
	ds_bpermute_b32 v138, v144, v78
	v_cvt_pk_bf16_f32 v136, v118, v119
	v_cvt_pk_bf16_f32 v137, v116, v117
	global_store_dwordx2 v146, v[136:137], s[0:1] offset:2048 nt
	v_cvt_pk_bf16_f32 v136, v114, v115
	s_waitcnt lgkmcnt(0)
	v_add_f32_e32 v78, v78, v138
	ds_bpermute_b32 v138, v145, v78
	v_cvt_pk_bf16_f32 v137, v112, v113
	global_store_dwordx2 v146, v[136:137], s[0:1] offset:2560 nt
	v_cvt_pk_bf16_f32 v136, v110, v111
	v_cvt_pk_bf16_f32 v137, v108, v109
	s_waitcnt lgkmcnt(0)
	v_add_f32_e32 v78, v78, v138
	ds_bpermute_b32 v138, v147, v78
	global_store_dwordx2 v146, v[136:137], s[0:1] offset:3072 nt
	v_cvt_pk_bf16_f32 v136, v106, v107
	v_cvt_pk_bf16_f32 v137, v104, v105
	global_store_dwordx2 v146, v[136:137], s[0:1] offset:3584 nt
	s_waitcnt lgkmcnt(0)
	v_add_f32_e32 v204, v78, v138
	v_fmamk_f32 v135, v204, 0xba000000, v135
	v_fmamk_f32 v131, v204, 0xba000000, v131
	v_fmamk_f32 v133, v204, 0xba000000, v133
	v_fmac_f32_e32 v134, 0xba000000, v204
	v_fmamk_f32 v129, v204, 0xba000000, v129
	v_fmac_f32_e32 v130, 0xba000000, v204
	v_mov_b32_e32 v138, v135
	v_mov_b32_e32 v139, v131
	v_fmac_f32_e32 v132, 0xba000000, v204
	v_fmac_f32_e32 v128, 0xba000000, v204
	v_mov_b32_e32 v136, v134
	v_mov_b32_e32 v137, v130
	v_pk_mul_f32 v[138:139], v[138:139], v[138:139]
	v_mov_b32_e32 v140, v133
	v_mov_b32_e32 v141, v129
	v_pk_fma_f32 v[136:137], v[136:137], v[136:137], v[138:139]
	v_mov_b32_e32 v138, v132
	v_mov_b32_e32 v139, v128
	v_pk_mul_f32 v[140:141], v[140:141], v[140:141]
	v_fmamk_f32 v127, v204, 0xba000000, v127
	v_pk_fma_f32 v[138:139], v[138:139], v[138:139], v[140:141]
	v_fmac_f32_e32 v126, 0xba000000, v204
	v_fmamk_f32 v125, v204, 0xba000000, v125
	v_fmac_f32_e32 v124, 0xba000000, v204
	v_pk_add_f32 v[136:137], v[136:137], v[138:139]
	v_pk_mul_f32 v[138:139], v[124:125], v[124:125]
	v_pk_mul_f32 v[140:141], v[126:127], v[126:127]
	v_fmac_f32_e32 v122, 0xba000000, v204
	v_pk_mov_b32 v[202:203], v[140:141], v[138:139] op_sel:[1,0]
	v_mov_b32_e32 v141, v139
	v_fmamk_f32 v123, v204, 0xba000000, v123
	v_fmac_f32_e32 v120, 0xba000000, v204
	v_mul_f32_e32 v78, v122, v122
	v_pk_add_f32 v[138:139], v[202:203], v[140:141]
	v_fmamk_f32 v121, v204, 0xba000000, v121
	v_pk_fma_f32 v[140:141], v[122:123], v[122:123], v[78:79] op_sel_hi:[1,1,0]
	v_mul_f32_e32 v78, v120, v120
	v_pk_add_f32 v[136:137], v[136:137], v[136:137] op_sel_hi:[0,1]
	v_pk_add_f32 v[138:139], v[138:139], v[138:139] op_sel_hi:[0,1]
	v_pk_fma_f32 v[202:203], v[120:121], v[120:121], v[78:79] op_sel_hi:[1,1,0]
	v_fmamk_f32 v117, v204, 0xba000000, v117
	v_fmac_f32_e32 v116, 0xba000000, v204
	v_fmamk_f32 v119, v204, 0xba000000, v119
	v_fmac_f32_e32 v118, 0xba000000, v204
	v_mul_f32_e32 v140, v118, v118
	v_mul_f32_e32 v202, v119, v119
	v_mul_f32_e32 v138, v116, v116
	v_mul_f32_e32 v136, v117, v117
	v_pk_add_f32 v[140:141], v[140:141], v[202:203]
	v_pk_add_f32 v[136:137], v[138:139], v[136:137]
	v_fmamk_f32 v115, v204, 0xba000000, v115
	v_pk_add_f32 v[136:137], v[140:141], v[136:137]
	v_fmac_f32_e32 v114, 0xba000000, v204
	v_fmamk_f32 v113, v204, 0xba000000, v113
	v_fmac_f32_e32 v112, 0xba000000, v204
	v_pk_add_f32 v[140:141], v[136:137], v[136:137] op_sel_hi:[0,1]
	v_pk_mul_f32 v[136:137], v[112:113], v[112:113]
	v_pk_mul_f32 v[138:139], v[114:115], v[114:115]
	v_fmac_f32_e32 v110, 0xba000000, v204
	v_pk_mov_b32 v[202:203], v[138:139], v[136:137] op_sel:[1,0]
	v_mov_b32_e32 v139, v137
	v_pk_add_f32 v[136:137], v[202:203], v[138:139]
	v_fmamk_f32 v111, v204, 0xba000000, v111
	v_fmac_f32_e32 v108, 0xba000000, v204
	v_mul_f32_e32 v78, v110, v110
	v_pk_add_f32 v[206:207], v[136:137], v[136:137] op_sel_hi:[0,1]
	v_fmamk_f32 v109, v204, 0xba000000, v109
	v_pk_fma_f32 v[136:137], v[110:111], v[110:111], v[78:79] op_sel_hi:[1,1,0]
	v_mul_f32_e32 v78, v108, v108
	v_pk_fma_f32 v[138:139], v[108:109], v[108:109], v[78:79] op_sel_hi:[1,1,0]
	v_fmamk_f32 v107, v204, 0xba000000, v107
	v_fmac_f32_e32 v106, 0xba000000, v204
	v_mul_f32_e32 v136, v106, v106
	v_mul_f32_e32 v138, v107, v107
	v_pk_add_f32 v[208:209], v[136:137], v[138:139]
	v_mov_b32_e32 v136, v170
	v_fmamk_f32 v105, v204, 0xba000000, v105
	v_ashrrev_i32_e32 v137, 31, v136
	v_lshlrev_b64 v[136:137], 4, v[136:137]
	v_lshl_add_u64 v[210:211], s[16:17], 0, v[136:137]
	v_fmac_f32_e32 v104, 0xba000000, v204
	v_lshl_add_u64 v[212:213], s[20:21], 0, v[136:137]
	global_load_dwordx4 v[136:139], v[210:211], off
	global_load_dwordx4 v[202:205], v[212:213], off
	v_mul_f32_e32 v206, v104, v104
	v_mul_f32_e32 v140, v105, v105
	v_pk_add_f32 v[140:141], v[206:207], v[140:141]
	s_waitcnt vmcnt(0)
	v_pk_add_f32 v[202:203], v[202:203], 1.0 op_sel_hi:[1,0]
	v_pk_add_f32 v[140:141], v[208:209], v[140:141]
	s_nop 0
	v_add_f32_e32 v78, v140, v141
	ds_bpermute_b32 v140, v1, v78
	s_waitcnt lgkmcnt(0)
	v_add_f32_e32 v78, v78, v140
	ds_bpermute_b32 v140, v142, v78
	s_waitcnt lgkmcnt(0)
	v_add_f32_e32 v78, v78, v140
	ds_bpermute_b32 v140, v143, v78
	s_waitcnt lgkmcnt(0)
	v_add_f32_e32 v78, v78, v140
	ds_bpermute_b32 v140, v144, v78
	s_waitcnt lgkmcnt(0)
	v_add_f32_e32 v78, v78, v140
	ds_bpermute_b32 v140, v145, v78
	s_waitcnt lgkmcnt(0)
	v_add_f32_e32 v78, v78, v140
	ds_bpermute_b32 v140, v147, v78
	s_waitcnt lgkmcnt(0)
; #define LAS __attribute__((address_space(3)))
; __device__ __forceinline__ unsigned cvt_pk_bf16(float lo, float hi) { unsigned r; asm volatile("v_cvt_pk_bf16_f32 %0, %1, %2" : "=v"(r) : "v"(lo), "v"(hi)); return r; }
; __device__ __forceinline__ unsigned pk4_fp8(float a, float b, float c, float d) { int w = 0; w = __builtin_amdgcn_cvt_pk_fp8_f32(a, b, w, false); w = __builtin_amdgcn_cvt_pk_fp8_f32(c, d, w, true); return (unsigned)w; }
; __device__ __forceinline__ float bf_lo(unsigned w) { return __uint_as_float(w << 16); }
; __device__ __forceinline__ float bf_hi(unsigned w) { return __uint_as_float(w & 0xffff0000u); }
; __device__ __forceinline__ void p6_router(Frame& F) {
;     ...
;                 rstd = 1.f / sqrtf(wave_sum(s2) * (1.f / DM) + LN_EPS);
;                 int loq = lane; asm volatile("" : "+v"(loq));
; #pragma unroll
;                 for (int j = 0; j < 8; ++j) { const f32x4 sh = ((const f32x4*)(mod + (size_t)b * 12288 + 6144))[loq + 64 * j], sc = ((const f32x4*)(mod + (size_t)b * 12288 + 8192))[loq + 64 * j];
;                     const f32x4 y = v[j] * rstd * (sc + 1.0f) + sh;
;                     u32x2 wh; wh.x = cvt_pk_bf16(y[0], y[1]); wh.y = cvt_pk_bf16(y[2], y[3]);
;                     const f32x4 yl = {y[0] - bf_lo(wh.x), y[1] - bf_hi(wh.x), y[2] - bf_lo(wh.y), y[3] - bf_hi(wh.y)};
;                     u32x2 wl; wl.x = cvt_pk_bf16(yl[0], yl[1]); wl.y = cvt_pk_bf16(yl[2], yl[3]);
;                     { const int r = 2 * wave + q; LAS unsigned char* rowp = F.lds + r * 4096 + ((((lane >> 1) + 32 * j) ^ r) << 4) + (lane & 1) * 8;
;                       *(LAS u32x2*)rowp = wh; *(LAS u32x2*)(rowp + 65536) = wl; }
;                     U2F[(size_t)t * (DM / 4) + lane + 64 * j] = pk4_fp8(y[0], y[1], y[2], y[3]); }
	v_add_f32_e32 v78, v78, v140
	v_fmamk_f32 v78, v78, 0x3a000000, v148
	v_mul_f32_e32 v140, 0x4f800000, v78
	v_cmp_gt_f32_e32 vcc, s45, v78
	s_nop 1
	v_cndmask_b32_e32 v78, v78, v140, vcc
	v_sqrt_f32_e32 v140, v78
	s_nop 0
	v_add_u32_e32 v141, -1, v140
	v_fma_f32 v206, -v141, v140, v78
	v_cmp_ge_f32_e64 s[0:1], 0, v206
	v_add_u32_e32 v206, 1, v140
	s_nop 0
	v_cndmask_b32_e64 v141, v140, v141, s[0:1]
	v_fma_f32 v140, -v206, v140, v78
	v_cmp_lt_f32_e64 s[0:1], 0, v140
	s_nop 1
	v_cndmask_b32_e64 v140, v141, v206, s[0:1]
	v_mul_f32_e32 v141, 0x37800000, v140
	v_cndmask_b32_e32 v140, v140, v141, vcc
	v_cmp_class_f32_e32 vcc, v78, v149
	s_nop 1
	v_cndmask_b32_e32 v78, v140, v78, vcc
	v_div_scale_f32 v140, s[0:1], v78, v78, 1.0
	v_rcp_f32_e32 v141, v140
	s_lshl_b64 s[0:1], s[8:9], 11
	s_add_u32 s8, s40, s0
	s_addc_u32 s9, s44, s1
	v_fma_f32 v206, -v140, v141, 1.0
	v_fmac_f32_e32 v141, v206, v141
	v_div_scale_f32 v206, vcc, 1.0, v78, 1.0
	v_mul_f32_e32 v207, v206, v141
	v_fma_f32 v208, -v140, v207, v206
	v_fmac_f32_e32 v207, v208, v141
	v_fma_f32 v140, -v140, v207, v206
	v_div_fmas_f32 v140, v140, v141, v207
	v_div_fixup_f32 v78, v140, v78, 1.0
	v_pk_mul_f32 v[134:135], v[134:135], v[78:79] op_sel_hi:[1,0]
	v_pk_mul_f32 v[132:133], v[132:133], v[78:79] op_sel_hi:[1,0]
	v_pk_add_f32 v[140:141], v[204:205], 1.0 op_sel_hi:[1,0]
	v_pk_fma_f32 v[134:135], v[202:203], v[134:135], v[136:137]
	v_pk_fma_f32 v[132:133], v[140:141], v[132:133], v[138:139]
	v_mov_b32_e32 v139, v79
	v_cvt_pk_fp8_f32 v139, v134, v135
	v_cvt_pk_bf16_f32 v140, v134, v135
	v_cvt_pk_bf16_f32 v141, v132, v133
	v_pk_mul_f32 v[130:131], v[130:131], v[78:79] op_sel_hi:[1,0]
	v_cvt_pk_fp8_f32 v139, v132, v133 op_sel:[0,0,1]
	v_lshlrev_b32_e32 v136, 16, v140
	v_sub_f32_e32 v136, v134, v136
	v_and_b32_e32 v137, 0xffff0000, v140
	v_lshlrev_b32_e32 v138, 16, v141
	v_and_b32_e32 v134, 0xffff0000, v141
	v_sub_f32_e32 v137, v135, v137
	v_sub_f32_e32 v138, v132, v138
	v_sub_f32_e32 v134, v133, v134
	v_cvt_pk_bf16_f32 v202, v136, v137
	v_cvt_pk_bf16_f32 v203, v138, v134
	global_store_dword v150, v139, s[8:9] nt
	global_load_dwordx4 v[132:135], v[212:213], off offset:1024
	s_nop 0
	global_load_dwordx4 v[136:139], v[210:211], off offset:1024
	v_pk_mul_f32 v[128:129], v[128:129], v[78:79] op_sel_hi:[1,0]
	ds_write_b64 v159, v[140:141]
	ds_write_b64 v160, v[202:203]
	v_pk_mul_f32 v[126:127], v[126:127], v[78:79] op_sel_hi:[1,0]
	v_pk_mul_f32 v[124:125], v[124:125], v[78:79] op_sel_hi:[1,0]
	v_pk_mul_f32 v[122:123], v[122:123], v[78:79] op_sel_hi:[1,0]
	v_pk_mul_f32 v[120:121], v[120:121], v[78:79] op_sel_hi:[1,0]
	v_pk_mul_f32 v[118:119], v[118:119], v[78:79] op_sel_hi:[1,0]
	v_pk_mul_f32 v[116:117], v[116:117], v[78:79] op_sel_hi:[1,0]
	v_pk_mul_f32 v[112:113], v[112:113], v[78:79] op_sel_hi:[1,0]
	v_pk_mul_f32 v[110:111], v[110:111], v[78:79] op_sel_hi:[1,0]
	v_pk_mul_f32 v[108:109], v[108:109], v[78:79] op_sel_hi:[1,0]
	v_pk_mul_f32 v[106:107], v[106:107], v[78:79] op_sel_hi:[1,0]
	v_pk_mul_f32 v[104:105], v[104:105], v[78:79] op_sel_hi:[1,0]
	s_add_i32 s4, s4, 3
	s_ashr_i32 s5, s4, 31
	s_waitcnt vmcnt(1)
	v_pk_add_f32 v[134:135], v[134:135], 1.0 op_sel_hi:[1,0]
	v_pk_add_f32 v[132:133], v[132:133], 1.0 op_sel_hi:[1,0]
	s_waitcnt vmcnt(0)
	v_pk_fma_f32 v[128:129], v[134:135], v[128:129], v[138:139]
	v_pk_fma_f32 v[130:131], v[132:133], v[130:131], v[136:137]
	v_mov_b32_e32 v134, v79
	v_cvt_pk_fp8_f32 v134, v130, v131
	v_cvt_pk_bf16_f32 v136, v130, v131
	v_cvt_pk_bf16_f32 v137, v128, v129
	v_cvt_pk_fp8_f32 v134, v128, v129 op_sel:[0,0,1]
	v_lshlrev_b32_e32 v132, 16, v136
	v_and_b32_e32 v133, 0xffff0000, v136
	v_sub_f32_e32 v132, v130, v132
	v_sub_f32_e32 v133, v131, v133
	v_lshlrev_b32_e32 v130, 16, v137
	v_and_b32_e32 v131, 0xffff0000, v137
	v_sub_f32_e32 v130, v128, v130
	v_sub_f32_e32 v128, v129, v131
	v_cvt_pk_bf16_f32 v138, v132, v133
	v_cvt_pk_bf16_f32 v139, v130, v128
	global_store_dword v150, v134, s[8:9] offset:256 nt
	global_load_dwordx4 v[128:131], v[212:213], off offset:2048
	s_nop 0
	global_load_dwordx4 v[132:135], v[210:211], off offset:2048
	ds_write_b64 v161, v[136:137]
	ds_write_b64 v162, v[138:139]
	v_and_b32_e32 v137, 0xffff0000, v102
	v_and_b32_e32 v136, 0xffff0000, v100
	s_waitcnt vmcnt(1)
	v_pk_add_f32 v[130:131], v[130:131], 1.0 op_sel_hi:[1,0]
	v_pk_add_f32 v[128:129], v[128:129], 1.0 op_sel_hi:[1,0]
	s_waitcnt vmcnt(0)
	v_pk_fma_f32 v[124:125], v[130:131], v[124:125], v[134:135]
	v_pk_fma_f32 v[126:127], v[128:129], v[126:127], v[132:133]
	v_mov_b32_e32 v130, v79
	v_cvt_pk_fp8_f32 v130, v126, v127
	v_cvt_pk_bf16_f32 v132, v126, v127
	v_cvt_pk_bf16_f32 v133, v124, v125
	v_cvt_pk_fp8_f32 v130, v124, v125 op_sel:[0,0,1]
	v_lshlrev_b32_e32 v128, 16, v132
	v_and_b32_e32 v129, 0xffff0000, v132
	v_sub_f32_e32 v128, v126, v128
	v_sub_f32_e32 v129, v127, v129
	v_lshlrev_b32_e32 v126, 16, v133
	v_and_b32_e32 v127, 0xffff0000, v133
	v_sub_f32_e32 v126, v124, v126
	v_sub_f32_e32 v124, v125, v127
	v_cvt_pk_bf16_f32 v134, v128, v129
	v_cvt_pk_bf16_f32 v135, v126, v124
	global_store_dword v150, v130, s[8:9] offset:512 nt
	global_load_dwordx4 v[124:127], v[212:213], off offset:3072
	s_nop 0
	global_load_dwordx4 v[128:131], v[210:211], off offset:3072
	ds_write_b64 v165, v[132:133]
	ds_write_b64 v166, v[134:135]
	v_mov_b32_e32 v132, v79
	v_lshlrev_b32_e32 v135, 16, v102
	v_lshlrev_b32_e32 v134, 16, v100
	v_lshlrev_b32_e32 v133, 16, v103
	s_waitcnt vmcnt(1)
	v_pk_add_f32 v[126:127], v[126:127], 1.0 op_sel_hi:[1,0]
	v_pk_add_f32 v[124:125], v[124:125], 1.0 op_sel_hi:[1,0]
	s_waitcnt vmcnt(0)
; #define LAS __attribute__((address_space(3)))
; __device__ __forceinline__ unsigned cvt_pk_bf16(float lo, float hi) { unsigned r; asm volatile("v_cvt_pk_bf16_f32 %0, %1, %2" : "=v"(r) : "v"(lo), "v"(hi)); return r; }
; __device__ __forceinline__ unsigned pk4_fp8(float a, float b, float c, float d) { int w = 0; w = __builtin_amdgcn_cvt_pk_fp8_f32(a, b, w, false); w = __builtin_amdgcn_cvt_pk_fp8_f32(c, d, w, true); return (unsigned)w; }
; __device__ __forceinline__ float bf_lo(unsigned w) { return __uint_as_float(w << 16); }
; __device__ __forceinline__ float bf_hi(unsigned w) { return __uint_as_float(w & 0xffff0000u); }
; __device__ __forceinline__ void p6_router(Frame& F) {
;     ...
;                 for (int j = 0; j < 8; ++j) { const u32x2 zb = zr[q][j]; v[j] = (f32x4){bf_lo(zb.x), bf_hi(zb.x), bf_lo(zb.y), bf_hi(zb.y)}; s += (v[j][0] + v[j][1]) + (v[j][2] + v[j][3]); }
;     ...
;                 for (int j = 0; j < 8; ++j) { const f32x4 sh = ((const f32x4*)(mod + (size_t)b * 12288 + 6144))[loq + 64 * j], sc = ((const f32x4*)(mod + (size_t)b * 12288 + 8192))[loq + 64 * j];
;                     const f32x4 y = v[j] * rstd * (sc + 1.0f) + sh;
;                     u32x2 wh; wh.x = cvt_pk_bf16(y[0], y[1]); wh.y = cvt_pk_bf16(y[2], y[3]);
;                     const f32x4 yl = {y[0] - bf_lo(wh.x), y[1] - bf_hi(wh.x), y[2] - bf_lo(wh.y), y[3] - bf_hi(wh.y)};
;                     u32x2 wl; wl.x = cvt_pk_bf16(yl[0], yl[1]); wl.y = cvt_pk_bf16(yl[2], yl[3]);
;                     { const int r = 2 * wave + q; LAS unsigned char* rowp = F.lds + r * 4096 + ((((lane >> 1) + 32 * j) ^ r) << 4) + (lane & 1) * 8;
;                       *(LAS u32x2*)rowp = wh; *(LAS u32x2*)(rowp + 65536) = wl; }
;                     U2F[(size_t)t * (DM / 4) + lane + 64 * j] = pk4_fp8(y[0], y[1], y[2], y[3]); }
	v_pk_fma_f32 v[120:121], v[120:121], v[126:127], v[130:131]
	v_pk_fma_f32 v[122:123], v[122:123], v[124:125], v[128:129]
	v_mov_b32_e32 v126, v79
	v_cvt_pk_fp8_f32 v126, v122, v123
	v_cvt_pk_bf16_f32 v138, v122, v123
	v_cvt_pk_bf16_f32 v139, v120, v121
	v_cvt_pk_fp8_f32 v126, v120, v121 op_sel:[0,0,1]
	v_lshlrev_b32_e32 v124, 16, v138
	v_and_b32_e32 v125, 0xffff0000, v138
	v_sub_f32_e32 v124, v122, v124
	v_sub_f32_e32 v125, v123, v125
	v_lshlrev_b32_e32 v122, 16, v139
	v_and_b32_e32 v123, 0xffff0000, v139
	v_sub_f32_e32 v122, v120, v122
	v_sub_f32_e32 v120, v121, v123
	v_cvt_pk_bf16_f32 v140, v124, v125
	v_cvt_pk_bf16_f32 v141, v122, v120
	v_add_co_u32_e32 v120, vcc, s41, v212
	global_store_dword v150, v126, s[8:9] offset:768 nt
	s_nop 0
	v_addc_co_u32_e32 v121, vcc, 0, v213, vcc
	v_add_co_u32_e32 v122, vcc, s41, v210
	global_load_dwordx4 v[124:127], v[120:121], off
	s_nop 0
	v_addc_co_u32_e32 v123, vcc, 0, v211, vcc
	global_load_dwordx4 v[128:131], v[122:123], off
	ds_write_b64 v155, v[138:139]
	ds_write_b64 v156, v[140:141]
	v_and_b32_e32 v139, 0xffff0000, v103
	v_and_b32_e32 v138, 0xffff0000, v101
	v_and_b32_e32 v211, 0xffff0000, v99
	v_and_b32_e32 v210, 0xffff0000, v98
	s_waitcnt vmcnt(1)
	v_pk_add_f32 v[124:125], v[124:125], 1.0 op_sel_hi:[1,0]
	v_pk_add_f32 v[126:127], v[126:127], 1.0 op_sel_hi:[1,0]
	s_waitcnt vmcnt(0)
	v_pk_fma_f32 v[118:119], v[118:119], v[124:125], v[128:129]
	s_nop 0
	v_cvt_pk_fp8_f32 v132, v118, v119
	v_pk_fma_f32 v[116:117], v[116:117], v[126:127], v[130:131]
	v_cvt_pk_bf16_f32 v140, v118, v119
	v_lshlrev_b32_e32 v131, 16, v99
	v_cvt_pk_fp8_f32 v132, v116, v117 op_sel:[0,0,1]
	v_cvt_pk_bf16_f32 v141, v116, v117
	v_lshlrev_b32_e32 v100, 16, v140
	v_and_b32_e32 v102, 0xffff0000, v140
	v_lshlrev_b32_e32 v124, 16, v141
	v_and_b32_e32 v125, 0xffff0000, v141
	v_sub_f32_e32 v100, v118, v100
	v_sub_f32_e32 v102, v119, v102
	v_sub_f32_e32 v118, v116, v124
	v_sub_f32_e32 v116, v117, v125
	v_cvt_pk_bf16_f32 v160, v100, v102
	v_cvt_pk_bf16_f32 v161, v118, v116
	global_store_dword v150, v132, s[8:9] offset:1024 nt
	global_load_dwordx4 v[202:205], v[122:123], off offset:1024
	global_load_dwordx4 v[206:209], v[120:121], off offset:1024
	v_lshlrev_b32_e32 v132, 16, v101
	v_pk_add_f32 v[100:101], v[134:135], v[136:137]
	v_pk_add_f32 v[102:103], v[132:133], v[138:139]
	v_lshlrev_b32_e32 v130, 16, v98
	v_pk_add_f32 v[100:101], v[100:101], v[102:103]
	v_pk_add_f32 v[98:99], v[130:131], v[210:211]
	v_add_f32_e32 v100, 0, v100
	v_add_f32_e32 v100, v100, v101
	v_lshlrev_b32_e32 v126, 16, v96
	v_and_b32_e32 v127, 0xffff0000, v96
	v_lshlrev_b32_e32 v128, 16, v97
	v_and_b32_e32 v129, 0xffff0000, v97
	v_lshlrev_b32_e32 v101, 16, v94
	v_and_b32_e32 v125, 0xffff0000, v94
	v_lshlrev_b32_e32 v119, 16, v95
	v_and_b32_e32 v117, 0xffff0000, v95
	v_pk_add_f32 v[94:95], v[98:99], v[98:99] op_sel:[0,1] op_sel_hi:[1,0]
	v_add_f32_e32 v118, v126, v127
	v_add_f32_e32 v116, v128, v129
	v_mov_b32_e32 v95, v125
	v_pk_add_f32 v[94:95], v[100:101], v[94:95]
	v_pk_add_f32 v[96:97], v[118:119], v[116:117]
	v_lshlrev_b32_e32 v103, 16, v93
	v_lshlrev_b32_e32 v102, 16, v92
	v_pk_add_f32 v[212:213], v[94:95], v[96:97]
	v_pk_add_f32 v[216:217], v[102:103], v[214:215]
	v_lshlrev_b32_e32 v96, 16, v90
	v_and_b32_e32 v97, 0xffff0000, v90
	v_lshlrev_b32_e32 v98, 16, v91
	v_and_b32_e32 v99, 0xffff0000, v91
	v_lshlrev_b32_e32 v94, 16, v88
	v_and_b32_e32 v95, 0xffff0000, v88
	v_lshlrev_b32_e32 v93, 16, v89
	v_and_b32_e32 v91, 0xffff0000, v89
	v_pk_add_f32 v[88:89], v[212:213], v[212:213] op_sel:[0,1] op_sel_hi:[1,0]
	v_pk_add_f32 v[212:213], v[216:217], v[216:217] op_sel:[0,1] op_sel_hi:[1,0]
	v_add_f32_e32 v92, v96, v97
	v_add_f32_e32 v90, v98, v99
	v_mov_b32_e32 v89, v94
	v_mov_b32_e32 v213, v95
	v_pk_add_f32 v[88:89], v[88:89], v[212:213]
	v_pk_add_f32 v[212:213], v[92:93], v[90:91]
	ds_write_b64 v169, v[140:141]
	ds_write_b64 v171, v[160:161]
	v_pk_add_f32 v[88:89], v[88:89], v[212:213]
	v_mov_b32_e32 v90, v79
	v_add_f32_e32 v88, v88, v89
	ds_bpermute_b32 v89, v1, v88
	s_waitcnt lgkmcnt(0)
	v_add_f32_e32 v88, v88, v89
	ds_bpermute_b32 v89, v142, v88
	s_waitcnt lgkmcnt(0)
	v_add_f32_e32 v88, v88, v89
	ds_bpermute_b32 v89, v143, v88
	s_waitcnt lgkmcnt(0)
	v_add_f32_e32 v88, v88, v89
	ds_bpermute_b32 v89, v144, v88
	s_waitcnt lgkmcnt(0)
	v_add_f32_e32 v92, v88, v89
	v_pk_mul_f32 v[88:89], v[114:115], v[78:79] op_sel_hi:[1,0]
	ds_bpermute_b32 v100, v145, v92
	s_waitcnt vmcnt(0)
	v_pk_add_f32 v[140:141], v[206:207], 1.0 op_sel_hi:[1,0]
	s_nop 0
	v_pk_fma_f32 v[88:89], v[88:89], v[140:141], v[202:203]
	v_pk_add_f32 v[114:115], v[208:209], 1.0 op_sel_hi:[1,0]
	v_cvt_pk_fp8_f32 v90, v88, v89
	v_pk_fma_f32 v[112:113], v[112:113], v[114:115], v[204:205]
	v_cvt_pk_bf16_f32 v140, v88, v89
	s_nop 0
	v_cvt_pk_fp8_f32 v90, v112, v113 op_sel:[0,0,1]
	v_cvt_pk_bf16_f32 v141, v112, v113
	v_lshlrev_b32_e32 v114, 16, v140
	v_and_b32_e32 v115, 0xffff0000, v140
	v_lshlrev_b32_e32 v116, 16, v141
	v_and_b32_e32 v118, 0xffff0000, v141
	v_sub_f32_e32 v88, v88, v114
	v_sub_f32_e32 v89, v89, v115
	v_sub_f32_e32 v114, v112, v116
	v_sub_f32_e32 v112, v113, v118
	v_cvt_pk_bf16_f32 v160, v88, v89
	v_cvt_pk_bf16_f32 v161, v114, v112
	global_store_dword v150, v90, s[8:9] offset:1280 nt
	global_load_dwordx4 v[112:115], v[120:121], off offset:2048
	global_load_dwordx4 v[202:205], v[122:123], off offset:2048
	s_waitcnt lgkmcnt(0)
	v_add_f32_e32 v88, v92, v100
	ds_bpermute_b32 v89, v147, v88
	v_mov_b32_e32 v118, v79
	ds_write_b64 v152, v[140:141]
	ds_write_b64 v153, v[160:161]
	s_waitcnt lgkmcnt(2)
; #define LAS __attribute__((address_space(3)))
; __device__ __forceinline__ unsigned cvt_pk_bf16(float lo, float hi) { unsigned r; asm volatile("v_cvt_pk_bf16_f32 %0, %1, %2" : "=v"(r) : "v"(lo), "v"(hi)); return r; }
; __device__ __forceinline__ unsigned pk4_fp8(float a, float b, float c, float d) { int w = 0; w = __builtin_amdgcn_cvt_pk_fp8_f32(a, b, w, false); w = __builtin_amdgcn_cvt_pk_fp8_f32(c, d, w, true); return (unsigned)w; }
; __device__ __forceinline__ float bf_lo(unsigned w) { return __uint_as_float(w << 16); }
; __device__ __forceinline__ float bf_hi(unsigned w) { return __uint_as_float(w & 0xffff0000u); }
; __device__ __forceinline__ void p6_router(Frame& F) {
;     ...
;                 for (int j = 0; j < 8; ++j) { v[j] = v[j] * rstd * pw[j] + pb[j]; { u32x2 xb; xb.x = cvt_pk_bf16(v[j][0], v[j][1]); xb.y = cvt_pk_bf16(v[j][2], v[j][3]); ((u32x2*)(X1 + (size_t)t * DM))[lane + 64 * j] = xb; } s += (v[j][0] + v[j][1]) + (v[j][2] + v[j][3]); }
;                 mean = wave_sum(s) * (1.f / DM); s2 = 0.f;
; #pragma unroll
;                 for (int j = 0; j < 8; ++j) { v[j] = v[j] - mean; s2 += (v[j][0] * v[j][0] + v[j][1] * v[j][1]) + (v[j][2] * v[j][2] + v[j][3] * v[j][3]); }
;                 rstd = 1.f / sqrtf(wave_sum(s2) * (1.f / DM) + LN_EPS);
;                 int loq = lane; asm volatile("" : "+v"(loq));
; #pragma unroll
;                 for (int j = 0; j < 8; ++j) { const f32x4 sh = ((const f32x4*)(mod + (size_t)b * 12288 + 6144))[loq + 64 * j], sc = ((const f32x4*)(mod + (size_t)b * 12288 + 8192))[loq + 64 * j];
;                     const f32x4 y = v[j] * rstd * (sc + 1.0f) + sh;
;                     u32x2 wh; wh.x = cvt_pk_bf16(y[0], y[1]); wh.y = cvt_pk_bf16(y[2], y[3]);
;                     const f32x4 yl = {y[0] - bf_lo(wh.x), y[1] - bf_hi(wh.x), y[2] - bf_lo(wh.y), y[3] - bf_hi(wh.y)};
;                     u32x2 wl; wl.x = cvt_pk_bf16(yl[0], yl[1]); wl.y = cvt_pk_bf16(yl[2], yl[3]);
;                     { const int r = 2 * wave + q; LAS unsigned char* rowp = F.lds + r * 4096 + ((((lane >> 1) + 32 * j) ^ r) << 4) + (lane & 1) * 8;
;                       *(LAS u32x2*)rowp = wh; *(LAS u32x2*)(rowp + 65536) = wl; }
;                     U2F[(size_t)t * (DM / 4) + lane + 64 * j] = pk4_fp8(y[0], y[1], y[2], y[3]); }
	v_add_f32_e32 v124, v88, v89
	v_fmac_f32_e32 v126, 0xba000000, v124
	v_fmac_f32_e32 v128, 0xba000000, v124
	v_fmac_f32_e32 v96, 0xba000000, v124
	v_fmac_f32_e32 v127, 0xba000000, v124
	v_fmac_f32_e32 v129, 0xba000000, v124
	v_fmac_f32_e32 v101, 0xba000000, v124
	v_fmac_f32_e32 v97, 0xba000000, v124
	v_mul_f32_e32 v90, v126, v126
	v_mul_f32_e32 v92, v128, v128
	v_mul_f32_e32 v100, v96, v96
	v_pk_fma_f32 v[216:217], v[126:127], v[126:127], v[90:91] op_sel_hi:[1,1,0]
	v_pk_fma_f32 v[218:219], v[128:129], v[128:129], v[92:93] op_sel_hi:[1,1,0]
	v_pk_fma_f32 v[224:225], v[96:97], v[96:97], v[100:101] op_sel_hi:[1,1,0]
	v_fmac_f32_e32 v138, 0xba000000, v124
	v_fmac_f32_e32 v136, 0xba000000, v124
	v_fmac_f32_e32 v139, 0xba000000, v124
	v_fmac_f32_e32 v137, 0xba000000, v124
	v_fmac_f32_e32 v210, 0xba000000, v124
	v_fmac_f32_e32 v211, 0xba000000, v124
	v_fmac_f32_e32 v131, 0xba000000, v124
	v_fmac_f32_e32 v132, 0xba000000, v124
	v_fmac_f32_e32 v134, 0xba000000, v124
	v_fmac_f32_e32 v133, 0xba000000, v124
	v_fmac_f32_e32 v135, 0xba000000, v124
	v_fmac_f32_e32 v130, 0xba000000, v124
	v_fmac_f32_e32 v214, 0xba000000, v124
	v_fmac_f32_e32 v215, 0xba000000, v124
	v_fmac_f32_e32 v103, 0xba000000, v124
	v_pk_mul_f32 v[206:207], v[136:137], v[136:137]
	v_pk_mul_f32 v[208:209], v[138:139], v[138:139]
	v_mov_b32_e32 v212, v131
	v_mov_b32_e32 v213, v211
	v_mov_b32_e32 v131, v210
	v_mov_b32_e32 v88, v103
	v_mov_b32_e32 v89, v215
	v_mov_b32_e32 v103, v214
	v_pk_fma_f32 v[206:207], v[134:135], v[134:135], v[206:207]
	v_pk_fma_f32 v[208:209], v[132:133], v[132:133], v[208:209]
	v_pk_mul_f32 v[210:211], v[212:213], v[212:213]
	v_pk_mul_f32 v[214:215], v[130:131], v[130:131]
	v_pk_add_f32 v[206:207], v[206:207], v[208:209]
	v_pk_mov_b32 v[208:209], v[214:215], v[210:211] op_sel:[1,0]
	v_mov_b32_e32 v215, v211
	v_pk_add_f32 v[208:209], v[208:209], v[214:215]
	v_fmac_f32_e32 v117, 0xba000000, v124
	v_fmac_f32_e32 v119, 0xba000000, v124
	v_fmac_f32_e32 v125, 0xba000000, v124
	v_fmac_f32_e32 v102, 0xba000000, v124
	v_pk_add_f32 v[206:207], v[206:207], v[206:207] op_sel_hi:[0,1]
	v_pk_add_f32 v[208:209], v[208:209], v[208:209] op_sel_hi:[0,1]
	v_pk_mul_f32 v[220:221], v[88:89], v[88:89]
	v_pk_mul_f32 v[222:223], v[102:103], v[102:103]
	v_mul_f32_e32 v216, v101, v101
	v_mul_f32_e32 v218, v125, v125
	v_mul_f32_e32 v206, v117, v117
	v_mul_f32_e32 v208, v119, v119
	v_fmac_f32_e32 v98, 0xba000000, v124
	v_pk_mov_b32 v[210:211], v[222:223], v[220:221] op_sel:[1,0]
	v_mov_b32_e32 v223, v221
	v_pk_add_f32 v[214:215], v[216:217], v[218:219]
	v_pk_add_f32 v[206:207], v[208:209], v[206:207]
	v_fmac_f32_e32 v99, 0xba000000, v124
	v_mul_f32_e32 v116, v98, v98
	v_pk_add_f32 v[210:211], v[210:211], v[222:223]
	v_pk_add_f32 v[206:207], v[214:215], v[206:207]
	v_pk_add_f32 v[210:211], v[210:211], v[210:211] op_sel_hi:[0,1]
	v_pk_add_f32 v[206:207], v[206:207], v[206:207] op_sel_hi:[0,1]
	v_fmac_f32_e32 v91, 0xba000000, v124
	v_fmac_f32_e32 v93, 0xba000000, v124
	v_fmac_f32_e32 v95, 0xba000000, v124
	v_fmac_f32_e32 v94, 0xba000000, v124
	s_waitcnt vmcnt(1)
	v_pk_add_f32 v[112:113], v[112:113], 1.0 op_sel_hi:[1,0]
	v_pk_add_f32 v[114:115], v[114:115], 1.0 op_sel_hi:[1,0]
	s_waitcnt vmcnt(0)
	v_pk_fma_f32 v[110:111], v[110:111], v[112:113], v[202:203]
	v_pk_fma_f32 v[108:109], v[108:109], v[114:115], v[204:205]
	v_cvt_pk_fp8_f32 v118, v110, v111
	v_cvt_pk_bf16_f32 v140, v110, v111
	v_cvt_pk_bf16_f32 v141, v108, v109
	v_mul_f32_e32 v224, v94, v94
	v_cvt_pk_fp8_f32 v118, v108, v109 op_sel:[0,0,1]
	v_lshlrev_b32_e32 v90, 16, v140
	v_and_b32_e32 v92, 0xffff0000, v140
	v_lshlrev_b32_e32 v100, 16, v141
	v_and_b32_e32 v112, 0xffff0000, v141
	v_sub_f32_e32 v90, v110, v90
	v_sub_f32_e32 v92, v111, v92
	v_sub_f32_e32 v100, v108, v100
	v_sub_f32_e32 v108, v109, v112
	v_cvt_pk_bf16_f32 v152, v90, v92
	v_cvt_pk_bf16_f32 v153, v100, v108
	global_store_dword v150, v118, s[8:9] offset:1536 nt
	global_load_dwordx4 v[108:111], v[122:123], off offset:3072
	global_load_dwordx4 v[112:115], v[120:121], off offset:3072
	v_pk_fma_f32 v[120:121], v[98:99], v[98:99], v[116:117] op_sel_hi:[1,1,0]
	v_mul_f32_e32 v210, v93, v93
	v_mul_f32_e32 v120, v95, v95
	v_mul_f32_e32 v206, v91, v91
	v_pk_add_f32 v[120:121], v[224:225], v[120:121]
	v_pk_add_f32 v[122:123], v[210:211], v[206:207]
	v_mov_b32_e32 v100, v79
	v_pk_add_f32 v[120:121], v[120:121], v[122:123]
	v_mov_b32_e32 v122, v133
	v_add_f32_e32 v90, v120, v121
	ds_bpermute_b32 v92, v1, v90
	v_mov_b32_e32 v120, v135
	v_mov_b32_e32 v135, v136
	ds_write_b64 v163, v[140:141]
	ds_write_b64 v164, v[152:153]
	v_mov_b32_e32 v121, v137
	s_waitcnt lgkmcnt(2)
	v_add_f32_e32 v90, v90, v92
	ds_bpermute_b32 v92, v142, v90
	v_mov_b32_e32 v123, v139
	s_waitcnt lgkmcnt(0)
	v_add_f32_e32 v90, v90, v92
	ds_bpermute_b32 v92, v143, v90
	s_waitcnt lgkmcnt(0)
	v_add_f32_e32 v90, v90, v92
	ds_bpermute_b32 v92, v144, v90
	s_waitcnt lgkmcnt(0)
	v_add_f32_e32 v90, v90, v92
	ds_bpermute_b32 v92, v145, v90
	s_waitcnt lgkmcnt(0)
	v_add_f32_e32 v90, v90, v92
	ds_bpermute_b32 v92, v147, v90
	s_waitcnt lgkmcnt(0)
	v_add_f32_e32 v90, v90, v92
	v_fmamk_f32 v90, v90, 0x3a000000, v148
	v_mul_f32_e32 v92, 0x4f800000, v90
	v_cmp_gt_f32_e32 vcc, s45, v90
	s_waitcnt vmcnt(0)
; #define LAS __attribute__((address_space(3)))
; __device__ __forceinline__ unsigned cvt_pk_bf16(float lo, float hi) { unsigned r; asm volatile("v_cvt_pk_bf16_f32 %0, %1, %2" : "=v"(r) : "v"(lo), "v"(hi)); return r; }
; __device__ __forceinline__ unsigned pk4_fp8(float a, float b, float c, float d) { int w = 0; w = __builtin_amdgcn_cvt_pk_fp8_f32(a, b, w, false); w = __builtin_amdgcn_cvt_pk_fp8_f32(c, d, w, true); return (unsigned)w; }
; __device__ __forceinline__ float bf_lo(unsigned w) { return __uint_as_float(w << 16); }
; __device__ __forceinline__ float bf_hi(unsigned w) { return __uint_as_float(w & 0xffff0000u); }
; __device__ __forceinline__ void p6_router(Frame& F) {
;     ...
;                 float rstd = 1.f / sqrtf(wave_sum(s2) * (1.f / DM) + LN_EPS);
;                 s = 0.f;
; #pragma unroll
;                 for (int j = 0; j < 8; ++j) { v[j] = v[j] * rstd * pw[j] + pb[j]; { u32x2 xb; xb.x = cvt_pk_bf16(v[j][0], v[j][1]); xb.y = cvt_pk_bf16(v[j][2], v[j][3]); ((u32x2*)(X1 + (size_t)t * DM))[lane + 64 * j] = xb; } s += (v[j][0] + v[j][1]) + (v[j][2] + v[j][3]); }
;                 mean = wave_sum(s) * (1.f / DM); s2 = 0.f;
; #pragma unroll
;                 for (int j = 0; j < 8; ++j) { v[j] = v[j] - mean; s2 += (v[j][0] * v[j][0] + v[j][1] * v[j][1]) + (v[j][2] * v[j][2] + v[j][3] * v[j][3]); }
;                 rstd = 1.f / sqrtf(wave_sum(s2) * (1.f / DM) + LN_EPS);
;                 int loq = lane; asm volatile("" : "+v"(loq));
; #pragma unroll
;                 for (int j = 0; j < 8; ++j) { const f32x4 sh = ((const f32x4*)(mod + (size_t)b * 12288 + 6144))[loq + 64 * j], sc = ((const f32x4*)(mod + (size_t)b * 12288 + 8192))[loq + 64 * j];
;                     const f32x4 y = v[j] * rstd * (sc + 1.0f) + sh;
;                     u32x2 wh; wh.x = cvt_pk_bf16(y[0], y[1]); wh.y = cvt_pk_bf16(y[2], y[3]);
;                     const f32x4 yl = {y[0] - bf_lo(wh.x), y[1] - bf_hi(wh.x), y[2] - bf_lo(wh.y), y[3] - bf_hi(wh.y)};
;                     u32x2 wl; wl.x = cvt_pk_bf16(yl[0], yl[1]); wl.y = cvt_pk_bf16(yl[2], yl[3]);
;                     { const int r = 2 * wave + q; LAS unsigned char* rowp = F.lds + r * 4096 + ((((lane >> 1) + 32 * j) ^ r) << 4) + (lane & 1) * 8;
;                       *(LAS u32x2*)rowp = wh; *(LAS u32x2*)(rowp + 65536) = wl; }
;                     U2F[(size_t)t * (DM / 4) + lane + 64 * j] = pk4_fp8(y[0], y[1], y[2], y[3]); }
	v_pk_add_f32 v[112:113], v[112:113], 1.0 op_sel_hi:[1,0]
	v_cndmask_b32_e32 v90, v90, v92, vcc
	v_sqrt_f32_e32 v92, v90
	v_pk_fma_f32 v[106:107], v[106:107], v[112:113], v[108:109]
	v_pk_add_f32 v[114:115], v[114:115], 1.0 op_sel_hi:[1,0]
	v_cvt_pk_fp8_f32 v100, v106, v107
	v_add_u32_e32 v116, -1, v92
	v_add_u32_e32 v118, 1, v92
	v_fma_f32 v124, -v116, v92, v90
	v_fma_f32 v133, -v118, v92, v90
	v_cmp_ge_f32_e64 s[0:1], 0, v124
	v_pk_fma_f32 v[104:105], v[104:105], v[114:115], v[110:111]
	v_cvt_pk_bf16_f32 v108, v106, v107
	s_nop 0
	v_cndmask_b32_e64 v92, v92, v116, s[0:1]
	v_cmp_lt_f32_e64 s[0:1], 0, v133
	v_lshlrev_b32_e32 v78, 16, v108
	v_and_b32_e32 v110, 0xffff0000, v108
	v_cndmask_b32_e64 v92, v92, v118, s[0:1]
	v_mul_f32_e32 v116, 0x37800000, v92
	v_cndmask_b32_e32 v92, v92, v116, vcc
	v_cmp_class_f32_e32 vcc, v90, v149
	v_cvt_pk_bf16_f32 v109, v104, v105
	v_sub_f32_e32 v78, v106, v78
	v_lshlrev_b32_e32 v111, 16, v109
	v_cndmask_b32_e32 v90, v92, v90, vcc
	v_div_scale_f32 v92, s[0:1], v90, v90, 1.0
	v_rcp_f32_e32 v116, v92
	v_div_scale_f32 v118, vcc, 1.0, v90, 1.0
	v_sub_f32_e32 v106, v107, v110
	v_fma_f32 v124, -v92, v116, 1.0
	v_fmac_f32_e32 v116, v124, v116
	v_mul_f32_e32 v124, v118, v116
	v_fma_f32 v136, -v92, v124, v118
	v_fmac_f32_e32 v124, v136, v116
	v_fma_f32 v92, -v92, v124, v118
	v_div_fmas_f32 v92, v92, v116, v124
	v_and_b32_e32 v112, 0xffff0000, v109
	v_sub_f32_e32 v107, v104, v111
	v_cvt_pk_bf16_f32 v106, v78, v106
	v_div_fixup_f32 v78, v92, v90, 1.0
	v_mov_b32_e32 v133, v138
	v_sub_f32_e32 v110, v105, v112
	v_cvt_pk_fp8_f32 v100, v104, v105 op_sel:[0,0,1]
	v_cvt_pk_bf16_f32 v107, v107, v110
	v_pk_mul_f32 v[104:105], v[134:135], v[78:79] op_sel_hi:[1,0]
	ds_write_b64 v157, v[108:109]
	ds_write_b64 v158, v[106:107]
	v_pk_mul_f32 v[106:107], v[132:133], v[78:79] op_sel_hi:[1,0]
	v_pk_fma_f32 v[70:71], v[70:71], v[104:105], v[10:11]
	v_pk_mul_f32 v[10:11], v[120:121], v[78:79] op_sel_hi:[1,0]
	v_pk_fma_f32 v[72:73], v[72:73], v[106:107], v[12:13]
	v_pk_mul_f32 v[12:13], v[122:123], v[78:79] op_sel_hi:[1,0]
	v_pk_fma_f32 v[62:63], v[62:63], v[10:11], v[66:67]
	v_pk_fma_f32 v[64:65], v[64:65], v[12:13], v[68:69]
	v_mov_b32_e32 v10, v62
	v_mov_b32_e32 v11, v70
	v_mov_b32_e32 v12, v63
	v_mov_b32_e32 v13, v71
	v_pk_add_f32 v[10:11], v[10:11], v[12:13]
	v_mov_b32_e32 v12, v65
	v_mov_b32_e32 v13, v73
	v_mov_b32_e32 v66, v64
	v_mov_b32_e32 v67, v72
	v_pk_add_f32 v[12:13], v[12:13], v[66:67]
	v_pk_mul_f32 v[66:67], v[212:213], v[78:79] op_sel_hi:[1,0]
	v_pk_add_f32 v[10:11], v[10:11], v[12:13]
	v_pk_mul_f32 v[12:13], v[130:131], v[78:79] op_sel_hi:[1,0]
	v_pk_fma_f32 v[56:57], v[56:57], v[66:67], v[60:61]
	v_pk_fma_f32 v[54:55], v[54:55], v[12:13], v[58:59]
	v_mov_b32_e32 v13, v57
	v_mov_b32_e32 v12, v54
	v_pk_mov_b32 v[58:59], v[54:55], v[56:57] op_sel:[1,0]
	v_pk_mul_f32 v[60:61], v[128:129], v[78:79] op_sel_hi:[1,0]
	v_pk_add_f32 v[12:13], v[12:13], v[58:59]
	v_pk_mul_f32 v[58:59], v[126:127], v[78:79] op_sel_hi:[1,0]
	v_mov_b32_e32 v124, v101
	v_mov_b32_e32 v116, v119
	v_pk_fma_f32 v[48:49], v[48:49], v[60:61], v[52:53]
	v_pk_fma_f32 v[46:47], v[46:47], v[58:59], v[50:51]
	v_pk_mul_f32 v[58:59], v[124:125], v[78:79] op_sel_hi:[1,0]
	v_pk_mul_f32 v[60:61], v[116:117], v[78:79] op_sel_hi:[1,0]
	v_add_f32_e32 v11, 0, v11
	v_pk_add_f32 v[12:13], v[12:13], v[12:13] op_sel_hi:[0,1]
	v_pk_fma_f32 v[40:41], v[40:41], v[60:61], v[44:45]
	v_pk_fma_f32 v[38:39], v[38:39], v[58:59], v[42:43]
	v_add_f32_e32 v11, v10, v11
	v_add_f32_e32 v51, v46, v47
	v_add_f32_e32 v53, v49, v48
	v_mov_b32_e32 v50, v38
	v_mov_b32_e32 v52, v39
	v_mov_b32_e32 v12, v41
	v_mov_b32_e32 v10, v40
	v_pk_add_f32 v[42:43], v[50:51], v[52:53]
	v_pk_add_f32 v[10:11], v[12:13], v[10:11]
	v_pk_mul_f32 v[12:13], v[88:89], v[78:79] op_sel_hi:[1,0]
	v_pk_add_f32 v[10:11], v[42:43], v[10:11]
	v_pk_fma_f32 v[32:33], v[32:33], v[12:13], v[36:37]
	v_pk_add_f32 v[42:43], v[10:11], v[10:11] op_sel_hi:[0,1]
	v_pk_mul_f32 v[10:11], v[102:103], v[78:79] op_sel_hi:[1,0]
	v_mov_b32_e32 v90, v93
	v_pk_fma_f32 v[30:31], v[30:31], v[10:11], v[34:35]
	v_mov_b32_e32 v11, v33
	v_mov_b32_e32 v10, v30
	v_pk_mov_b32 v[12:13], v[30:31], v[32:33] op_sel:[1,0]
	s_lshl_b64 s[0:1], s[4:5], 12
	v_pk_add_f32 v[10:11], v[10:11], v[12:13]
	v_pk_mul_f32 v[12:13], v[98:99], v[78:79] op_sel_hi:[1,0]
	v_pk_add_f32 v[34:35], v[10:11], v[10:11] op_sel_hi:[0,1]
	v_pk_mul_f32 v[10:11], v[96:97], v[78:79] op_sel_hi:[1,0]
	v_pk_fma_f32 v[24:25], v[24:25], v[12:13], v[28:29]
	v_pk_fma_f32 v[22:23], v[22:23], v[10:11], v[26:27]
	v_pk_mul_f32 v[12:13], v[94:95], v[78:79] op_sel_hi:[1,0]
	v_pk_mul_f32 v[10:11], v[90:91], v[78:79] op_sel_hi:[1,0]
	v_pk_fma_f32 v[12:13], v[14:15], v[12:13], v[18:19]
	v_pk_fma_f32 v[10:11], v[16:17], v[10:11], v[20:21]
	v_add_f32_e32 v27, v22, v23
	v_add_f32_e32 v29, v25, v24
	v_mov_b32_e32 v26, v12
	v_mov_b32_e32 v28, v13
	v_mov_b32_e32 v34, v11
	v_mov_b32_e32 v42, v10
	v_pk_add_f32 v[14:15], v[26:27], v[28:29]
	v_pk_add_f32 v[16:17], v[34:35], v[42:43]
	s_add_u32 s0, s42, s0
	v_pk_add_f32 v[14:15], v[14:15], v[16:17]
	s_addc_u32 s1, s43, s1
	v_add_f32_e32 v15, v14, v15
	ds_bpermute_b32 v16, v1, v15
	global_store_dword v150, v100, s[8:9] offset:1792 nt
	v_cvt_pk_bf16_f32 v104, v70, v71
	v_cvt_pk_bf16_f32 v105, v72, v73
	global_store_dwordx2 v146, v[104:105], s[0:1] nt
	s_waitcnt lgkmcnt(0)
	v_add_f32_e32 v16, v15, v16
	ds_bpermute_b32 v17, v142, v16
	v_cvt_pk_bf16_f32 v14, v62, v63
	v_cvt_pk_bf16_f32 v15, v64, v65
	global_store_dwordx2 v146, v[14:15], s[0:1] offset:512 nt
	v_cvt_pk_bf16_f32 v14, v54, v55
	s_waitcnt lgkmcnt(0)
; __device__ __forceinline__ unsigned cvt_pk_bf16(float lo, float hi) { unsigned r; asm volatile("v_cvt_pk_bf16_f32 %0, %1, %2" : "=v"(r) : "v"(lo), "v"(hi)); return r; }
; __device__ __forceinline__ void p6_router(Frame& F) {
;     ...
;                 for (int j = 0; j < 8; ++j) { v[j] = v[j] * rstd * pw[j] + pb[j]; { u32x2 xb; xb.x = cvt_pk_bf16(v[j][0], v[j][1]); xb.y = cvt_pk_bf16(v[j][2], v[j][3]); ((u32x2*)(X1 + (size_t)t * DM))[lane + 64 * j] = xb; } s += (v[j][0] + v[j][1]) + (v[j][2] + v[j][3]); }
;                 mean = wave_sum(s) * (1.f / DM); s2 = 0.f;
; #pragma unroll
;                 for (int j = 0; j < 8; ++j) { v[j] = v[j] - mean; s2 += (v[j][0] * v[j][0] + v[j][1] * v[j][1]) + (v[j][2] * v[j][2] + v[j][3] * v[j][3]); }
;                 rstd = 1.f / sqrtf(wave_sum(s2) * (1.f / DM) + LN_EPS);
;                 int loq = lane; asm volatile("" : "+v"(loq));
; #pragma unroll
;                 for (int j = 0; j < 8; ++j) { const f32x4 sh = ((const f32x4*)(mod + (size_t)b * 12288 + 6144))[loq + 64 * j], sc = ((const f32x4*)(mod + (size_t)b * 12288 + 8192))[loq + 64 * j];
	v_add_f32_e32 v16, v16, v17
	ds_bpermute_b32 v17, v143, v16
	v_cvt_pk_bf16_f32 v15, v56, v57
	global_store_dwordx2 v146, v[14:15], s[0:1] offset:1024 nt
	v_cvt_pk_bf16_f32 v14, v46, v47
	v_cvt_pk_bf16_f32 v15, v48, v49
	s_waitcnt lgkmcnt(0)
	v_add_f32_e32 v16, v16, v17
	ds_bpermute_b32 v17, v144, v16
	global_store_dwordx2 v146, v[14:15], s[0:1] offset:1536 nt
	v_cvt_pk_bf16_f32 v14, v38, v39
	v_cvt_pk_bf16_f32 v15, v40, v41
	global_store_dwordx2 v146, v[14:15], s[0:1] offset:2048 nt
	s_waitcnt lgkmcnt(0)
	v_add_f32_e32 v16, v16, v17
	ds_bpermute_b32 v17, v145, v16
	v_cvt_pk_bf16_f32 v14, v30, v31
	v_cvt_pk_bf16_f32 v15, v32, v33
	global_store_dwordx2 v146, v[14:15], s[0:1] offset:2560 nt
	v_cvt_pk_bf16_f32 v14, v22, v23
	s_waitcnt lgkmcnt(0)
	v_add_f32_e32 v16, v16, v17
	ds_bpermute_b32 v17, v147, v16
	v_cvt_pk_bf16_f32 v15, v24, v25
	global_store_dwordx2 v146, v[14:15], s[0:1] offset:3072 nt
	v_cvt_pk_bf16_f32 v14, v12, v13
	v_cvt_pk_bf16_f32 v15, v10, v11
	s_waitcnt lgkmcnt(0)
	v_add_f32_e32 v26, v16, v17
	v_fmamk_f32 v71, v26, 0xba000000, v71
	v_fmamk_f32 v63, v26, 0xba000000, v63
	v_fmamk_f32 v73, v26, 0xba000000, v73
	v_fmac_f32_e32 v70, 0xba000000, v26
	v_fmamk_f32 v65, v26, 0xba000000, v65
	v_fmac_f32_e32 v62, 0xba000000, v26
	v_mov_b32_e32 v16, v71
	v_mov_b32_e32 v17, v63
	global_store_dwordx2 v146, v[14:15], s[0:1] offset:3584 nt
	v_fmac_f32_e32 v72, 0xba000000, v26
	v_fmac_f32_e32 v64, 0xba000000, v26
	v_mov_b32_e32 v14, v70
	v_mov_b32_e32 v15, v62
	v_pk_mul_f32 v[16:17], v[16:17], v[16:17]
	v_mov_b32_e32 v18, v73
	v_mov_b32_e32 v19, v65
	v_pk_fma_f32 v[14:15], v[14:15], v[14:15], v[16:17]
	v_mov_b32_e32 v16, v72
	v_mov_b32_e32 v17, v64
	v_pk_mul_f32 v[18:19], v[18:19], v[18:19]
	v_fmamk_f32 v55, v26, 0xba000000, v55
	v_pk_fma_f32 v[16:17], v[16:17], v[16:17], v[18:19]
	v_fmac_f32_e32 v54, 0xba000000, v26
	v_pk_add_f32 v[14:15], v[14:15], v[16:17]
	v_fmamk_f32 v57, v26, 0xba000000, v57
	v_fmac_f32_e32 v56, 0xba000000, v26
	v_pk_add_f32 v[14:15], v[14:15], v[14:15] op_sel_hi:[0,1]
	v_pk_mul_f32 v[16:17], v[56:57], v[56:57]
	v_pk_mul_f32 v[18:19], v[54:55], v[54:55]
	v_fmac_f32_e32 v46, 0xba000000, v26
	v_pk_mov_b32 v[20:21], v[18:19], v[16:17] op_sel:[1,0]
	v_mov_b32_e32 v19, v17
	v_fmamk_f32 v47, v26, 0xba000000, v47
	v_fmac_f32_e32 v48, 0xba000000, v26
	v_mul_f32_e32 v14, v46, v46
	v_pk_add_f32 v[16:17], v[20:21], v[18:19]
	v_fmamk_f32 v49, v26, 0xba000000, v49
	v_pk_fma_f32 v[18:19], v[46:47], v[46:47], v[14:15] op_sel_hi:[1,1,0]
	v_mul_f32_e32 v14, v48, v48
	v_pk_add_f32 v[16:17], v[16:17], v[16:17] op_sel_hi:[0,1]
	v_pk_fma_f32 v[20:21], v[48:49], v[48:49], v[14:15] op_sel_hi:[1,1,0]
	v_fmamk_f32 v41, v26, 0xba000000, v41
	v_fmac_f32_e32 v40, 0xba000000, v26
	v_fmamk_f32 v39, v26, 0xba000000, v39
	v_fmac_f32_e32 v38, 0xba000000, v26
	v_mul_f32_e32 v18, v38, v38
	v_mul_f32_e32 v20, v39, v39
	v_mul_f32_e32 v16, v40, v40
	v_mul_f32_e32 v14, v41, v41
	v_pk_add_f32 v[18:19], v[18:19], v[20:21]
	v_pk_add_f32 v[14:15], v[16:17], v[14:15]
	v_fmamk_f32 v31, v26, 0xba000000, v31
	v_fmac_f32_e32 v30, 0xba000000, v26
	v_fmamk_f32 v33, v26, 0xba000000, v33
	v_fmac_f32_e32 v32, 0xba000000, v26
	v_pk_add_f32 v[14:15], v[18:19], v[14:15]
	v_pk_mul_f32 v[16:17], v[32:33], v[32:33]
	v_pk_mul_f32 v[18:19], v[30:31], v[30:31]
	v_pk_add_f32 v[14:15], v[14:15], v[14:15] op_sel_hi:[0,1]
	v_pk_mov_b32 v[20:21], v[18:19], v[16:17] op_sel:[1,0]
	v_mov_b32_e32 v19, v17
	v_fmac_f32_e32 v22, 0xba000000, v26
	v_pk_add_f32 v[16:17], v[20:21], v[18:19]
	v_fmamk_f32 v23, v26, 0xba000000, v23
	v_fmac_f32_e32 v24, 0xba000000, v26
	v_mul_f32_e32 v14, v22, v22
	v_pk_add_f32 v[34:35], v[16:17], v[16:17] op_sel_hi:[0,1]
	v_fmamk_f32 v25, v26, 0xba000000, v25
	v_pk_fma_f32 v[16:17], v[22:23], v[22:23], v[14:15] op_sel_hi:[1,1,0]
	v_mul_f32_e32 v14, v24, v24
	v_pk_fma_f32 v[18:19], v[24:25], v[24:25], v[14:15] op_sel_hi:[1,1,0]
	v_fmamk_f32 v13, v26, 0xba000000, v13
	v_fmac_f32_e32 v12, 0xba000000, v26
	v_mul_f32_e32 v16, v12, v12
	v_mul_f32_e32 v18, v13, v13
	v_pk_add_f32 v[36:37], v[16:17], v[18:19]
	v_mov_b32_e32 v16, v170
	v_fmamk_f32 v11, v26, 0xba000000, v11
	v_ashrrev_i32_e32 v17, 31, v16
	v_lshlrev_b64 v[18:19], 4, v[16:17]
	v_lshl_add_u64 v[16:17], s[16:17], 0, v[18:19]
	v_fmac_f32_e32 v10, 0xba000000, v26
	v_lshl_add_u64 v[42:43], s[20:21], 0, v[18:19]
	global_load_dwordx4 v[18:21], v[16:17], off
	global_load_dwordx4 v[26:29], v[42:43], off
	v_mul_f32_e32 v34, v10, v10
	v_mul_f32_e32 v14, v11, v11
	v_pk_add_f32 v[14:15], v[34:35], v[14:15]
	s_waitcnt vmcnt(0)
	v_pk_add_f32 v[28:29], v[28:29], 1.0 op_sel_hi:[1,0]
	v_pk_add_f32 v[14:15], v[36:37], v[14:15]
	v_pk_add_f32 v[26:27], v[26:27], 1.0 op_sel_hi:[1,0]
	v_add_f32_e32 v14, v14, v15
	ds_bpermute_b32 v15, v1, v14
	s_waitcnt lgkmcnt(0)
	v_add_f32_e32 v14, v14, v15
	ds_bpermute_b32 v15, v142, v14
	s_waitcnt lgkmcnt(0)
	v_add_f32_e32 v14, v14, v15
	ds_bpermute_b32 v15, v143, v14
	s_waitcnt lgkmcnt(0)
	v_add_f32_e32 v14, v14, v15
	ds_bpermute_b32 v15, v144, v14
	s_waitcnt lgkmcnt(0)
	v_add_f32_e32 v14, v14, v15
	ds_bpermute_b32 v15, v145, v14
	s_waitcnt lgkmcnt(0)
	v_add_f32_e32 v14, v14, v15
	ds_bpermute_b32 v15, v147, v14
	s_waitcnt lgkmcnt(0)
; #define LAS __attribute__((address_space(3)))
; __device__ __forceinline__ unsigned cvt_pk_bf16(float lo, float hi) { unsigned r; asm volatile("v_cvt_pk_bf16_f32 %0, %1, %2" : "=v"(r) : "v"(lo), "v"(hi)); return r; }
; __device__ __forceinline__ unsigned pk4_fp8(float a, float b, float c, float d) { int w = 0; w = __builtin_amdgcn_cvt_pk_fp8_f32(a, b, w, false); w = __builtin_amdgcn_cvt_pk_fp8_f32(c, d, w, true); return (unsigned)w; }
; __device__ __forceinline__ float bf_lo(unsigned w) { return __uint_as_float(w << 16); }
; __device__ __forceinline__ float bf_hi(unsigned w) { return __uint_as_float(w & 0xffff0000u); }
; __device__ __forceinline__ void p6_router(Frame& F) {
;     ...
;                 rstd = 1.f / sqrtf(wave_sum(s2) * (1.f / DM) + LN_EPS);
;                 int loq = lane; asm volatile("" : "+v"(loq));
; #pragma unroll
;                 for (int j = 0; j < 8; ++j) { const f32x4 sh = ((const f32x4*)(mod + (size_t)b * 12288 + 6144))[loq + 64 * j], sc = ((const f32x4*)(mod + (size_t)b * 12288 + 8192))[loq + 64 * j];
;                     const f32x4 y = v[j] * rstd * (sc + 1.0f) + sh;
;                     u32x2 wh; wh.x = cvt_pk_bf16(y[0], y[1]); wh.y = cvt_pk_bf16(y[2], y[3]);
;                     const f32x4 yl = {y[0] - bf_lo(wh.x), y[1] - bf_hi(wh.x), y[2] - bf_lo(wh.y), y[3] - bf_hi(wh.y)};
;                     u32x2 wl; wl.x = cvt_pk_bf16(yl[0], yl[1]); wl.y = cvt_pk_bf16(yl[2], yl[3]);
;                     { const int r = 2 * wave + q; LAS unsigned char* rowp = F.lds + r * 4096 + ((((lane >> 1) + 32 * j) ^ r) << 4) + (lane & 1) * 8;
;                       *(LAS u32x2*)rowp = wh; *(LAS u32x2*)(rowp + 65536) = wl; }
;                     U2F[(size_t)t * (DM / 4) + lane + 64 * j] = pk4_fp8(y[0], y[1], y[2], y[3]); }
	v_add_f32_e32 v14, v14, v15
	v_fmac_f32_e32 v148, 0x3a000000, v14
	v_mul_f32_e32 v14, 0x4f800000, v148
	v_cmp_gt_f32_e32 vcc, s45, v148
	s_nop 1
	v_cndmask_b32_e32 v14, v148, v14, vcc
	v_sqrt_f32_e32 v15, v14
	s_nop 0
	v_add_u32_e32 v34, -1, v15
	v_fma_f32 v35, -v34, v15, v14
	v_cmp_ge_f32_e64 s[0:1], 0, v35
	v_add_u32_e32 v35, 1, v15
	s_nop 0
	v_cndmask_b32_e64 v34, v15, v34, s[0:1]
	v_fma_f32 v15, -v35, v15, v14
	v_cmp_lt_f32_e64 s[0:1], 0, v15
	s_nop 1
	v_cndmask_b32_e64 v15, v34, v35, s[0:1]
	v_mul_f32_e32 v34, 0x37800000, v15
	v_cndmask_b32_e32 v15, v15, v34, vcc
	v_cmp_class_f32_e32 vcc, v14, v149
	s_nop 1
	v_cndmask_b32_e32 v14, v15, v14, vcc
	v_div_scale_f32 v15, s[0:1], v14, v14, 1.0
	v_rcp_f32_e32 v34, v15
	s_lshl_b64 s[0:1], s[4:5], 11
	s_add_u32 s0, s40, s0
	s_addc_u32 s1, s44, s1
	v_fma_f32 v35, -v15, v34, 1.0
	v_fmac_f32_e32 v34, v35, v34
	v_div_scale_f32 v35, vcc, 1.0, v14, 1.0
	v_mul_f32_e32 v36, v35, v34
	v_fma_f32 v37, -v15, v36, v35
	v_fmac_f32_e32 v36, v37, v34
	v_fma_f32 v15, -v15, v36, v35
	v_div_fmas_f32 v15, v15, v34, v36
	v_div_fixup_f32 v14, v15, v14, 1.0
	v_pk_mul_f32 v[34:35], v[70:71], v[14:15] op_sel_hi:[1,0]
	v_pk_mul_f32 v[36:37], v[72:73], v[14:15] op_sel_hi:[1,0]
	v_pk_fma_f32 v[18:19], v[26:27], v[34:35], v[18:19]
	v_pk_fma_f32 v[20:21], v[28:29], v[36:37], v[20:21]
	v_mov_b32_e32 v28, v79
	v_cvt_pk_fp8_f32 v28, v18, v19
	v_cvt_pk_bf16_f32 v34, v18, v19
	v_cvt_pk_bf16_f32 v35, v20, v21
	v_cvt_pk_fp8_f32 v28, v20, v21 op_sel:[0,0,1]
	v_lshlrev_b32_e32 v15, 16, v34
	v_sub_f32_e32 v15, v18, v15
	v_and_b32_e32 v26, 0xffff0000, v34
	v_lshlrev_b32_e32 v27, 16, v35
	v_and_b32_e32 v18, 0xffff0000, v35
	v_sub_f32_e32 v26, v19, v26
	v_sub_f32_e32 v27, v20, v27
	v_sub_f32_e32 v18, v21, v18
	v_cvt_pk_bf16_f32 v36, v15, v26
	v_cvt_pk_bf16_f32 v37, v27, v18
	global_store_dword v150, v28, s[0:1] nt
	global_load_dwordx4 v[18:21], v[42:43], off offset:1024
	s_nop 0
	global_load_dwordx4 v[26:29], v[16:17], off offset:1024
	ds_write_b64 v172, v[34:35]
	ds_write_b64 v173, v[36:37]
	v_pk_mul_f32 v[34:35], v[62:63], v[14:15] op_sel_hi:[1,0]
	v_pk_mul_f32 v[36:37], v[64:65], v[14:15] op_sel_hi:[1,0]
	s_waitcnt vmcnt(1)
	v_pk_add_f32 v[18:19], v[18:19], 1.0 op_sel_hi:[1,0]
	s_waitcnt vmcnt(0)
	v_pk_fma_f32 v[18:19], v[18:19], v[34:35], v[26:27]
	v_mov_b32_e32 v27, v79
	v_cvt_pk_fp8_f32 v27, v18, v19
	v_pk_add_f32 v[20:21], v[20:21], 1.0 op_sel_hi:[1,0]
	v_cvt_pk_bf16_f32 v34, v18, v19
	s_nop 0
	v_pk_fma_f32 v[20:21], v[20:21], v[36:37], v[28:29]
	v_lshlrev_b32_e32 v15, 16, v34
	v_cvt_pk_fp8_f32 v27, v20, v21 op_sel:[0,0,1]
	v_and_b32_e32 v26, 0xffff0000, v34
	v_cvt_pk_bf16_f32 v35, v20, v21
	v_sub_f32_e32 v15, v18, v15
	v_sub_f32_e32 v26, v19, v26
	v_lshlrev_b32_e32 v18, 16, v35
	v_and_b32_e32 v19, 0xffff0000, v35
	v_sub_f32_e32 v18, v20, v18
	v_sub_f32_e32 v19, v21, v19
	v_cvt_pk_bf16_f32 v36, v15, v26
	v_cvt_pk_bf16_f32 v37, v18, v19
	global_store_dword v150, v27, s[0:1] offset:256 nt
	global_load_dwordx4 v[18:21], v[42:43], off offset:2048
	s_nop 0
	global_load_dwordx4 v[26:29], v[16:17], off offset:2048
	ds_write_b64 v174, v[34:35]
	ds_write_b64 v175, v[36:37]
	v_pk_mul_f32 v[34:35], v[54:55], v[14:15] op_sel_hi:[1,0]
	v_pk_mul_f32 v[36:37], v[56:57], v[14:15] op_sel_hi:[1,0]
	s_waitcnt vmcnt(1)
	v_pk_add_f32 v[18:19], v[18:19], 1.0 op_sel_hi:[1,0]
	s_waitcnt vmcnt(0)
	v_pk_fma_f32 v[18:19], v[18:19], v[34:35], v[26:27]
	v_mov_b32_e32 v27, v79
	v_cvt_pk_fp8_f32 v27, v18, v19
	v_pk_add_f32 v[20:21], v[20:21], 1.0 op_sel_hi:[1,0]
	v_cvt_pk_bf16_f32 v34, v18, v19
	s_nop 0
	v_pk_fma_f32 v[20:21], v[20:21], v[36:37], v[28:29]
	v_lshlrev_b32_e32 v15, 16, v34
	v_cvt_pk_fp8_f32 v27, v20, v21 op_sel:[0,0,1]
	v_and_b32_e32 v26, 0xffff0000, v34
	v_cvt_pk_bf16_f32 v35, v20, v21
	v_sub_f32_e32 v15, v18, v15
	v_sub_f32_e32 v26, v19, v26
	v_lshlrev_b32_e32 v18, 16, v35
	v_and_b32_e32 v19, 0xffff0000, v35
	v_sub_f32_e32 v18, v20, v18
	v_sub_f32_e32 v19, v21, v19
	v_cvt_pk_bf16_f32 v36, v15, v26
	v_cvt_pk_bf16_f32 v37, v18, v19
	global_store_dword v150, v27, s[0:1] offset:512 nt
	global_load_dwordx4 v[18:21], v[42:43], off offset:3072
	s_nop 0
	global_load_dwordx4 v[26:29], v[16:17], off offset:3072
	v_mov_b32_e32 v15, v79
	v_pk_mul_f32 v[44:45], v[46:47], v[14:15] op_sel_hi:[1,0]
	v_pk_mul_f32 v[46:47], v[48:49], v[14:15] op_sel_hi:[1,0]
	v_add_co_u32_e32 v42, vcc, s41, v42
	ds_write_b64 v167, v[34:35]
	ds_write_b64 v168, v[36:37]
	v_addc_co_u32_e32 v43, vcc, 0, v43, vcc
	s_waitcnt vmcnt(1)
	v_pk_add_f32 v[18:19], v[18:19], 1.0 op_sel_hi:[1,0]
	s_waitcnt vmcnt(0)
	v_pk_fma_f32 v[18:19], v[44:45], v[18:19], v[26:27]
	v_pk_add_f32 v[20:21], v[20:21], 1.0 op_sel_hi:[1,0]
	v_cvt_pk_fp8_f32 v15, v18, v19
	v_pk_fma_f32 v[20:21], v[46:47], v[20:21], v[28:29]
	v_cvt_pk_bf16_f32 v34, v18, v19
	v_add_co_u32_e32 v44, vcc, s41, v16
	v_cvt_pk_fp8_f32 v15, v20, v21 op_sel:[0,0,1]
	v_cvt_pk_bf16_f32 v35, v20, v21
	v_lshlrev_b32_e32 v26, 16, v34
	v_and_b32_e32 v27, 0xffff0000, v34
	v_lshlrev_b32_e32 v28, 16, v35
	v_and_b32_e32 v29, 0xffff0000, v35
	v_sub_f32_e32 v18, v18, v26
	v_sub_f32_e32 v19, v19, v27
	v_sub_f32_e32 v26, v20, v28
	v_sub_f32_e32 v20, v21, v29
	v_cvt_pk_bf16_f32 v36, v18, v19
	v_cvt_pk_bf16_f32 v37, v26, v20
	global_store_dword v150, v15, s[0:1] offset:768 nt
	global_load_dwordx4 v[18:21], v[42:43], off
	v_addc_co_u32_e32 v45, vcc, 0, v17, vcc
	global_load_dwordx4 v[26:29], v[44:45], off
	v_mov_b32_e32 v15, v79
	v_pk_mul_f32 v[16:17], v[38:39], v[14:15] op_sel_hi:[1,0]
	v_pk_mul_f32 v[38:39], v[40:41], v[14:15] op_sel_hi:[1,0]
	ds_write_b64 v176, v[34:35]
	ds_write_b64 v177, v[36:37]
	s_waitcnt vmcnt(1)
; #define LAS __attribute__((address_space(3)))
; __device__ __forceinline__ unsigned cvt_pk_bf16(float lo, float hi) { unsigned r; asm volatile("v_cvt_pk_bf16_f32 %0, %1, %2" : "=v"(r) : "v"(lo), "v"(hi)); return r; }
; __device__ __forceinline__ unsigned pk4_fp8(float a, float b, float c, float d) { int w = 0; w = __builtin_amdgcn_cvt_pk_fp8_f32(a, b, w, false); w = __builtin_amdgcn_cvt_pk_fp8_f32(c, d, w, true); return (unsigned)w; }
; __device__ __forceinline__ float bf_lo(unsigned w) { return __uint_as_float(w << 16); }
; __device__ __forceinline__ void p6_router(Frame& F) {
;     ...
; #pragma unroll
;                 for (int j = 0; j < 8; ++j) { const f32x4 sh = ((const f32x4*)(mod + (size_t)b * 12288 + 6144))[loq + 64 * j], sc = ((const f32x4*)(mod + (size_t)b * 12288 + 8192))[loq + 64 * j];
;                     const f32x4 y = v[j] * rstd * (sc + 1.0f) + sh;
;                     u32x2 wh; wh.x = cvt_pk_bf16(y[0], y[1]); wh.y = cvt_pk_bf16(y[2], y[3]);
;                     const f32x4 yl = {y[0] - bf_lo(wh.x), y[1] - bf_hi(wh.x), y[2] - bf_lo(wh.y), y[3] - bf_hi(wh.y)};
;                     u32x2 wl; wl.x = cvt_pk_bf16(yl[0], yl[1]); wl.y = cvt_pk_bf16(yl[2], yl[3]);
;                     { const int r = 2 * wave + q; LAS unsigned char* rowp = F.lds + r * 4096 + ((((lane >> 1) + 32 * j) ^ r) << 4) + (lane & 1) * 8;
;                       *(LAS u32x2*)rowp = wh; *(LAS u32x2*)(rowp + 65536) = wl; }
;                     U2F[(size_t)t * (DM / 4) + lane + 64 * j] = pk4_fp8(y[0], y[1], y[2], y[3]); }
;             }
;             __builtin_amdgcn_sched_barrier(0);
;             bf16x8 bh[2][2], bl[2][2]; f32x4 cur[2] = {(f32x4){0.f, 0.f, 0.f, 0.f}, (f32x4){0.f, 0.f, 0.f, 0.f}};
;             const bf16_t* wbh = WRH + (size_t)fr * DM + wave * 256 + fq * 8; const bf16_t* wbl = WRL + (size_t)fr * DM + wave * 256 + fq * 8;
; #pragma unroll
;             for (int n = 0; n < 2; ++n) { bh[0][n] = *(const bf16x8*)(wbh + (size_t)(16 * n) * DM); bl[0][n] = *(const bf16x8*)(wbl + (size_t)(16 * n) * DM); }
;             if (rp == 0) {
; #pragma unroll
;                 for (int q = 0; q < 2; ++q)
; #pragma unroll
;                     for (int j = 0; j < 8; ++j) zr[q][j] = ((const u32x2*)(ZB + (size_t)(ta + 2 + q) * DM))[lane + 64 * j];
;             }
;             __syncthreads();
	v_pk_add_f32 v[18:19], v[18:19], 1.0 op_sel_hi:[1,0]
	v_pk_add_f32 v[20:21], v[20:21], 1.0 op_sel_hi:[1,0]
	s_waitcnt vmcnt(0)
	v_pk_fma_f32 v[16:17], v[16:17], v[18:19], v[26:27]
	s_nop 0
	v_cvt_pk_fp8_f32 v15, v16, v17
	v_pk_fma_f32 v[20:21], v[38:39], v[20:21], v[28:29]
	v_cvt_pk_bf16_f32 v34, v16, v17
	s_nop 0
	v_cvt_pk_fp8_f32 v15, v20, v21 op_sel:[0,0,1]
	v_cvt_pk_bf16_f32 v35, v20, v21
	v_lshlrev_b32_e32 v18, 16, v34
	v_and_b32_e32 v19, 0xffff0000, v34
	v_lshlrev_b32_e32 v26, 16, v35
	v_and_b32_e32 v27, 0xffff0000, v35
	v_sub_f32_e32 v16, v16, v18
	v_sub_f32_e32 v17, v17, v19
	v_sub_f32_e32 v18, v20, v26
	v_sub_f32_e32 v19, v21, v27
	v_cvt_pk_bf16_f32 v20, v16, v17
	v_cvt_pk_bf16_f32 v21, v18, v19
	global_store_dword v150, v15, s[0:1] offset:1024 nt
	global_load_dwordx4 v[16:19], v[42:43], off offset:1024
	global_load_dwordx4 v[26:29], v[44:45], off offset:1024
	v_mov_b32_e32 v15, v79
	v_pk_mul_f32 v[30:31], v[30:31], v[14:15] op_sel_hi:[1,0]
	v_pk_mul_f32 v[32:33], v[32:33], v[14:15] op_sel_hi:[1,0]
	ds_write_b64 v178, v[34:35]
	ds_write_b64 v179, v[20:21]
	s_waitcnt vmcnt(1)
	v_pk_add_f32 v[16:17], v[16:17], 1.0 op_sel_hi:[1,0]
	s_waitcnt vmcnt(0)
	v_pk_fma_f32 v[16:17], v[30:31], v[16:17], v[26:27]
	v_pk_add_f32 v[18:19], v[18:19], 1.0 op_sel_hi:[1,0]
	v_cvt_pk_fp8_f32 v15, v16, v17
	v_pk_fma_f32 v[18:19], v[32:33], v[18:19], v[28:29]
	v_cvt_pk_bf16_f32 v20, v16, v17
	s_nop 0
	v_cvt_pk_fp8_f32 v15, v18, v19 op_sel:[0,0,1]
	v_cvt_pk_bf16_f32 v21, v18, v19
	v_lshlrev_b32_e32 v26, 16, v20
	v_and_b32_e32 v27, 0xffff0000, v20
	v_lshlrev_b32_e32 v28, 16, v21
	v_and_b32_e32 v29, 0xffff0000, v21
	v_sub_f32_e32 v16, v16, v26
	v_sub_f32_e32 v17, v17, v27
	v_sub_f32_e32 v26, v18, v28
	v_sub_f32_e32 v18, v19, v29
	v_cvt_pk_bf16_f32 v30, v16, v17
	v_cvt_pk_bf16_f32 v31, v26, v18
	global_store_dword v150, v15, s[0:1] offset:1280 nt
	global_load_dwordx4 v[16:19], v[42:43], off offset:2048
	global_load_dwordx4 v[26:29], v[44:45], off offset:2048
	v_mov_b32_e32 v15, v79
	v_pk_mul_f32 v[22:23], v[22:23], v[14:15] op_sel_hi:[1,0]
	v_pk_mul_f32 v[24:25], v[24:25], v[14:15] op_sel_hi:[1,0]
	ds_write_b64 v180, v[20:21]
	ds_write_b64 v181, v[30:31]
	s_waitcnt vmcnt(1)
	v_pk_add_f32 v[16:17], v[16:17], 1.0 op_sel_hi:[1,0]
	s_waitcnt vmcnt(0)
	v_pk_fma_f32 v[16:17], v[22:23], v[16:17], v[26:27]
	v_pk_add_f32 v[18:19], v[18:19], 1.0 op_sel_hi:[1,0]
	v_cvt_pk_fp8_f32 v15, v16, v17
	v_pk_fma_f32 v[18:19], v[24:25], v[18:19], v[28:29]
	v_cvt_pk_bf16_f32 v24, v16, v17
	s_nop 0
	v_cvt_pk_fp8_f32 v15, v18, v19 op_sel:[0,0,1]
	v_cvt_pk_bf16_f32 v25, v18, v19
	v_lshlrev_b32_e32 v20, 16, v24
	v_and_b32_e32 v21, 0xffff0000, v24
	v_lshlrev_b32_e32 v22, 16, v25
	v_and_b32_e32 v23, 0xffff0000, v25
	v_sub_f32_e32 v16, v16, v20
	v_sub_f32_e32 v17, v17, v21
	v_sub_f32_e32 v20, v18, v22
	v_sub_f32_e32 v18, v19, v23
	v_cvt_pk_bf16_f32 v26, v16, v17
	v_cvt_pk_bf16_f32 v27, v20, v18
	global_store_dword v150, v15, s[0:1] offset:1536 nt
	global_load_dwordx4 v[16:19], v[42:43], off offset:3072
	global_load_dwordx4 v[20:23], v[44:45], off offset:3072
	v_pk_mul_f32 v[12:13], v[12:13], v[14:15] op_sel_hi:[1,0]
	v_pk_mul_f32 v[10:11], v[10:11], v[14:15] op_sel_hi:[1,0]
	ds_write_b64 v184, v[24:25]
	ds_write_b64 v185, v[26:27]
	s_waitcnt vmcnt(1)
	v_pk_add_f32 v[16:17], v[16:17], 1.0 op_sel_hi:[1,0]
	s_waitcnt vmcnt(0)
	v_pk_fma_f32 v[12:13], v[12:13], v[16:17], v[20:21]
	v_pk_add_f32 v[14:15], v[18:19], 1.0 op_sel_hi:[1,0]
	v_cvt_pk_fp8_f32 v79, v12, v13
	v_pk_fma_f32 v[10:11], v[10:11], v[14:15], v[22:23]
	v_cvt_pk_bf16_f32 v14, v12, v13
	s_nop 0
	v_cvt_pk_fp8_f32 v79, v10, v11 op_sel:[0,0,1]
	v_lshlrev_b32_e32 v16, 16, v14
	v_and_b32_e32 v17, 0xffff0000, v14
	v_cvt_pk_bf16_f32 v15, v10, v11
	v_sub_f32_e32 v12, v12, v16
	v_lshlrev_b32_e32 v18, 16, v15
	v_and_b32_e32 v19, 0xffff0000, v15
	v_sub_f32_e32 v13, v13, v17
	v_sub_f32_e32 v16, v10, v18
	v_sub_f32_e32 v17, v11, v19
	v_cvt_pk_bf16_f32 v12, v12, v13
	v_cvt_pk_bf16_f32 v13, v16, v17
	ds_write_b64 v182, v[14:15]
	ds_write_b64 v183, v[12:13]
	global_store_dword v150, v79, s[0:1] offset:1792 nt
	global_load_dwordx4 v[10:13], v[84:85], off
	global_load_dwordx4 v[14:17], v[74:75], off
	global_load_dwordx4 v[18:21], v[86:87], off
	global_load_dwordx4 v[22:25], v[76:77], off
	s_waitcnt lgkmcnt(0)
	s_barrier
; #define LAS __attribute__((address_space(3)))
; __device__ __forceinline__ void p6_router(Frame& F) {
;     ...
; #pragma unroll
;             for (int ks = 0; ks < 8; ++ks) {
;                 if (ks < 7) {
; #pragma unroll
;                     for (int n = 0; n < 2; ++n) { bh[(ks + 1) & 1][n] = *(const bf16x8*)(wbh + (size_t)(16 * n) * DM + (ks + 1) * 32); bl[(ks + 1) & 1][n] = *(const bf16x8*)(wbl + (size_t)(16 * n) * DM + (ks + 1) * 32); }
;                 }
;                 const LAS unsigned char* ap = F.lds + fr * 4096 + (((wave * 32 + ks * 4 + fq) ^ fr) << 4);
;                 const bf16x8 ah = *(const LAS bf16x8*)ap, al = *(const LAS bf16x8*)(ap + 65536);
; #pragma unroll
;                 for (int n = 0; n < 2; ++n) {
;                     cur[n] = __builtin_amdgcn_mfma_f32_16x16x32_bf16(ah, bh[ks & 1][n], cur[n], 0, 0, 0);
;                     cur[n] = __builtin_amdgcn_mfma_f32_16x16x32_bf16(ah, bl[ks & 1][n], cur[n], 0, 0, 0);
;                     cur[n] = __builtin_amdgcn_mfma_f32_16x16x32_bf16(al, bh[ks & 1][n], cur[n], 0, 0, 0);
;                 }
;                 __builtin_amdgcn_sched_barrier(0);
;             }
;             accp[0] = cur[0]; accp[1] = cur[1];
;             __syncthreads();
;         };
;         pass(0, acc[0]); pass(1, acc[1]);
;     }
;     LAS float* red = (LAS float*)F.lds;
;     LAS float* lg = red + 8 * 1024;
;     LAS int* aE = (LAS int*)(lg + 1024); LAS int* aP = aE + 128; LAS float* aW = (LAS float*)(aP + 128);
; #pragma unroll
;     for (int a = 0; a < 2; ++a)
; #pragma unroll
;         for (int n = 0; n < 2; ++n)
; #pragma unroll
;             for (int i = 0; i < 4; ++i) { const int m = 4 * fq + i; red[wave * 1024 + (4 * (m >> 1) + 2 * a + (m & 1)) * 32 + 16 * n + fr] = acc[a][n][i]; }
;     __syncthreads();
;     for (int i = tid; i < 1024; i += 512) { float s = F.in[I_BR][i & 31];
	ds_read_b128 v[26:29], v186
	ds_read_b128 v[30:33], v187
	s_waitcnt vmcnt(3) lgkmcnt(1)
	v_mfma_f32_16x16x32_bf16 v[34:37], v[26:29], v[10:13], 0
	s_waitcnt vmcnt(2)
	v_mfma_f32_16x16x32_bf16 v[38:41], v[26:29], v[14:17], 0
	s_waitcnt vmcnt(1)
	v_mfma_f32_16x16x32_bf16 v[18:21], v[26:29], v[18:21], v[34:37]
	s_waitcnt vmcnt(0)
	v_mfma_f32_16x16x32_bf16 v[22:25], v[26:29], v[22:25], v[38:41]
	global_load_dwordx4 v[26:29], v[80:81], off offset:64
	s_nop 0
	global_load_dwordx4 v[34:37], v[82:83], off offset:64
	s_waitcnt lgkmcnt(0)
	v_mfma_f32_16x16x32_bf16 v[10:13], v[30:33], v[10:13], v[18:21]
	s_nop 2
	global_load_dwordx4 v[18:21], v[74:75], off offset:64
	global_load_dwordx4 v[38:41], v[76:77], off offset:64
	v_mfma_f32_16x16x32_bf16 v[14:17], v[30:33], v[14:17], v[22:25]
	s_nop 2
	ds_read_b128 v[22:25], v188
	ds_read_b128 v[30:33], v189
	s_waitcnt vmcnt(3) lgkmcnt(1)
	v_mfma_f32_16x16x32_bf16 v[10:13], v[22:25], v[26:29], v[10:13]
	s_waitcnt vmcnt(1)
	v_mfma_f32_16x16x32_bf16 v[14:17], v[22:25], v[18:21], v[14:17]
	v_mfma_f32_16x16x32_bf16 v[10:13], v[22:25], v[34:37], v[10:13]
	s_waitcnt lgkmcnt(0)
	v_mfma_f32_16x16x32_bf16 v[10:13], v[30:33], v[26:29], v[10:13]
	global_load_dwordx4 v[26:29], v[80:81], off offset:128
	global_load_dwordx4 v[34:37], v[82:83], off offset:128
	s_waitcnt vmcnt(2)
	v_mfma_f32_16x16x32_bf16 v[14:17], v[22:25], v[38:41], v[14:17]
	global_load_dwordx4 v[22:25], v[74:75], off offset:128
	global_load_dwordx4 v[38:41], v[76:77], off offset:128
	v_mfma_f32_16x16x32_bf16 v[14:17], v[30:33], v[18:21], v[14:17]
	ds_read_b128 v[18:21], v190
	ds_read_b128 v[30:33], v191
	s_waitcnt vmcnt(3) lgkmcnt(1)
	v_mfma_f32_16x16x32_bf16 v[10:13], v[18:21], v[26:29], v[10:13]
	s_waitcnt vmcnt(1)
	v_mfma_f32_16x16x32_bf16 v[14:17], v[18:21], v[22:25], v[14:17]
	v_mfma_f32_16x16x32_bf16 v[10:13], v[18:21], v[34:37], v[10:13]
	s_waitcnt lgkmcnt(0)
	v_mfma_f32_16x16x32_bf16 v[10:13], v[30:33], v[26:29], v[10:13]
	global_load_dwordx4 v[26:29], v[80:81], off offset:192
	global_load_dwordx4 v[34:37], v[82:83], off offset:192
	s_waitcnt vmcnt(2)
	v_mfma_f32_16x16x32_bf16 v[14:17], v[18:21], v[38:41], v[14:17]
	global_load_dwordx4 v[18:21], v[74:75], off offset:192
	global_load_dwordx4 v[38:41], v[76:77], off offset:192
	v_mfma_f32_16x16x32_bf16 v[14:17], v[30:33], v[22:25], v[14:17]
	ds_read_b128 v[22:25], v192
	ds_read_b128 v[30:33], v193
	s_waitcnt vmcnt(3) lgkmcnt(1)
	v_mfma_f32_16x16x32_bf16 v[10:13], v[22:25], v[26:29], v[10:13]
	s_waitcnt vmcnt(1)
	v_mfma_f32_16x16x32_bf16 v[14:17], v[22:25], v[18:21], v[14:17]
	v_mfma_f32_16x16x32_bf16 v[10:13], v[22:25], v[34:37], v[10:13]
	s_waitcnt lgkmcnt(0)
	v_mfma_f32_16x16x32_bf16 v[10:13], v[30:33], v[26:29], v[10:13]
	global_load_dwordx4 v[26:29], v[80:81], off offset:256
	global_load_dwordx4 v[34:37], v[82:83], off offset:256
	s_waitcnt vmcnt(2)
	v_mfma_f32_16x16x32_bf16 v[14:17], v[22:25], v[38:41], v[14:17]
	global_load_dwordx4 v[22:25], v[74:75], off offset:256
	global_load_dwordx4 v[38:41], v[76:77], off offset:256
	v_mfma_f32_16x16x32_bf16 v[14:17], v[30:33], v[18:21], v[14:17]
	ds_read_b128 v[18:21], v194
	ds_read_b128 v[30:33], v195
	s_waitcnt vmcnt(3) lgkmcnt(1)
	v_mfma_f32_16x16x32_bf16 v[10:13], v[18:21], v[26:29], v[10:13]
	s_waitcnt vmcnt(1)
	v_mfma_f32_16x16x32_bf16 v[14:17], v[18:21], v[22:25], v[14:17]
	v_mfma_f32_16x16x32_bf16 v[10:13], v[18:21], v[34:37], v[10:13]
	s_waitcnt lgkmcnt(0)
	v_mfma_f32_16x16x32_bf16 v[10:13], v[30:33], v[26:29], v[10:13]
	global_load_dwordx4 v[26:29], v[80:81], off offset:320
	global_load_dwordx4 v[34:37], v[82:83], off offset:320
	s_waitcnt vmcnt(2)
	v_mfma_f32_16x16x32_bf16 v[14:17], v[18:21], v[38:41], v[14:17]
	global_load_dwordx4 v[18:21], v[74:75], off offset:320
	global_load_dwordx4 v[38:41], v[76:77], off offset:320
	v_mfma_f32_16x16x32_bf16 v[14:17], v[30:33], v[22:25], v[14:17]
	ds_read_b128 v[22:25], v196
	ds_read_b128 v[30:33], v197
	s_waitcnt vmcnt(3) lgkmcnt(1)
	v_mfma_f32_16x16x32_bf16 v[10:13], v[22:25], v[26:29], v[10:13]
	s_waitcnt vmcnt(1)
	v_mfma_f32_16x16x32_bf16 v[14:17], v[22:25], v[18:21], v[14:17]
	v_mfma_f32_16x16x32_bf16 v[10:13], v[22:25], v[34:37], v[10:13]
	s_waitcnt lgkmcnt(0)
	v_mfma_f32_16x16x32_bf16 v[10:13], v[30:33], v[26:29], v[10:13]
	global_load_dwordx4 v[26:29], v[80:81], off offset:384
	global_load_dwordx4 v[34:37], v[82:83], off offset:384
	s_waitcnt vmcnt(2)
	v_mfma_f32_16x16x32_bf16 v[14:17], v[22:25], v[38:41], v[14:17]
	global_load_dwordx4 v[22:25], v[74:75], off offset:384
	global_load_dwordx4 v[38:41], v[76:77], off offset:384
	v_mfma_f32_16x16x32_bf16 v[14:17], v[30:33], v[18:21], v[14:17]
	ds_read_b128 v[18:21], v199
	ds_read_b128 v[30:33], v201
	s_waitcnt vmcnt(3) lgkmcnt(1)
	v_mfma_f32_16x16x32_bf16 v[10:13], v[18:21], v[26:29], v[10:13]
	s_waitcnt vmcnt(1)
	v_mfma_f32_16x16x32_bf16 v[14:17], v[18:21], v[22:25], v[14:17]
	v_mfma_f32_16x16x32_bf16 v[10:13], v[18:21], v[34:37], v[10:13]
	s_waitcnt lgkmcnt(0)
	v_mfma_f32_16x16x32_bf16 v[10:13], v[30:33], v[26:29], v[10:13]
	global_load_dwordx4 v[26:29], v[80:81], off offset:448
	global_load_dwordx4 v[34:37], v[82:83], off offset:448
	s_waitcnt vmcnt(2)
	v_mfma_f32_16x16x32_bf16 v[14:17], v[18:21], v[38:41], v[14:17]
	global_load_dwordx4 v[18:21], v[74:75], off offset:448
	global_load_dwordx4 v[38:41], v[76:77], off offset:448
	v_mfma_f32_16x16x32_bf16 v[14:17], v[30:33], v[22:25], v[14:17]
	ds_read_b128 v[22:25], v198
	ds_read_b128 v[30:33], v200
	s_waitcnt vmcnt(3) lgkmcnt(1)
	v_mfma_f32_16x16x32_bf16 v[10:13], v[22:25], v[26:29], v[10:13]
	s_waitcnt vmcnt(1)
	v_mfma_f32_16x16x32_bf16 v[14:17], v[22:25], v[18:21], v[14:17]
	v_mfma_f32_16x16x32_bf16 v[10:13], v[22:25], v[34:37], v[10:13]
	s_waitcnt vmcnt(0)
	v_mfma_f32_16x16x32_bf16 v[14:17], v[22:25], v[38:41], v[14:17]
	s_waitcnt lgkmcnt(0)
	v_mfma_f32_16x16x32_bf16 v[10:13], v[30:33], v[26:29], v[10:13]
	v_mfma_f32_16x16x32_bf16 v[14:17], v[30:33], v[18:21], v[14:17]
	s_lshl_b32 s0, s46, 12
	v_lshlrev_b32_e32 v18, 10, v154
	s_add_i32 s0, s0, 0
	v_lshlrev_b32_e32 v19, 2, v151
	v_add3_u32 v18, s0, v18, v19
	s_barrier
	ds_write2_b32 v18, v2, v6 offset1:16
	ds_write2_b32 v18, v3, v7 offset0:32 offset1:48
	ds_write2_b32 v18, v4, v8 offset0:128 offset1:144
	ds_write2_b32 v18, v5, v9 offset0:160 offset1:176
	ds_write2_b32 v18, v10, v14 offset0:64 offset1:80
	ds_write2_b32 v18, v11, v15 offset0:96 offset1:112
	ds_write2_b32 v18, v12, v16 offset0:192 offset1:208
	ds_write2_b32 v18, v13, v17 offset0:224 offset1:240
	v_and_b32_e32 v5, 31, v0
	v_lshlrev_b32_e32 v2, 2, v5
	s_waitcnt lgkmcnt(0)
	s_barrier
	global_load_dword v2, v2, s[14:15]
	v_or_b32_e32 v3, 0xfffffe00, v0
	v_lshl_add_u32 v4, v0, 2, 0
	s_mov_b64 s[0:1], 0

; __device__ __forceinline__ void p6_router(Frame& F) {
;     ...
;     if (tid < 128) { myE = aE[tid]; myR = __hip_atomic_fetch_add(lc + myE, 1, __ATOMIC_RELAXED, __HIP_MEMORY_SCOPE_WORKGROUP); }
;     __syncthreads();
;     if (tid < 32) { const int n = lc[tid]; lc[32 + tid] = n > 0 ? (int)__hip_atomic_fetch_add(F.ctl + CW_CNT + 64 * tid, (unsigned)n, RLX_AGENT) : 0; }
;     __syncthreads();
;     if (tid < 128) { const int pos = lc[32 + myE] + myR;
;         ((int*)(F.ws + WS_TOKL))[myE * NTOK + pos] = t0 + (tid >> 2);
;         ((int*)(F.ws + WS_ASG_E))[t0 * 4 + tid] = myE; ((int*)(F.ws + WS_ASG_P))[t0 * 4 + tid] = pos; ((float*)(F.ws + WS_ASG_W))[t0 * 4 + tid] = aW[tid]; }
.LBB0_928:
	s_or_b64 exec, exec, s[4:5]
	s_waitcnt lgkmcnt(0)
	s_barrier
	s_and_saveexec_b64 s[4:5], s[0:1]
	s_cbranch_execz .LBB0_930
	v_lshl_add_u32 v3, v1, 2, 0
	ds_read_b32 v3, v3 offset:38528
	v_lshl_add_u32 v5, v0, 2, 0
	ds_read_b32 v6, v5 offset:37888
	v_lshrrev_b32_e32 v4, 2, v0
	v_or_b32_e32 v4, s3, v4
	s_waitcnt lgkmcnt(1)
	v_add_u32_e32 v7, v3, v2
	v_lshl_add_u32 v2, v1, 13, v7
	v_ashrrev_i32_e32 v3, 31, v2
	v_lshl_add_u64 v[2:3], v[2:3], 2, s[82:83]
	v_add_co_u32_e32 v2, vcc, 0x300000, v2
	s_nop 1
	v_addc_co_u32_e32 v3, vcc, 0, v3, vcc
	global_store_dword v[2:3], v4, off nt
	v_lshl_or_b32 v2, s2, 7, v0
	v_ashrrev_i32_e32 v3, 31, v2
	v_lshl_add_u64 v[2:3], v[2:3], 2, s[82:83]
	v_add_co_u32_e32 v4, vcc, 0x200000, v2
	s_nop 1
	v_addc_co_u32_e32 v5, vcc, 0, v3, vcc
	global_store_dword v[4:5], v1, off nt
	v_add_co_u32_e32 v4, vcc, 0x220000, v2
	s_nop 1
	v_addc_co_u32_e32 v5, vcc, 0, v3, vcc
	v_add_co_u32_e32 v2, vcc, 0x240000, v2
	global_store_dword v[4:5], v7, off nt
	s_nop 0
	v_addc_co_u32_e32 v3, vcc, 0, v3, vcc
	s_waitcnt lgkmcnt(0)
	global_store_dword v[2:3], v6, off nt
